# GEMM K-loops: removed provably dead lgkmcnt waits inside the MFMA clusters (the counter is already 0 from the wait before the barrier), 250 sites
# speedup vs baseline: 1.0036x; 1.0036x over previous
.LBB0_143:
	ds_read_b128 v[148:151], v142
	ds_read_b128 v[152:155], v142 offset:1024
	ds_read_b128 v[156:159], v142 offset:2048
	ds_read_b128 v[160:163], v142 offset:3072
	ds_read_b128 v[164:167], v143
	ds_read_b128 v[174:177], v143 offset:1024
	ds_read_b128 v[178:181], v143 offset:2048
	ds_read_b128 v[182:185], v143 offset:3072
	s_add_u32 s40, s22, 0x100
	s_addc_u32 s41, s23, 0
	s_cmp_eq_u32 s82, 12
	s_cselect_b32 s58, s33, s40
	s_cselect_b32 s59, s13, s41
	s_cselect_b32 s56, s79, s80
	s_cselect_b32 s57, s15, s81
	s_add_u32 s54, s58, 0x80
	s_addc_u32 s55, s59, 0
	ds_read_b128 v[186:189], v144
	ds_read_b128 v[190:193], v144 offset:1024
	ds_read_b128 v[194:197], v144 offset:2048
	ds_read_b128 v[198:201], v144 offset:3072
	ds_read_b128 v[202:205], v144 offset:4096
	ds_read_b128 v[206:209], v144 offset:5120
	ds_read_b128 v[210:213], v144 offset:6144
	ds_read_b128 v[214:217], v144 offset:7168
	s_add_u32 s22, s22, 0x40080
	s_addc_u32 s23, s23, 0
	s_mov_b32 s83, m0
	s_mov_b32 m0, s67
	s_nop 2
	global_load_lds_dwordx4 v136, s[22:23]
	s_mov_b32 m0, s83
	s_nop 0
	s_mov_b32 s83, m0
	s_mov_b32 m0, s76
	s_nop 2
	global_load_lds_dwordx4 v138, s[22:23]
	s_mov_b32 m0, s83
	s_waitcnt vmcnt(8)
	s_waitcnt lgkmcnt(0)
	s_barrier
	s_setprio 1
	v_mfma_f32_16x16x32_bf16 v[126:129], v[148:151], v[186:189], v[126:129]
	v_mfma_f32_16x16x32_bf16 v[122:125], v[156:159], v[186:189], v[122:125]
	v_mfma_f32_16x16x32_bf16 v[110:113], v[148:151], v[194:197], v[110:113]
	v_mfma_f32_16x16x32_bf16 v[106:109], v[156:159], v[194:197], v[106:109]
	v_mfma_f32_16x16x32_bf16 v[94:97], v[148:151], v[202:205], v[94:97]
	v_mfma_f32_16x16x32_bf16 v[90:93], v[156:159], v[202:205], v[90:93]
	v_mfma_f32_16x16x32_bf16 v[78:81], v[148:151], v[210:213], v[78:81]
	v_mfma_f32_16x16x32_bf16 v[74:77], v[156:159], v[210:213], v[74:77]
	v_mfma_f32_16x16x32_bf16 v[126:129], v[152:155], v[190:193], v[126:129]
	v_mfma_f32_16x16x32_bf16 v[122:125], v[160:163], v[190:193], v[122:125]
	v_mfma_f32_16x16x32_bf16 v[110:113], v[152:155], v[198:201], v[110:113]
	v_mfma_f32_16x16x32_bf16 v[106:109], v[160:163], v[198:201], v[106:109]
	v_mfma_f32_16x16x32_bf16 v[94:97], v[152:155], v[206:209], v[94:97]
	v_mfma_f32_16x16x32_bf16 v[90:93], v[160:163], v[206:209], v[90:93]
	v_mfma_f32_16x16x32_bf16 v[78:81], v[152:155], v[214:217], v[78:81]
	v_mfma_f32_16x16x32_bf16 v[74:77], v[160:163], v[214:217], v[74:77]
	s_setprio 0
	s_setprio 1
	v_mfma_f32_16x16x32_bf16 v[118:121], v[164:167], v[186:189], v[118:121]
	v_mfma_f32_16x16x32_bf16 v[114:117], v[178:181], v[186:189], v[114:117]
	v_mfma_f32_16x16x32_bf16 v[102:105], v[164:167], v[194:197], v[102:105]
	v_mfma_f32_16x16x32_bf16 v[98:101], v[178:181], v[194:197], v[98:101]
	v_mfma_f32_16x16x32_bf16 v[86:89], v[164:167], v[202:205], v[86:89]
	v_mfma_f32_16x16x32_bf16 v[82:85], v[178:181], v[202:205], v[82:85]
	v_mfma_f32_16x16x32_bf16 v[70:73], v[164:167], v[210:213], v[70:73]
	v_mfma_f32_16x16x32_bf16 v[66:69], v[178:181], v[210:213], v[66:69]
	v_mfma_f32_16x16x32_bf16 v[118:121], v[174:177], v[190:193], v[118:121]
	v_mfma_f32_16x16x32_bf16 v[114:117], v[182:185], v[190:193], v[114:117]
	v_mfma_f32_16x16x32_bf16 v[102:105], v[174:177], v[198:201], v[102:105]
	v_mfma_f32_16x16x32_bf16 v[98:101], v[182:185], v[198:201], v[98:101]
	v_mfma_f32_16x16x32_bf16 v[86:89], v[174:177], v[206:209], v[86:89]
	v_mfma_f32_16x16x32_bf16 v[82:85], v[182:185], v[206:209], v[82:85]
	v_mfma_f32_16x16x32_bf16 v[70:73], v[174:177], v[214:217], v[70:73]
	v_mfma_f32_16x16x32_bf16 v[66:69], v[182:185], v[214:217], v[66:69]
	s_setprio 0
	s_barrier
	ds_read_b128 v[186:189], v144 offset:16384
	ds_read_b128 v[190:193], v144 offset:17408
	ds_read_b128 v[194:197], v144 offset:18432
	ds_read_b128 v[198:201], v144 offset:19456
	ds_read_b128 v[202:205], v144 offset:20480
	ds_read_b128 v[206:209], v144 offset:21504
	ds_read_b128 v[210:213], v144 offset:22528
	ds_read_b128 v[214:217], v144 offset:23552
	s_mov_b32 s22, m0
	s_mov_b32 m0, s30
	s_nop 2
	global_load_lds_dwordx4 v137, s[56:57]
	s_mov_b32 m0, s22
	s_nop 0
	s_mov_b32 s22, m0
	s_mov_b32 m0, s31
	s_nop 2
	global_load_lds_dwordx4 v139, s[56:57]
	s_mov_b32 m0, s22
	s_add_u32 s22, s56, 0x40000
	s_addc_u32 s23, s57, 0
	s_mov_b32 s83, m0
	s_mov_b32 m0, s34
	s_nop 2
	global_load_lds_dwordx4 v137, s[22:23]
	s_mov_b32 m0, s83
	s_nop 0
	s_mov_b32 s83, m0
	s_mov_b32 m0, s35
	s_nop 2
	global_load_lds_dwordx4 v139, s[22:23]
	s_mov_b32 m0, s83
	s_mov_b32 s22, m0
	s_mov_b32 m0, s21
	s_nop 2
	global_load_lds_dwordx4 v136, s[58:59]
	s_mov_b32 m0, s22
	s_nop 0
	s_mov_b32 s22, m0
	s_mov_b32 m0, s36
	s_nop 2
	global_load_lds_dwordx4 v138, s[58:59]
	s_mov_b32 m0, s22
	s_waitcnt vmcnt(8)
	s_waitcnt lgkmcnt(0)
	s_barrier
	s_setprio 1
	v_mfma_f32_16x16x32_bf16 v[62:65], v[148:151], v[186:189], v[62:65]
	v_mfma_f32_16x16x32_bf16 v[58:61], v[156:159], v[186:189], v[58:61]
	v_mfma_f32_16x16x32_bf16 v[46:49], v[148:151], v[194:197], v[46:49]
	v_mfma_f32_16x16x32_bf16 v[42:45], v[156:159], v[194:197], v[42:45]
	v_mfma_f32_16x16x32_bf16 v[30:33], v[148:151], v[202:205], v[30:33]
	v_mfma_f32_16x16x32_bf16 v[26:29], v[156:159], v[202:205], v[26:29]
	v_mfma_f32_16x16x32_bf16 v[14:17], v[148:151], v[210:213], v[14:17]
	v_mfma_f32_16x16x32_bf16 v[10:13], v[156:159], v[210:213], v[10:13]
	v_mfma_f32_16x16x32_bf16 v[62:65], v[152:155], v[190:193], v[62:65]
	v_mfma_f32_16x16x32_bf16 v[58:61], v[160:163], v[190:193], v[58:61]
	v_mfma_f32_16x16x32_bf16 v[46:49], v[152:155], v[198:201], v[46:49]
	v_mfma_f32_16x16x32_bf16 v[42:45], v[160:163], v[198:201], v[42:45]
	v_mfma_f32_16x16x32_bf16 v[30:33], v[152:155], v[206:209], v[30:33]
	v_mfma_f32_16x16x32_bf16 v[26:29], v[160:163], v[206:209], v[26:29]
	v_mfma_f32_16x16x32_bf16 v[14:17], v[152:155], v[214:217], v[14:17]
	v_mfma_f32_16x16x32_bf16 v[10:13], v[160:163], v[214:217], v[10:13]
	s_setprio 0
	s_setprio 1
	v_mfma_f32_16x16x32_bf16 v[54:57], v[164:167], v[186:189], v[54:57]
	v_mfma_f32_16x16x32_bf16 v[50:53], v[178:181], v[186:189], v[50:53]
	v_mfma_f32_16x16x32_bf16 v[38:41], v[164:167], v[194:197], v[38:41]
	v_mfma_f32_16x16x32_bf16 v[34:37], v[178:181], v[194:197], v[34:37]
	v_mfma_f32_16x16x32_bf16 v[22:25], v[164:167], v[202:205], v[22:25]
	v_mfma_f32_16x16x32_bf16 v[18:21], v[178:181], v[202:205], v[18:21]
	v_mfma_f32_16x16x32_bf16 v[6:9], v[164:167], v[210:213], v[6:9]
	v_mfma_f32_16x16x32_bf16 v[2:5], v[178:181], v[210:213], v[2:5]
	v_mfma_f32_16x16x32_bf16 v[54:57], v[174:177], v[190:193], v[54:57]
	v_mfma_f32_16x16x32_bf16 v[50:53], v[182:185], v[190:193], v[50:53]
	v_mfma_f32_16x16x32_bf16 v[38:41], v[174:177], v[198:201], v[38:41]
	v_mfma_f32_16x16x32_bf16 v[34:37], v[182:185], v[198:201], v[34:37]
	v_mfma_f32_16x16x32_bf16 v[22:25], v[174:177], v[206:209], v[22:25]
	v_mfma_f32_16x16x32_bf16 v[18:21], v[182:185], v[206:209], v[18:21]
	v_mfma_f32_16x16x32_bf16 v[6:9], v[174:177], v[214:217], v[6:9]
	v_mfma_f32_16x16x32_bf16 v[2:5], v[182:185], v[214:217], v[2:5]
	s_setprio 0
	s_barrier
	ds_read_b128 v[148:151], v145
	ds_read_b128 v[152:155], v145 offset:1024
	ds_read_b128 v[156:159], v145 offset:2048
	ds_read_b128 v[160:163], v145 offset:3072
	ds_read_b128 v[164:167], v146
	ds_read_b128 v[174:177], v146 offset:1024
	ds_read_b128 v[178:181], v146 offset:2048
	ds_read_b128 v[182:185], v146 offset:3072
	ds_read_b128 v[186:189], v144 offset:32768
	ds_read_b128 v[190:193], v144 offset:33792
	ds_read_b128 v[194:197], v144 offset:34816
	ds_read_b128 v[198:201], v144 offset:35840
	ds_read_b128 v[202:205], v144 offset:36864
	ds_read_b128 v[206:209], v144 offset:37888
	ds_read_b128 v[210:213], v144 offset:38912
	ds_read_b128 v[214:217], v144 offset:39936
	s_add_u32 s22, s58, 0x40000
	s_addc_u32 s23, s59, 0
	s_mov_b32 s58, m0
	s_mov_b32 m0, s37
	s_nop 2
	global_load_lds_dwordx4 v136, s[22:23]
	s_mov_b32 m0, s58
	s_nop 0
	s_mov_b32 s58, m0
	s_mov_b32 m0, s52
	s_nop 2
	global_load_lds_dwordx4 v138, s[22:23]
	s_mov_b32 m0, s58
	s_waitcnt vmcnt(8)
	s_waitcnt lgkmcnt(0)
	s_barrier
	s_setprio 1
	v_mfma_f32_16x16x32_bf16 v[126:129], v[148:151], v[186:189], v[126:129]
	v_mfma_f32_16x16x32_bf16 v[122:125], v[156:159], v[186:189], v[122:125]
	v_mfma_f32_16x16x32_bf16 v[110:113], v[148:151], v[194:197], v[110:113]
	v_mfma_f32_16x16x32_bf16 v[106:109], v[156:159], v[194:197], v[106:109]
	v_mfma_f32_16x16x32_bf16 v[94:97], v[148:151], v[202:205], v[94:97]
	v_mfma_f32_16x16x32_bf16 v[90:93], v[156:159], v[202:205], v[90:93]
	v_mfma_f32_16x16x32_bf16 v[78:81], v[148:151], v[210:213], v[78:81]
	v_mfma_f32_16x16x32_bf16 v[74:77], v[156:159], v[210:213], v[74:77]
	v_mfma_f32_16x16x32_bf16 v[126:129], v[152:155], v[190:193], v[126:129]
	v_mfma_f32_16x16x32_bf16 v[122:125], v[160:163], v[190:193], v[122:125]
	v_mfma_f32_16x16x32_bf16 v[110:113], v[152:155], v[198:201], v[110:113]
	v_mfma_f32_16x16x32_bf16 v[106:109], v[160:163], v[198:201], v[106:109]
	v_mfma_f32_16x16x32_bf16 v[94:97], v[152:155], v[206:209], v[94:97]
	v_mfma_f32_16x16x32_bf16 v[90:93], v[160:163], v[206:209], v[90:93]
	v_mfma_f32_16x16x32_bf16 v[78:81], v[152:155], v[214:217], v[78:81]
	v_mfma_f32_16x16x32_bf16 v[74:77], v[160:163], v[214:217], v[74:77]
	s_setprio 0
	s_setprio 1
	v_mfma_f32_16x16x32_bf16 v[118:121], v[164:167], v[186:189], v[118:121]
	v_mfma_f32_16x16x32_bf16 v[114:117], v[178:181], v[186:189], v[114:117]
	v_mfma_f32_16x16x32_bf16 v[102:105], v[164:167], v[194:197], v[102:105]
	v_mfma_f32_16x16x32_bf16 v[98:101], v[178:181], v[194:197], v[98:101]
	v_mfma_f32_16x16x32_bf16 v[86:89], v[164:167], v[202:205], v[86:89]
	v_mfma_f32_16x16x32_bf16 v[82:85], v[178:181], v[202:205], v[82:85]
	v_mfma_f32_16x16x32_bf16 v[70:73], v[164:167], v[210:213], v[70:73]
	v_mfma_f32_16x16x32_bf16 v[66:69], v[178:181], v[210:213], v[66:69]
	v_mfma_f32_16x16x32_bf16 v[118:121], v[174:177], v[190:193], v[118:121]
	v_mfma_f32_16x16x32_bf16 v[114:117], v[182:185], v[190:193], v[114:117]
	v_mfma_f32_16x16x32_bf16 v[102:105], v[174:177], v[198:201], v[102:105]
	v_mfma_f32_16x16x32_bf16 v[98:101], v[182:185], v[198:201], v[98:101]
	v_mfma_f32_16x16x32_bf16 v[86:89], v[174:177], v[206:209], v[86:89]
	v_mfma_f32_16x16x32_bf16 v[82:85], v[182:185], v[206:209], v[82:85]
	v_mfma_f32_16x16x32_bf16 v[70:73], v[174:177], v[214:217], v[70:73]
	v_mfma_f32_16x16x32_bf16 v[66:69], v[182:185], v[214:217], v[66:69]
	s_setprio 0
	s_barrier
	ds_read_b128 v[186:189], v144 offset:49152
	ds_read_b128 v[190:193], v144 offset:50176
	ds_read_b128 v[194:197], v144 offset:51200
	ds_read_b128 v[198:201], v144 offset:52224
	ds_read_b128 v[202:205], v144 offset:53248
	ds_read_b128 v[206:209], v144 offset:54272
	ds_read_b128 v[210:213], v144 offset:55296
	ds_read_b128 v[214:217], v144 offset:56320
	s_add_u32 s22, s56, 0x80
	s_addc_u32 s23, s57, 0
	s_mov_b32 s58, m0
	s_mov_b32 m0, s61
	s_nop 2
	global_load_lds_dwordx4 v137, s[22:23]
	s_mov_b32 m0, s58
	s_nop 0
	s_mov_b32 s58, m0
	s_mov_b32 m0, s62
	s_nop 2
	global_load_lds_dwordx4 v139, s[22:23]
	s_mov_b32 m0, s58
	s_add_u32 s22, s56, 0x40080
	s_addc_u32 s23, s57, 0
	s_mov_b32 s56, m0
	s_mov_b32 m0, s65
	s_nop 2
	global_load_lds_dwordx4 v137, s[22:23]
	s_mov_b32 m0, s56
	s_nop 0
	s_mov_b32 s56, m0
	s_mov_b32 m0, s66
	s_nop 2
	global_load_lds_dwordx4 v139, s[22:23]
	s_mov_b32 m0, s56
	s_mov_b32 s22, m0
	s_mov_b32 m0, s63
	s_nop 2
	global_load_lds_dwordx4 v136, s[54:55]
	s_mov_b32 m0, s22
	s_nop 0
	s_mov_b32 s22, m0
	s_mov_b32 m0, s64
	s_nop 2
	global_load_lds_dwordx4 v138, s[54:55]
	s_mov_b32 m0, s22
	s_waitcnt vmcnt(8)
	s_waitcnt lgkmcnt(0)
	s_barrier
	s_setprio 1
	v_mfma_f32_16x16x32_bf16 v[62:65], v[148:151], v[186:189], v[62:65]
	v_mfma_f32_16x16x32_bf16 v[58:61], v[156:159], v[186:189], v[58:61]
	v_mfma_f32_16x16x32_bf16 v[46:49], v[148:151], v[194:197], v[46:49]
	v_mfma_f32_16x16x32_bf16 v[42:45], v[156:159], v[194:197], v[42:45]
	v_mfma_f32_16x16x32_bf16 v[30:33], v[148:151], v[202:205], v[30:33]
	v_mfma_f32_16x16x32_bf16 v[26:29], v[156:159], v[202:205], v[26:29]
	v_mfma_f32_16x16x32_bf16 v[14:17], v[148:151], v[210:213], v[14:17]
	v_mfma_f32_16x16x32_bf16 v[10:13], v[156:159], v[210:213], v[10:13]
	v_mfma_f32_16x16x32_bf16 v[62:65], v[152:155], v[190:193], v[62:65]
	v_mfma_f32_16x16x32_bf16 v[58:61], v[160:163], v[190:193], v[58:61]
	v_mfma_f32_16x16x32_bf16 v[46:49], v[152:155], v[198:201], v[46:49]
	v_mfma_f32_16x16x32_bf16 v[42:45], v[160:163], v[198:201], v[42:45]
	v_mfma_f32_16x16x32_bf16 v[30:33], v[152:155], v[206:209], v[30:33]
	v_mfma_f32_16x16x32_bf16 v[26:29], v[160:163], v[206:209], v[26:29]
	v_mfma_f32_16x16x32_bf16 v[14:17], v[152:155], v[214:217], v[14:17]
	v_mfma_f32_16x16x32_bf16 v[10:13], v[160:163], v[214:217], v[10:13]
	s_setprio 0
	s_setprio 1
	v_mfma_f32_16x16x32_bf16 v[54:57], v[164:167], v[186:189], v[54:57]
	v_mfma_f32_16x16x32_bf16 v[50:53], v[178:181], v[186:189], v[50:53]
	v_mfma_f32_16x16x32_bf16 v[38:41], v[164:167], v[194:197], v[38:41]
	v_mfma_f32_16x16x32_bf16 v[34:37], v[178:181], v[194:197], v[34:37]
	v_mfma_f32_16x16x32_bf16 v[22:25], v[164:167], v[202:205], v[22:25]
	v_mfma_f32_16x16x32_bf16 v[18:21], v[178:181], v[202:205], v[18:21]
	v_mfma_f32_16x16x32_bf16 v[6:9], v[164:167], v[210:213], v[6:9]
	v_mfma_f32_16x16x32_bf16 v[2:5], v[178:181], v[210:213], v[2:5]
	v_mfma_f32_16x16x32_bf16 v[54:57], v[174:177], v[190:193], v[54:57]
	v_mfma_f32_16x16x32_bf16 v[50:53], v[182:185], v[190:193], v[50:53]
	v_mfma_f32_16x16x32_bf16 v[38:41], v[174:177], v[198:201], v[38:41]
	v_mfma_f32_16x16x32_bf16 v[34:37], v[182:185], v[198:201], v[34:37]
	v_mfma_f32_16x16x32_bf16 v[22:25], v[174:177], v[206:209], v[22:25]
	v_mfma_f32_16x16x32_bf16 v[18:21], v[182:185], v[206:209], v[18:21]
	v_mfma_f32_16x16x32_bf16 v[6:9], v[174:177], v[214:217], v[6:9]
	v_mfma_f32_16x16x32_bf16 v[2:5], v[182:185], v[214:217], v[2:5]
	s_setprio 0
	s_barrier
	s_add_i32 s82, s82, 2
	s_add_u32 s80, s80, 0x100
	s_addc_u32 s81, s81, 0
	s_cmp_gt_u32 s82, 13
	s_mov_b64 s[22:23], s[40:41]
	s_cbranch_scc0 .LBB0_143
	s_and_b64 vcc, exec, s[10:11]
	s_cbranch_vccz .LBB0_146
	s_barrier

.Lpeel170:
	ds_read_b128 v[142:145], v136
	ds_read_b128 v[146:149], v136 offset:1024
	ds_read_b128 v[150:153], v136 offset:2048
	ds_read_b128 v[154:157], v136 offset:3072
	ds_read_b128 v[158:161], v137
	ds_read_b128 v[162:165], v137 offset:1024
	ds_read_b128 v[166:169], v137 offset:2048
	ds_read_b128 v[174:177], v137 offset:3072
	s_add_u32 s14, s12, 0x100
	s_addc_u32 s15, s13, 0
	s_cmp_eq_u32 s56, 12
	s_cselect_b32 s20, s10, s14
	s_cselect_b32 s21, s11, s15
	s_cselect_b32 s18, s8, s54
	s_cselect_b32 s19, s9, s55
	s_add_u32 s16, s20, 0x80
	s_addc_u32 s17, s21, 0
	ds_read_b128 v[178:181], v138
	ds_read_b128 v[182:185], v138 offset:1024
	ds_read_b128 v[186:189], v138 offset:2048
	ds_read_b128 v[190:193], v138 offset:3072
	ds_read_b128 v[194:197], v138 offset:4096
	ds_read_b128 v[198:201], v138 offset:5120
	ds_read_b128 v[202:205], v138 offset:6144
	ds_read_b128 v[206:209], v138 offset:7168
	s_add_u32 s12, s12, 0x40080
	s_addc_u32 s13, s13, 0
	s_mov_b32 s57, m0
	s_mov_b32 m0, s52
	s_nop 2
	global_load_lds_dwordx4 v132, s[12:13]
	s_mov_b32 m0, s57
	s_nop 0
	s_mov_b32 s57, m0
	s_mov_b32 m0, s53
	s_nop 2
	global_load_lds_dwordx4 v134, s[12:13]
	s_mov_b32 m0, s57
	s_waitcnt vmcnt(8)
	s_waitcnt lgkmcnt(0)
	s_barrier
	s_setprio 1
	v_mfma_f32_16x16x32_bf16 v[126:129], v[142:145], v[178:181], 0
	v_mfma_f32_16x16x32_bf16 v[122:125], v[150:153], v[178:181], 0
	v_mfma_f32_16x16x32_bf16 v[110:113], v[142:145], v[186:189], 0
	v_mfma_f32_16x16x32_bf16 v[106:109], v[150:153], v[186:189], 0
	v_mfma_f32_16x16x32_bf16 v[94:97], v[142:145], v[194:197], 0
	v_mfma_f32_16x16x32_bf16 v[90:93], v[150:153], v[194:197], 0
	v_mfma_f32_16x16x32_bf16 v[78:81], v[142:145], v[202:205], 0
	v_mfma_f32_16x16x32_bf16 v[74:77], v[150:153], v[202:205], 0
	v_mfma_f32_16x16x32_bf16 v[126:129], v[146:149], v[182:185], v[126:129]
	v_mfma_f32_16x16x32_bf16 v[122:125], v[154:157], v[182:185], v[122:125]
	v_mfma_f32_16x16x32_bf16 v[110:113], v[146:149], v[190:193], v[110:113]
	v_mfma_f32_16x16x32_bf16 v[106:109], v[154:157], v[190:193], v[106:109]
	v_mfma_f32_16x16x32_bf16 v[94:97], v[146:149], v[198:201], v[94:97]
	v_mfma_f32_16x16x32_bf16 v[90:93], v[154:157], v[198:201], v[90:93]
	v_mfma_f32_16x16x32_bf16 v[78:81], v[146:149], v[206:209], v[78:81]
	v_mfma_f32_16x16x32_bf16 v[74:77], v[154:157], v[206:209], v[74:77]
	s_setprio 0
	s_setprio 1
	v_mfma_f32_16x16x32_bf16 v[118:121], v[158:161], v[178:181], 0
	v_mfma_f32_16x16x32_bf16 v[114:117], v[166:169], v[178:181], 0
	v_mfma_f32_16x16x32_bf16 v[102:105], v[158:161], v[186:189], 0
	v_mfma_f32_16x16x32_bf16 v[98:101], v[166:169], v[186:189], 0
	v_mfma_f32_16x16x32_bf16 v[86:89], v[158:161], v[194:197], 0
	v_mfma_f32_16x16x32_bf16 v[82:85], v[166:169], v[194:197], 0
	v_mfma_f32_16x16x32_bf16 v[70:73], v[158:161], v[202:205], 0
	v_mfma_f32_16x16x32_bf16 v[66:69], v[166:169], v[202:205], 0
	v_mfma_f32_16x16x32_bf16 v[118:121], v[162:165], v[182:185], v[118:121]
	v_mfma_f32_16x16x32_bf16 v[114:117], v[174:177], v[182:185], v[114:117]
	v_mfma_f32_16x16x32_bf16 v[102:105], v[162:165], v[190:193], v[102:105]
	v_mfma_f32_16x16x32_bf16 v[98:101], v[174:177], v[190:193], v[98:101]
	v_mfma_f32_16x16x32_bf16 v[86:89], v[162:165], v[198:201], v[86:89]
	v_mfma_f32_16x16x32_bf16 v[82:85], v[174:177], v[198:201], v[82:85]
	v_mfma_f32_16x16x32_bf16 v[70:73], v[162:165], v[206:209], v[70:73]
	v_mfma_f32_16x16x32_bf16 v[66:69], v[174:177], v[206:209], v[66:69]
	s_setprio 0
	s_barrier
	ds_read_b128 v[178:181], v138 offset:16384
	ds_read_b128 v[182:185], v138 offset:17408
	ds_read_b128 v[186:189], v138 offset:18432
	ds_read_b128 v[190:193], v138 offset:19456
	ds_read_b128 v[194:197], v138 offset:20480
	ds_read_b128 v[198:201], v138 offset:21504
	ds_read_b128 v[202:205], v138 offset:22528
	ds_read_b128 v[206:209], v138 offset:23552
	s_mov_b32 s12, m0
	s_mov_b32 m0, s24
	s_nop 2
	global_load_lds_dwordx4 v133, s[18:19]
	s_mov_b32 m0, s12
	s_nop 0
	s_mov_b32 s12, m0
	s_mov_b32 m0, s25
	s_nop 2
	global_load_lds_dwordx4 v135, s[18:19]
	s_mov_b32 m0, s12
	s_add_u32 s12, s18, 0x40000
	s_addc_u32 s13, s19, 0
	s_mov_b32 s57, m0
	s_mov_b32 m0, s28
	s_nop 2
	global_load_lds_dwordx4 v133, s[12:13]
	s_mov_b32 m0, s57
	s_nop 0
	s_mov_b32 s57, m0
	s_mov_b32 m0, s29
	s_nop 2
	global_load_lds_dwordx4 v135, s[12:13]
	s_mov_b32 m0, s57
	s_mov_b32 s12, m0
	s_mov_b32 m0, s5
	s_nop 2
	global_load_lds_dwordx4 v132, s[20:21]
	s_mov_b32 m0, s12
	s_nop 0
	s_mov_b32 s12, m0
	s_mov_b32 m0, s30
	s_nop 2
	global_load_lds_dwordx4 v134, s[20:21]
	s_mov_b32 m0, s12
	s_waitcnt vmcnt(8)
	s_waitcnt lgkmcnt(0)
	s_barrier
	s_setprio 1
	v_mfma_f32_16x16x32_bf16 v[62:65], v[142:145], v[178:181], 0
	v_mfma_f32_16x16x32_bf16 v[58:61], v[150:153], v[178:181], 0
	v_mfma_f32_16x16x32_bf16 v[46:49], v[142:145], v[186:189], 0
	v_mfma_f32_16x16x32_bf16 v[42:45], v[150:153], v[186:189], 0
	v_mfma_f32_16x16x32_bf16 v[30:33], v[142:145], v[194:197], 0
	v_mfma_f32_16x16x32_bf16 v[26:29], v[150:153], v[194:197], 0
	v_mfma_f32_16x16x32_bf16 v[14:17], v[142:145], v[202:205], 0
	v_mfma_f32_16x16x32_bf16 v[10:13], v[150:153], v[202:205], 0
	v_mfma_f32_16x16x32_bf16 v[62:65], v[146:149], v[182:185], v[62:65]
	v_mfma_f32_16x16x32_bf16 v[58:61], v[154:157], v[182:185], v[58:61]
	v_mfma_f32_16x16x32_bf16 v[46:49], v[146:149], v[190:193], v[46:49]
	v_mfma_f32_16x16x32_bf16 v[42:45], v[154:157], v[190:193], v[42:45]
	v_mfma_f32_16x16x32_bf16 v[30:33], v[146:149], v[198:201], v[30:33]
	v_mfma_f32_16x16x32_bf16 v[26:29], v[154:157], v[198:201], v[26:29]
	v_mfma_f32_16x16x32_bf16 v[14:17], v[146:149], v[206:209], v[14:17]
	v_mfma_f32_16x16x32_bf16 v[10:13], v[154:157], v[206:209], v[10:13]
	s_setprio 0
	s_setprio 1
	v_mfma_f32_16x16x32_bf16 v[54:57], v[158:161], v[178:181], 0
	v_mfma_f32_16x16x32_bf16 v[50:53], v[166:169], v[178:181], 0
	v_mfma_f32_16x16x32_bf16 v[38:41], v[158:161], v[186:189], 0
	v_mfma_f32_16x16x32_bf16 v[34:37], v[166:169], v[186:189], 0
	v_mfma_f32_16x16x32_bf16 v[22:25], v[158:161], v[194:197], 0
	v_mfma_f32_16x16x32_bf16 v[18:21], v[166:169], v[194:197], 0
	v_mfma_f32_16x16x32_bf16 v[6:9], v[158:161], v[202:205], 0
	v_mfma_f32_16x16x32_bf16 v[2:5], v[166:169], v[202:205], 0
	v_mfma_f32_16x16x32_bf16 v[54:57], v[162:165], v[182:185], v[54:57]
	v_mfma_f32_16x16x32_bf16 v[50:53], v[174:177], v[182:185], v[50:53]
	v_mfma_f32_16x16x32_bf16 v[38:41], v[162:165], v[190:193], v[38:41]
	v_mfma_f32_16x16x32_bf16 v[34:37], v[174:177], v[190:193], v[34:37]
	v_mfma_f32_16x16x32_bf16 v[22:25], v[162:165], v[198:201], v[22:25]
	v_mfma_f32_16x16x32_bf16 v[18:21], v[174:177], v[198:201], v[18:21]
	v_mfma_f32_16x16x32_bf16 v[6:9], v[162:165], v[206:209], v[6:9]
	v_mfma_f32_16x16x32_bf16 v[2:5], v[174:177], v[206:209], v[2:5]
	s_setprio 0
	s_barrier
	s_branch .Lmid170
.LBB0_170:
	ds_read_b128 v[142:145], v136
	ds_read_b128 v[146:149], v136 offset:1024
	ds_read_b128 v[150:153], v136 offset:2048
	ds_read_b128 v[154:157], v136 offset:3072
	ds_read_b128 v[158:161], v137
	ds_read_b128 v[162:165], v137 offset:1024
	ds_read_b128 v[166:169], v137 offset:2048
	ds_read_b128 v[174:177], v137 offset:3072
	s_add_u32 s14, s12, 0x100
	s_addc_u32 s15, s13, 0
	s_cmp_eq_u32 s56, 12
	s_cselect_b32 s20, s10, s14
	s_cselect_b32 s21, s11, s15
	s_cselect_b32 s18, s8, s54
	s_cselect_b32 s19, s9, s55
	s_add_u32 s16, s20, 0x80
	s_addc_u32 s17, s21, 0
	ds_read_b128 v[178:181], v138
	ds_read_b128 v[182:185], v138 offset:1024
	ds_read_b128 v[186:189], v138 offset:2048
	ds_read_b128 v[190:193], v138 offset:3072
	ds_read_b128 v[194:197], v138 offset:4096
	ds_read_b128 v[198:201], v138 offset:5120
	ds_read_b128 v[202:205], v138 offset:6144
	ds_read_b128 v[206:209], v138 offset:7168
	s_add_u32 s12, s12, 0x40080
	s_addc_u32 s13, s13, 0
	s_mov_b32 s57, m0
	s_mov_b32 m0, s52
	s_nop 2
	global_load_lds_dwordx4 v132, s[12:13]
	s_mov_b32 m0, s57
	s_nop 0
	s_mov_b32 s57, m0
	s_mov_b32 m0, s53
	s_nop 2
	global_load_lds_dwordx4 v134, s[12:13]
	s_mov_b32 m0, s57
	s_waitcnt vmcnt(8)
	s_waitcnt lgkmcnt(0)
	s_barrier
	s_setprio 1
	v_mfma_f32_16x16x32_bf16 v[126:129], v[142:145], v[178:181], v[126:129]
	v_mfma_f32_16x16x32_bf16 v[122:125], v[150:153], v[178:181], v[122:125]
	v_mfma_f32_16x16x32_bf16 v[110:113], v[142:145], v[186:189], v[110:113]
	v_mfma_f32_16x16x32_bf16 v[106:109], v[150:153], v[186:189], v[106:109]
	v_mfma_f32_16x16x32_bf16 v[94:97], v[142:145], v[194:197], v[94:97]
	v_mfma_f32_16x16x32_bf16 v[90:93], v[150:153], v[194:197], v[90:93]
	v_mfma_f32_16x16x32_bf16 v[78:81], v[142:145], v[202:205], v[78:81]
	v_mfma_f32_16x16x32_bf16 v[74:77], v[150:153], v[202:205], v[74:77]
	v_mfma_f32_16x16x32_bf16 v[126:129], v[146:149], v[182:185], v[126:129]
	v_mfma_f32_16x16x32_bf16 v[122:125], v[154:157], v[182:185], v[122:125]
	v_mfma_f32_16x16x32_bf16 v[110:113], v[146:149], v[190:193], v[110:113]
	v_mfma_f32_16x16x32_bf16 v[106:109], v[154:157], v[190:193], v[106:109]
	v_mfma_f32_16x16x32_bf16 v[94:97], v[146:149], v[198:201], v[94:97]
	v_mfma_f32_16x16x32_bf16 v[90:93], v[154:157], v[198:201], v[90:93]
	v_mfma_f32_16x16x32_bf16 v[78:81], v[146:149], v[206:209], v[78:81]
	v_mfma_f32_16x16x32_bf16 v[74:77], v[154:157], v[206:209], v[74:77]
	s_setprio 0
	s_setprio 1
	v_mfma_f32_16x16x32_bf16 v[118:121], v[158:161], v[178:181], v[118:121]
	v_mfma_f32_16x16x32_bf16 v[114:117], v[166:169], v[178:181], v[114:117]
	v_mfma_f32_16x16x32_bf16 v[102:105], v[158:161], v[186:189], v[102:105]
	v_mfma_f32_16x16x32_bf16 v[98:101], v[166:169], v[186:189], v[98:101]
	v_mfma_f32_16x16x32_bf16 v[86:89], v[158:161], v[194:197], v[86:89]
	v_mfma_f32_16x16x32_bf16 v[82:85], v[166:169], v[194:197], v[82:85]
	v_mfma_f32_16x16x32_bf16 v[70:73], v[158:161], v[202:205], v[70:73]
	v_mfma_f32_16x16x32_bf16 v[66:69], v[166:169], v[202:205], v[66:69]
	v_mfma_f32_16x16x32_bf16 v[118:121], v[162:165], v[182:185], v[118:121]
	v_mfma_f32_16x16x32_bf16 v[114:117], v[174:177], v[182:185], v[114:117]
	v_mfma_f32_16x16x32_bf16 v[102:105], v[162:165], v[190:193], v[102:105]
	v_mfma_f32_16x16x32_bf16 v[98:101], v[174:177], v[190:193], v[98:101]
	v_mfma_f32_16x16x32_bf16 v[86:89], v[162:165], v[198:201], v[86:89]
	v_mfma_f32_16x16x32_bf16 v[82:85], v[174:177], v[198:201], v[82:85]
	v_mfma_f32_16x16x32_bf16 v[70:73], v[162:165], v[206:209], v[70:73]
	v_mfma_f32_16x16x32_bf16 v[66:69], v[174:177], v[206:209], v[66:69]
	s_setprio 0
	s_barrier
	ds_read_b128 v[178:181], v138 offset:16384
	ds_read_b128 v[182:185], v138 offset:17408
	ds_read_b128 v[186:189], v138 offset:18432
	ds_read_b128 v[190:193], v138 offset:19456
	ds_read_b128 v[194:197], v138 offset:20480
	ds_read_b128 v[198:201], v138 offset:21504
	ds_read_b128 v[202:205], v138 offset:22528
	ds_read_b128 v[206:209], v138 offset:23552
	s_mov_b32 s12, m0
	s_mov_b32 m0, s24
	s_nop 2
	global_load_lds_dwordx4 v133, s[18:19]
	s_mov_b32 m0, s12
	s_nop 0
	s_mov_b32 s12, m0
	s_mov_b32 m0, s25
	s_nop 2
	global_load_lds_dwordx4 v135, s[18:19]
	s_mov_b32 m0, s12
	s_add_u32 s12, s18, 0x40000
	s_addc_u32 s13, s19, 0
	s_mov_b32 s57, m0
	s_mov_b32 m0, s28
	s_nop 2
	global_load_lds_dwordx4 v133, s[12:13]
	s_mov_b32 m0, s57
	s_nop 0
	s_mov_b32 s57, m0
	s_mov_b32 m0, s29
	s_nop 2
	global_load_lds_dwordx4 v135, s[12:13]
	s_mov_b32 m0, s57
	s_mov_b32 s12, m0
	s_mov_b32 m0, s5
	s_nop 2
	global_load_lds_dwordx4 v132, s[20:21]
	s_mov_b32 m0, s12
	s_nop 0
	s_mov_b32 s12, m0
	s_mov_b32 m0, s30
	s_nop 2
	global_load_lds_dwordx4 v134, s[20:21]
	s_mov_b32 m0, s12
	s_waitcnt vmcnt(8)
	s_waitcnt lgkmcnt(0)
	s_barrier
	s_setprio 1
	v_mfma_f32_16x16x32_bf16 v[62:65], v[142:145], v[178:181], v[62:65]
	v_mfma_f32_16x16x32_bf16 v[58:61], v[150:153], v[178:181], v[58:61]
	v_mfma_f32_16x16x32_bf16 v[46:49], v[142:145], v[186:189], v[46:49]
	v_mfma_f32_16x16x32_bf16 v[42:45], v[150:153], v[186:189], v[42:45]
	v_mfma_f32_16x16x32_bf16 v[30:33], v[142:145], v[194:197], v[30:33]
	v_mfma_f32_16x16x32_bf16 v[26:29], v[150:153], v[194:197], v[26:29]
	v_mfma_f32_16x16x32_bf16 v[14:17], v[142:145], v[202:205], v[14:17]
	v_mfma_f32_16x16x32_bf16 v[10:13], v[150:153], v[202:205], v[10:13]
	v_mfma_f32_16x16x32_bf16 v[62:65], v[146:149], v[182:185], v[62:65]
	v_mfma_f32_16x16x32_bf16 v[58:61], v[154:157], v[182:185], v[58:61]
	v_mfma_f32_16x16x32_bf16 v[46:49], v[146:149], v[190:193], v[46:49]
	v_mfma_f32_16x16x32_bf16 v[42:45], v[154:157], v[190:193], v[42:45]
	v_mfma_f32_16x16x32_bf16 v[30:33], v[146:149], v[198:201], v[30:33]
	v_mfma_f32_16x16x32_bf16 v[26:29], v[154:157], v[198:201], v[26:29]
	v_mfma_f32_16x16x32_bf16 v[14:17], v[146:149], v[206:209], v[14:17]
	v_mfma_f32_16x16x32_bf16 v[10:13], v[154:157], v[206:209], v[10:13]
	s_setprio 0
	s_setprio 1
	v_mfma_f32_16x16x32_bf16 v[54:57], v[158:161], v[178:181], v[54:57]
	v_mfma_f32_16x16x32_bf16 v[50:53], v[166:169], v[178:181], v[50:53]
	v_mfma_f32_16x16x32_bf16 v[38:41], v[158:161], v[186:189], v[38:41]
	v_mfma_f32_16x16x32_bf16 v[34:37], v[166:169], v[186:189], v[34:37]
	v_mfma_f32_16x16x32_bf16 v[22:25], v[158:161], v[194:197], v[22:25]
	v_mfma_f32_16x16x32_bf16 v[18:21], v[166:169], v[194:197], v[18:21]
	v_mfma_f32_16x16x32_bf16 v[6:9], v[158:161], v[202:205], v[6:9]
	v_mfma_f32_16x16x32_bf16 v[2:5], v[166:169], v[202:205], v[2:5]
	v_mfma_f32_16x16x32_bf16 v[54:57], v[162:165], v[182:185], v[54:57]
	v_mfma_f32_16x16x32_bf16 v[50:53], v[174:177], v[182:185], v[50:53]
	v_mfma_f32_16x16x32_bf16 v[38:41], v[162:165], v[190:193], v[38:41]
	v_mfma_f32_16x16x32_bf16 v[34:37], v[174:177], v[190:193], v[34:37]
	v_mfma_f32_16x16x32_bf16 v[22:25], v[162:165], v[198:201], v[22:25]
	v_mfma_f32_16x16x32_bf16 v[18:21], v[174:177], v[198:201], v[18:21]
	v_mfma_f32_16x16x32_bf16 v[6:9], v[162:165], v[206:209], v[6:9]
	v_mfma_f32_16x16x32_bf16 v[2:5], v[174:177], v[206:209], v[2:5]
	s_setprio 0
	s_barrier
.Lmid170:
	ds_read_b128 v[142:145], v139
	ds_read_b128 v[146:149], v139 offset:1024
	ds_read_b128 v[150:153], v139 offset:2048
	ds_read_b128 v[154:157], v139 offset:3072
	ds_read_b128 v[158:161], v140
	ds_read_b128 v[162:165], v140 offset:1024
	ds_read_b128 v[166:169], v140 offset:2048
	ds_read_b128 v[174:177], v140 offset:3072
	ds_read_b128 v[178:181], v138 offset:32768
	ds_read_b128 v[182:185], v138 offset:33792
	ds_read_b128 v[186:189], v138 offset:34816
	ds_read_b128 v[190:193], v138 offset:35840
	ds_read_b128 v[194:197], v138 offset:36864
	ds_read_b128 v[198:201], v138 offset:37888
	ds_read_b128 v[202:205], v138 offset:38912
	ds_read_b128 v[206:209], v138 offset:39936
	s_add_u32 s12, s20, 0x40000
	s_addc_u32 s13, s21, 0
	s_mov_b32 s20, m0
	s_mov_b32 m0, s31
	s_nop 2
	global_load_lds_dwordx4 v132, s[12:13]
	s_mov_b32 m0, s20
	s_nop 0
	s_mov_b32 s20, m0
	s_mov_b32 m0, s33
	s_nop 2
	global_load_lds_dwordx4 v134, s[12:13]
	s_mov_b32 m0, s20
	s_waitcnt vmcnt(8)
	s_waitcnt lgkmcnt(0)
	s_barrier
	s_setprio 1
	v_mfma_f32_16x16x32_bf16 v[126:129], v[142:145], v[178:181], v[126:129]
	v_mfma_f32_16x16x32_bf16 v[122:125], v[150:153], v[178:181], v[122:125]
	v_mfma_f32_16x16x32_bf16 v[110:113], v[142:145], v[186:189], v[110:113]
	v_mfma_f32_16x16x32_bf16 v[106:109], v[150:153], v[186:189], v[106:109]
	v_mfma_f32_16x16x32_bf16 v[94:97], v[142:145], v[194:197], v[94:97]
	v_mfma_f32_16x16x32_bf16 v[90:93], v[150:153], v[194:197], v[90:93]
	v_mfma_f32_16x16x32_bf16 v[78:81], v[142:145], v[202:205], v[78:81]
	v_mfma_f32_16x16x32_bf16 v[74:77], v[150:153], v[202:205], v[74:77]
	v_mfma_f32_16x16x32_bf16 v[126:129], v[146:149], v[182:185], v[126:129]
	v_mfma_f32_16x16x32_bf16 v[122:125], v[154:157], v[182:185], v[122:125]
	v_mfma_f32_16x16x32_bf16 v[110:113], v[146:149], v[190:193], v[110:113]
	v_mfma_f32_16x16x32_bf16 v[106:109], v[154:157], v[190:193], v[106:109]
	v_mfma_f32_16x16x32_bf16 v[94:97], v[146:149], v[198:201], v[94:97]
	v_mfma_f32_16x16x32_bf16 v[90:93], v[154:157], v[198:201], v[90:93]
	v_mfma_f32_16x16x32_bf16 v[78:81], v[146:149], v[206:209], v[78:81]
	v_mfma_f32_16x16x32_bf16 v[74:77], v[154:157], v[206:209], v[74:77]
	s_setprio 0
	s_setprio 1
	v_mfma_f32_16x16x32_bf16 v[118:121], v[158:161], v[178:181], v[118:121]
	v_mfma_f32_16x16x32_bf16 v[114:117], v[166:169], v[178:181], v[114:117]
	v_mfma_f32_16x16x32_bf16 v[102:105], v[158:161], v[186:189], v[102:105]
	v_mfma_f32_16x16x32_bf16 v[98:101], v[166:169], v[186:189], v[98:101]
	v_mfma_f32_16x16x32_bf16 v[86:89], v[158:161], v[194:197], v[86:89]
	v_mfma_f32_16x16x32_bf16 v[82:85], v[166:169], v[194:197], v[82:85]
	v_mfma_f32_16x16x32_bf16 v[70:73], v[158:161], v[202:205], v[70:73]
	v_mfma_f32_16x16x32_bf16 v[66:69], v[166:169], v[202:205], v[66:69]
	v_mfma_f32_16x16x32_bf16 v[118:121], v[162:165], v[182:185], v[118:121]
	v_mfma_f32_16x16x32_bf16 v[114:117], v[174:177], v[182:185], v[114:117]
	v_mfma_f32_16x16x32_bf16 v[102:105], v[162:165], v[190:193], v[102:105]
	v_mfma_f32_16x16x32_bf16 v[98:101], v[174:177], v[190:193], v[98:101]
	v_mfma_f32_16x16x32_bf16 v[86:89], v[162:165], v[198:201], v[86:89]
	v_mfma_f32_16x16x32_bf16 v[82:85], v[174:177], v[198:201], v[82:85]
	v_mfma_f32_16x16x32_bf16 v[70:73], v[162:165], v[206:209], v[70:73]
	v_mfma_f32_16x16x32_bf16 v[66:69], v[174:177], v[206:209], v[66:69]
	s_setprio 0
	s_barrier
	ds_read_b128 v[178:181], v138 offset:49152
	ds_read_b128 v[182:185], v138 offset:50176
	ds_read_b128 v[186:189], v138 offset:51200
	ds_read_b128 v[190:193], v138 offset:52224
	ds_read_b128 v[194:197], v138 offset:53248
	ds_read_b128 v[198:201], v138 offset:54272
	ds_read_b128 v[202:205], v138 offset:55296
	ds_read_b128 v[206:209], v138 offset:56320
	s_add_u32 s12, s18, 0x80
	s_addc_u32 s13, s19, 0
	s_mov_b32 s20, m0
	s_mov_b32 m0, s34
	s_nop 2
	global_load_lds_dwordx4 v133, s[12:13]
	s_mov_b32 m0, s20
	s_nop 0
	s_mov_b32 s20, m0
	s_mov_b32 m0, s35
	s_nop 2
	global_load_lds_dwordx4 v135, s[12:13]
	s_mov_b32 m0, s20
	s_add_u32 s12, s18, 0x40080
	s_addc_u32 s13, s19, 0
	s_mov_b32 s18, m0
	s_mov_b32 m0, s40
	s_nop 2
	global_load_lds_dwordx4 v133, s[12:13]
	s_mov_b32 m0, s18
	s_nop 0
	s_mov_b32 s18, m0
	s_mov_b32 m0, s41
	s_nop 2
	global_load_lds_dwordx4 v135, s[12:13]
	s_mov_b32 m0, s18
	s_mov_b32 s12, m0
	s_mov_b32 m0, s36
	s_nop 2
	global_load_lds_dwordx4 v132, s[16:17]
	s_mov_b32 m0, s12
	s_nop 0
	s_mov_b32 s12, m0
	s_mov_b32 m0, s37
	s_nop 2
	global_load_lds_dwordx4 v134, s[16:17]
	s_mov_b32 m0, s12
	s_waitcnt vmcnt(8)
	s_waitcnt lgkmcnt(0)
	s_barrier
	s_setprio 1
	v_mfma_f32_16x16x32_bf16 v[62:65], v[142:145], v[178:181], v[62:65]
	v_mfma_f32_16x16x32_bf16 v[58:61], v[150:153], v[178:181], v[58:61]
	v_mfma_f32_16x16x32_bf16 v[46:49], v[142:145], v[186:189], v[46:49]
	v_mfma_f32_16x16x32_bf16 v[42:45], v[150:153], v[186:189], v[42:45]
	v_mfma_f32_16x16x32_bf16 v[30:33], v[142:145], v[194:197], v[30:33]
	v_mfma_f32_16x16x32_bf16 v[26:29], v[150:153], v[194:197], v[26:29]
	v_mfma_f32_16x16x32_bf16 v[14:17], v[142:145], v[202:205], v[14:17]
	v_mfma_f32_16x16x32_bf16 v[10:13], v[150:153], v[202:205], v[10:13]
	v_mfma_f32_16x16x32_bf16 v[62:65], v[146:149], v[182:185], v[62:65]
	v_mfma_f32_16x16x32_bf16 v[58:61], v[154:157], v[182:185], v[58:61]
	v_mfma_f32_16x16x32_bf16 v[46:49], v[146:149], v[190:193], v[46:49]
	v_mfma_f32_16x16x32_bf16 v[42:45], v[154:157], v[190:193], v[42:45]
	v_mfma_f32_16x16x32_bf16 v[30:33], v[146:149], v[198:201], v[30:33]
	v_mfma_f32_16x16x32_bf16 v[26:29], v[154:157], v[198:201], v[26:29]
	v_mfma_f32_16x16x32_bf16 v[14:17], v[146:149], v[206:209], v[14:17]
	v_mfma_f32_16x16x32_bf16 v[10:13], v[154:157], v[206:209], v[10:13]
	s_setprio 0
	s_setprio 1
	v_mfma_f32_16x16x32_bf16 v[54:57], v[158:161], v[178:181], v[54:57]
	v_mfma_f32_16x16x32_bf16 v[50:53], v[166:169], v[178:181], v[50:53]
	v_mfma_f32_16x16x32_bf16 v[38:41], v[158:161], v[186:189], v[38:41]
	v_mfma_f32_16x16x32_bf16 v[34:37], v[166:169], v[186:189], v[34:37]
	v_mfma_f32_16x16x32_bf16 v[22:25], v[158:161], v[194:197], v[22:25]
	v_mfma_f32_16x16x32_bf16 v[18:21], v[166:169], v[194:197], v[18:21]
	v_mfma_f32_16x16x32_bf16 v[6:9], v[158:161], v[202:205], v[6:9]
	v_mfma_f32_16x16x32_bf16 v[2:5], v[166:169], v[202:205], v[2:5]
	v_mfma_f32_16x16x32_bf16 v[54:57], v[162:165], v[182:185], v[54:57]
	v_mfma_f32_16x16x32_bf16 v[50:53], v[174:177], v[182:185], v[50:53]
	v_mfma_f32_16x16x32_bf16 v[38:41], v[162:165], v[190:193], v[38:41]
	v_mfma_f32_16x16x32_bf16 v[34:37], v[174:177], v[190:193], v[34:37]
	v_mfma_f32_16x16x32_bf16 v[22:25], v[162:165], v[198:201], v[22:25]
	v_mfma_f32_16x16x32_bf16 v[18:21], v[174:177], v[198:201], v[18:21]
	v_mfma_f32_16x16x32_bf16 v[6:9], v[162:165], v[206:209], v[6:9]
	v_mfma_f32_16x16x32_bf16 v[2:5], v[174:177], v[206:209], v[2:5]
	s_setprio 0
	s_barrier
	s_add_i32 s56, s56, 2
	s_add_u32 s54, s54, 0x100
	s_addc_u32 s55, s55, 0
	s_cmp_gt_u32 s56, 13
	s_mov_b64 s[12:13], s[14:15]
	s_cbranch_scc0 .LBB0_170
	s_cmpk_lt_u32 s23, 0x100
	s_cbranch_scc0 .LBB0_173
	s_barrier

.LBB0_190:
	ds_read_b128 v[18:21], v174
	ds_read_b128 v[22:25], v174 offset:1024
	ds_read_b128 v[26:29], v174 offset:2048
	ds_read_b128 v[30:33], v174 offset:3072
	ds_read_b128 v[2:5], v175
	ds_read_b128 v[6:9], v175 offset:1024
	ds_read_b128 v[10:13], v175 offset:2048
	ds_read_b128 v[14:17], v175 offset:3072
	s_add_u32 s76, s78, 0x100
	s_addc_u32 s77, s79, 0
	s_cmp_eq_u32 s33, 4
	s_cselect_b32 s84, s59, s76
	s_cselect_b32 s85, s7, s77
	s_cselect_b32 s82, s67, vcc_lo
	s_cselect_b32 s83, s57, vcc_hi
	s_add_u32 s80, s84, 0x80
	s_addc_u32 s81, s85, 0
	ds_read_b128 v[180:183], v176
	ds_read_b128 v[184:187], v176 offset:1024
	ds_read_b128 v[188:191], v176 offset:2048
	ds_read_b128 v[192:195], v176 offset:3072
	ds_read_b128 v[196:199], v176 offset:4096
	ds_read_b128 v[200:203], v176 offset:5120
	ds_read_b128 v[204:207], v176 offset:6144
	ds_read_b128 v[208:211], v176 offset:7168
	s_add_u32 s78, s78, 0x20080
	s_addc_u32 s79, s79, 0
	s_mov_b32 s88, m0
	s_mov_b32 m0, s96
	s_nop 2
	global_load_lds_dwordx4 v166, s[78:79]
	s_mov_b32 m0, s88
	s_nop 0
	s_mov_b32 s88, m0
	s_mov_b32 m0, s92
	s_nop 2
	global_load_lds_dwordx4 v168, s[78:79]
	s_mov_b32 m0, s88
	s_waitcnt vmcnt(8)
	s_waitcnt lgkmcnt(0)
	s_barrier
	s_setprio 1
	v_mfma_f32_16x16x128_f8f6f4 v[158:161], v[18:25], v[180:187], v[158:161]
	v_mfma_f32_16x16x128_f8f6f4 v[154:157], v[26:33], v[180:187], v[154:157]
	v_mfma_f32_16x16x128_f8f6f4 v[146:149], v[18:25], v[188:195], v[146:149]
	v_mfma_f32_16x16x128_f8f6f4 v[138:141], v[26:33], v[188:195], v[138:141]
	v_mfma_f32_16x16x128_f8f6f4 v[130:133], v[18:25], v[196:203], v[130:133]
	v_mfma_f32_16x16x128_f8f6f4 v[122:125], v[26:33], v[196:203], v[122:125]
	v_mfma_f32_16x16x128_f8f6f4 v[114:117], v[18:25], v[204:211], v[114:117]
	v_mfma_f32_16x16x128_f8f6f4 v[106:109], v[26:33], v[204:211], v[106:109]
	s_setprio 0
	s_setprio 1
	v_mfma_f32_16x16x128_f8f6f4 v[150:153], v[2:9], v[180:187], v[150:153]
	v_mfma_f32_16x16x128_f8f6f4 v[142:145], v[10:17], v[180:187], v[142:145]
	v_mfma_f32_16x16x128_f8f6f4 v[134:137], v[2:9], v[188:195], v[134:137]
	v_mfma_f32_16x16x128_f8f6f4 v[126:129], v[10:17], v[188:195], v[126:129]
	v_mfma_f32_16x16x128_f8f6f4 v[118:121], v[2:9], v[196:203], v[118:121]
	v_mfma_f32_16x16x128_f8f6f4 v[110:113], v[10:17], v[196:203], v[110:113]
	v_mfma_f32_16x16x128_f8f6f4 v[102:105], v[2:9], v[204:211], v[102:105]
	v_mfma_f32_16x16x128_f8f6f4 v[98:101], v[10:17], v[204:211], v[98:101]
	s_setprio 0
	s_barrier
	ds_read_b128 v[180:183], v176 offset:16384
	ds_read_b128 v[184:187], v176 offset:17408
	ds_read_b128 v[188:191], v176 offset:18432
	ds_read_b128 v[192:195], v176 offset:19456
	ds_read_b128 v[196:199], v176 offset:20480
	ds_read_b128 v[200:203], v176 offset:21504
	ds_read_b128 v[204:207], v176 offset:22528
	ds_read_b128 v[208:211], v176 offset:23552
	s_mov_b32 s78, m0
	s_mov_b32 m0, s36
	s_nop 2
	global_load_lds_dwordx4 v167, s[82:83]
	s_mov_b32 m0, s78
	s_nop 0
	s_mov_b32 s78, m0
	s_mov_b32 m0, s37
	s_nop 2
	global_load_lds_dwordx4 v169, s[82:83]
	s_mov_b32 m0, s78
	s_add_u32 s78, s82, 0x20000
	s_addc_u32 s79, s83, 0
	s_mov_b32 s88, m0
	s_mov_b32 m0, s55
	s_nop 2
	global_load_lds_dwordx4 v167, s[78:79]
	s_mov_b32 m0, s88
	s_nop 0
	s_mov_b32 s88, m0
	s_mov_b32 m0, s86
	s_nop 2
	global_load_lds_dwordx4 v169, s[78:79]
	s_mov_b32 m0, s88
	s_mov_b32 s78, m0
	s_mov_b32 m0, s35
	s_nop 2
	global_load_lds_dwordx4 v166, s[84:85]
	s_mov_b32 m0, s78
	s_nop 0
	s_mov_b32 s78, m0
	s_mov_b32 m0, s87
	s_nop 2
	global_load_lds_dwordx4 v168, s[84:85]
	s_mov_b32 m0, s78
	s_waitcnt vmcnt(8)
	s_waitcnt lgkmcnt(0)
	s_barrier
	s_setprio 1
	v_mfma_f32_16x16x128_f8f6f4 v[94:97], v[18:25], v[180:187], v[94:97]
	v_mfma_f32_16x16x128_f8f6f4 v[90:93], v[26:33], v[180:187], v[90:93]
	v_mfma_f32_16x16x128_f8f6f4 v[82:85], v[18:25], v[188:195], v[82:85]
	v_mfma_f32_16x16x128_f8f6f4 v[74:77], v[26:33], v[188:195], v[74:77]
	v_mfma_f32_16x16x128_f8f6f4 v[66:69], v[18:25], v[196:203], v[66:69]
	v_mfma_f32_16x16x128_f8f6f4 v[58:61], v[26:33], v[196:203], v[58:61]
	v_mfma_f32_16x16x128_f8f6f4 v[50:53], v[18:25], v[204:211], v[50:53]
	v_mfma_f32_16x16x128_f8f6f4 v[42:45], v[26:33], v[204:211], v[42:45]
	s_setprio 0
	s_setprio 1
	v_mfma_f32_16x16x128_f8f6f4 v[86:89], v[2:9], v[180:187], v[86:89]
	v_mfma_f32_16x16x128_f8f6f4 v[78:81], v[10:17], v[180:187], v[78:81]
	v_mfma_f32_16x16x128_f8f6f4 v[70:73], v[2:9], v[188:195], v[70:73]
	v_mfma_f32_16x16x128_f8f6f4 v[62:65], v[10:17], v[188:195], v[62:65]
	v_mfma_f32_16x16x128_f8f6f4 v[54:57], v[2:9], v[196:203], v[54:57]
	v_mfma_f32_16x16x128_f8f6f4 v[46:49], v[10:17], v[196:203], v[46:49]
	v_mfma_f32_16x16x128_f8f6f4 v[38:41], v[2:9], v[204:211], v[38:41]
	v_mfma_f32_16x16x128_f8f6f4 v[34:37], v[10:17], v[204:211], v[34:37]
	s_setprio 0
	s_barrier
	ds_read_b128 v[2:5], v177
	ds_read_b128 v[6:9], v177 offset:1024
	ds_read_b128 v[10:13], v177 offset:2048
	ds_read_b128 v[14:17], v177 offset:3072
	ds_read_b128 v[18:21], v178
	ds_read_b128 v[22:25], v178 offset:1024
	ds_read_b128 v[26:29], v178 offset:2048
	ds_read_b128 v[30:33], v178 offset:3072
	ds_read_b128 v[180:183], v176 offset:32768
	ds_read_b128 v[184:187], v176 offset:33792
	ds_read_b128 v[188:191], v176 offset:34816
	ds_read_b128 v[192:195], v176 offset:35840
	ds_read_b128 v[196:199], v176 offset:36864
	ds_read_b128 v[200:203], v176 offset:37888
	ds_read_b128 v[204:207], v176 offset:38912
	ds_read_b128 v[208:211], v176 offset:39936
	s_add_u32 s78, s84, 0x20000
	s_addc_u32 s79, s85, 0
	s_mov_b32 s84, m0
	s_mov_b32 m0, s89
	s_nop 2
	global_load_lds_dwordx4 v166, s[78:79]
	s_mov_b32 m0, s84
	s_nop 0
	s_mov_b32 s84, m0
	s_mov_b32 m0, s3
	s_nop 2
	global_load_lds_dwordx4 v168, s[78:79]
	s_mov_b32 m0, s84
	s_waitcnt vmcnt(8)
	s_waitcnt lgkmcnt(0)
	s_barrier
	s_setprio 1
	v_mfma_f32_16x16x128_f8f6f4 v[158:161], v[2:9], v[180:187], v[158:161]
	v_mfma_f32_16x16x128_f8f6f4 v[154:157], v[10:17], v[180:187], v[154:157]
	v_mfma_f32_16x16x128_f8f6f4 v[146:149], v[2:9], v[188:195], v[146:149]
	v_mfma_f32_16x16x128_f8f6f4 v[138:141], v[10:17], v[188:195], v[138:141]
	v_mfma_f32_16x16x128_f8f6f4 v[130:133], v[2:9], v[196:203], v[130:133]
	v_mfma_f32_16x16x128_f8f6f4 v[122:125], v[10:17], v[196:203], v[122:125]
	v_mfma_f32_16x16x128_f8f6f4 v[114:117], v[2:9], v[204:211], v[114:117]
	v_mfma_f32_16x16x128_f8f6f4 v[106:109], v[10:17], v[204:211], v[106:109]
	s_setprio 0
	s_setprio 1
	v_mfma_f32_16x16x128_f8f6f4 v[150:153], v[18:25], v[180:187], v[150:153]
	v_mfma_f32_16x16x128_f8f6f4 v[142:145], v[26:33], v[180:187], v[142:145]
	v_mfma_f32_16x16x128_f8f6f4 v[134:137], v[18:25], v[188:195], v[134:137]
	v_mfma_f32_16x16x128_f8f6f4 v[126:129], v[26:33], v[188:195], v[126:129]
	v_mfma_f32_16x16x128_f8f6f4 v[118:121], v[18:25], v[196:203], v[118:121]
	v_mfma_f32_16x16x128_f8f6f4 v[110:113], v[26:33], v[196:203], v[110:113]
	v_mfma_f32_16x16x128_f8f6f4 v[102:105], v[18:25], v[204:211], v[102:105]
	v_mfma_f32_16x16x128_f8f6f4 v[98:101], v[26:33], v[204:211], v[98:101]
	s_setprio 0
	s_barrier
	ds_read_b128 v[180:183], v176 offset:49152
	ds_read_b128 v[184:187], v176 offset:50176
	ds_read_b128 v[188:191], v176 offset:51200
	ds_read_b128 v[192:195], v176 offset:52224
	ds_read_b128 v[196:199], v176 offset:53248
	ds_read_b128 v[200:203], v176 offset:54272
	ds_read_b128 v[204:207], v176 offset:55296
	ds_read_b128 v[208:211], v176 offset:56320
	s_add_u32 s78, s82, 0x80
	s_addc_u32 s79, s83, 0
	s_mov_b32 s84, m0
	s_mov_b32 m0, s90
	s_nop 2
	global_load_lds_dwordx4 v167, s[78:79]
	s_mov_b32 m0, s84
	s_nop 0
	s_mov_b32 s84, m0
	s_mov_b32 m0, s28
	s_nop 2
	global_load_lds_dwordx4 v169, s[78:79]
	s_mov_b32 m0, s84
	s_add_u32 s78, s82, 0x20080
	s_addc_u32 s79, s83, 0
	s_mov_b32 s82, m0
	s_mov_b32 m0, s94
	s_nop 2
	global_load_lds_dwordx4 v167, s[78:79]
	s_mov_b32 m0, s82
	s_nop 0
	s_mov_b32 s82, m0
	s_mov_b32 m0, s95
	s_nop 2
	global_load_lds_dwordx4 v169, s[78:79]
	s_mov_b32 m0, s82
	s_mov_b32 s78, m0
	s_mov_b32 m0, s93
	s_nop 2
	global_load_lds_dwordx4 v166, s[80:81]
	s_mov_b32 m0, s78
	s_nop 0
	s_mov_b32 s78, m0
	s_mov_b32 m0, s2
	s_nop 2
	global_load_lds_dwordx4 v168, s[80:81]
	s_mov_b32 m0, s78
	s_waitcnt vmcnt(8)
	s_waitcnt lgkmcnt(0)
	s_barrier
	s_setprio 1
	v_mfma_f32_16x16x128_f8f6f4 v[94:97], v[2:9], v[180:187], v[94:97]
	v_mfma_f32_16x16x128_f8f6f4 v[90:93], v[10:17], v[180:187], v[90:93]
	v_mfma_f32_16x16x128_f8f6f4 v[82:85], v[2:9], v[188:195], v[82:85]
	v_mfma_f32_16x16x128_f8f6f4 v[74:77], v[10:17], v[188:195], v[74:77]
	v_mfma_f32_16x16x128_f8f6f4 v[66:69], v[2:9], v[196:203], v[66:69]
	v_mfma_f32_16x16x128_f8f6f4 v[58:61], v[10:17], v[196:203], v[58:61]
	v_mfma_f32_16x16x128_f8f6f4 v[50:53], v[2:9], v[204:211], v[50:53]
	v_mfma_f32_16x16x128_f8f6f4 v[42:45], v[10:17], v[204:211], v[42:45]
	s_setprio 0
	s_setprio 1
	v_mfma_f32_16x16x128_f8f6f4 v[86:89], v[18:25], v[180:187], v[86:89]
	v_mfma_f32_16x16x128_f8f6f4 v[78:81], v[26:33], v[180:187], v[78:81]
	v_mfma_f32_16x16x128_f8f6f4 v[70:73], v[18:25], v[188:195], v[70:73]
	v_mfma_f32_16x16x128_f8f6f4 v[62:65], v[26:33], v[188:195], v[62:65]
	v_mfma_f32_16x16x128_f8f6f4 v[54:57], v[18:25], v[196:203], v[54:57]
	v_mfma_f32_16x16x128_f8f6f4 v[46:49], v[26:33], v[196:203], v[46:49]
	v_mfma_f32_16x16x128_f8f6f4 v[38:41], v[18:25], v[204:211], v[38:41]
	v_mfma_f32_16x16x128_f8f6f4 v[34:37], v[26:33], v[204:211], v[34:37]
	s_setprio 0
	s_barrier
	s_add_i32 s33, s33, 2
	s_add_u32 vcc_lo, vcc_lo, 0x100
	s_addc_u32 vcc_hi, vcc_hi, 0
	s_cmp_gt_u32 s33, 5
	s_mov_b64 s[78:79], s[76:77]
	s_cbranch_scc0 .LBB0_190
	s_and_b64 vcc, exec, s[10:11]
	s_cbranch_vccz .LBB0_193
	s_barrier

.LBB0_217:
	s_cmp_lt_i32 s33, 0
	s_cbranch_scc1 .Lpeel1
	ds_read_b128 v[18:21], v168
	ds_read_b128 v[22:25], v168 offset:1024
	ds_read_b128 v[26:29], v168 offset:2048
	ds_read_b128 v[30:33], v168 offset:3072
	ds_read_b128 v[2:5], v169
	ds_read_b128 v[6:9], v169 offset:1024
	ds_read_b128 v[10:13], v169 offset:2048
	ds_read_b128 v[14:17], v169 offset:3072
	s_add_u32 s78, s80, 0x100
	s_addc_u32 s79, s81, 0
	s_cmp_eq_u32 s33, 4
	s_cselect_b32 s86, s57, s78
	s_cselect_b32 s87, s7, s79
	s_cselect_b32 s84, vcc_lo, vcc_hi
	s_cselect_b32 s85, s59, s89
	s_add_u32 s82, s86, 0x80
	s_addc_u32 s83, s87, 0
	ds_read_b128 v[176:179], v170
	ds_read_b128 v[180:183], v170 offset:1024
	ds_read_b128 v[184:187], v170 offset:2048
	ds_read_b128 v[188:191], v170 offset:3072
	ds_read_b128 v[192:195], v170 offset:4096
	ds_read_b128 v[196:199], v170 offset:5120
	ds_read_b128 v[200:203], v170 offset:6144
	ds_read_b128 v[204:207], v170 offset:7168
	s_add_u32 s80, s80, 0x20080
	s_addc_u32 s81, s81, 0
	s_mov_b32 s29, m0
	s_mov_b32 m0, s91
	s_nop 2
	global_load_lds_dwordx4 v162, s[80:81]
	s_mov_b32 m0, s29
	s_nop 0
	s_mov_b32 s29, m0
	s_mov_b32 m0, s92
	s_nop 2
	global_load_lds_dwordx4 v164, s[80:81]
	s_mov_b32 m0, s29
	s_waitcnt vmcnt(8)
	s_waitcnt lgkmcnt(0)
	s_barrier
	s_setprio 1
	v_mfma_f32_16x16x128_f8f6f4 v[158:161], v[18:25], v[176:183], v[158:161]
	v_mfma_f32_16x16x128_f8f6f4 v[154:157], v[26:33], v[176:183], v[154:157]
	v_mfma_f32_16x16x128_f8f6f4 v[146:149], v[18:25], v[184:191], v[146:149]
	v_mfma_f32_16x16x128_f8f6f4 v[138:141], v[26:33], v[184:191], v[138:141]
	v_mfma_f32_16x16x128_f8f6f4 v[130:133], v[18:25], v[192:199], v[130:133]
	v_mfma_f32_16x16x128_f8f6f4 v[122:125], v[26:33], v[192:199], v[122:125]
	v_mfma_f32_16x16x128_f8f6f4 v[114:117], v[18:25], v[200:207], v[114:117]
	v_mfma_f32_16x16x128_f8f6f4 v[106:109], v[26:33], v[200:207], v[106:109]
	s_setprio 0
	s_setprio 1
	v_mfma_f32_16x16x128_f8f6f4 v[150:153], v[2:9], v[176:183], v[150:153]
	v_mfma_f32_16x16x128_f8f6f4 v[142:145], v[10:17], v[176:183], v[142:145]
	v_mfma_f32_16x16x128_f8f6f4 v[134:137], v[2:9], v[184:191], v[134:137]
	v_mfma_f32_16x16x128_f8f6f4 v[126:129], v[10:17], v[184:191], v[126:129]
	v_mfma_f32_16x16x128_f8f6f4 v[118:121], v[2:9], v[192:199], v[118:121]
	v_mfma_f32_16x16x128_f8f6f4 v[110:113], v[10:17], v[192:199], v[110:113]
	v_mfma_f32_16x16x128_f8f6f4 v[102:105], v[2:9], v[200:207], v[102:105]
	v_mfma_f32_16x16x128_f8f6f4 v[98:101], v[10:17], v[200:207], v[98:101]
	s_setprio 0
	s_barrier
	ds_read_b128 v[176:179], v170 offset:16384
	ds_read_b128 v[180:183], v170 offset:17408
	ds_read_b128 v[184:187], v170 offset:18432
	ds_read_b128 v[188:191], v170 offset:19456
	ds_read_b128 v[192:195], v170 offset:20480
	ds_read_b128 v[196:199], v170 offset:21504
	ds_read_b128 v[200:203], v170 offset:22528
	ds_read_b128 v[204:207], v170 offset:23552
	s_mov_b32 s29, m0
	s_mov_b32 m0, s36
	s_nop 2
	global_load_lds_dwordx4 v163, s[84:85]
	s_mov_b32 m0, s29
	s_add_u32 s80, s84, 0x20000
	s_mov_b32 s29, m0
	s_mov_b32 m0, s37
	s_nop 2
	global_load_lds_dwordx4 v165, s[84:85]
	s_mov_b32 m0, s29
	s_addc_u32 s81, s85, 0
	s_mov_b32 s29, m0
	s_mov_b32 m0, s55
	s_nop 2
	global_load_lds_dwordx4 v163, s[80:81]
	s_mov_b32 m0, s29
	s_nop 0
	s_mov_b32 s29, m0
	s_mov_b32 m0, s77
	s_nop 2
	global_load_lds_dwordx4 v165, s[80:81]
	s_mov_b32 m0, s29
	s_nop 0
	s_mov_b32 s29, m0
	s_mov_b32 m0, s35
	s_nop 2
	global_load_lds_dwordx4 v162, s[86:87]
	s_mov_b32 m0, s29
	s_nop 0
	s_mov_b32 s29, m0
	s_mov_b32 m0, s88
	s_nop 2
	global_load_lds_dwordx4 v164, s[86:87]
	s_mov_b32 m0, s29
	s_waitcnt vmcnt(8)
	s_waitcnt lgkmcnt(0)
	s_barrier
	s_setprio 1
	v_mfma_f32_16x16x128_f8f6f4 v[94:97], v[18:25], v[176:183], v[94:97]
	v_mfma_f32_16x16x128_f8f6f4 v[90:93], v[26:33], v[176:183], v[90:93]
	v_mfma_f32_16x16x128_f8f6f4 v[82:85], v[18:25], v[184:191], v[82:85]
	v_mfma_f32_16x16x128_f8f6f4 v[74:77], v[26:33], v[184:191], v[74:77]
	v_mfma_f32_16x16x128_f8f6f4 v[66:69], v[18:25], v[192:199], v[66:69]
	v_mfma_f32_16x16x128_f8f6f4 v[58:61], v[26:33], v[192:199], v[58:61]
	v_mfma_f32_16x16x128_f8f6f4 v[50:53], v[18:25], v[200:207], v[50:53]
	v_mfma_f32_16x16x128_f8f6f4 v[42:45], v[26:33], v[200:207], v[42:45]
	s_setprio 0
	s_setprio 1
	v_mfma_f32_16x16x128_f8f6f4 v[86:89], v[2:9], v[176:183], v[86:89]
	v_mfma_f32_16x16x128_f8f6f4 v[78:81], v[10:17], v[176:183], v[78:81]
	v_mfma_f32_16x16x128_f8f6f4 v[70:73], v[2:9], v[184:191], v[70:73]
	v_mfma_f32_16x16x128_f8f6f4 v[62:65], v[10:17], v[184:191], v[62:65]
	v_mfma_f32_16x16x128_f8f6f4 v[54:57], v[2:9], v[192:199], v[54:57]
	v_mfma_f32_16x16x128_f8f6f4 v[46:49], v[10:17], v[192:199], v[46:49]
	v_mfma_f32_16x16x128_f8f6f4 v[38:41], v[2:9], v[200:207], v[38:41]
	v_mfma_f32_16x16x128_f8f6f4 v[34:37], v[10:17], v[200:207], v[34:37]
	s_setprio 0
	s_barrier
.Lmid1:
	ds_read_b128 v[2:5], v172
	ds_read_b128 v[6:9], v172 offset:1024
	ds_read_b128 v[10:13], v172 offset:2048
	ds_read_b128 v[14:17], v172 offset:3072
	ds_read_b128 v[18:21], v174
	ds_read_b128 v[22:25], v174 offset:1024
	ds_read_b128 v[26:29], v174 offset:2048
	ds_read_b128 v[30:33], v174 offset:3072
	ds_read_b128 v[176:179], v170 offset:32768
	ds_read_b128 v[180:183], v170 offset:33792
	ds_read_b128 v[184:187], v170 offset:34816
	ds_read_b128 v[188:191], v170 offset:35840
	ds_read_b128 v[192:195], v170 offset:36864
	ds_read_b128 v[196:199], v170 offset:37888
	ds_read_b128 v[200:203], v170 offset:38912
	ds_read_b128 v[204:207], v170 offset:39936
	s_add_u32 s80, s86, 0x20000
	s_addc_u32 s81, s87, 0
	s_mov_b32 s29, m0
	s_mov_b32 m0, s97
	s_nop 2
	global_load_lds_dwordx4 v162, s[80:81]
	s_mov_b32 m0, s29
	s_nop 0
	s_mov_b32 s29, m0
	s_mov_b32 m0, s3
	s_nop 2
	global_load_lds_dwordx4 v164, s[80:81]
	s_mov_b32 m0, s29
	s_waitcnt vmcnt(8)
	s_waitcnt lgkmcnt(0)
	s_barrier
	s_setprio 1
	v_mfma_f32_16x16x128_f8f6f4 v[158:161], v[2:9], v[176:183], v[158:161]
	v_mfma_f32_16x16x128_f8f6f4 v[154:157], v[10:17], v[176:183], v[154:157]
	v_mfma_f32_16x16x128_f8f6f4 v[146:149], v[2:9], v[184:191], v[146:149]
	v_mfma_f32_16x16x128_f8f6f4 v[138:141], v[10:17], v[184:191], v[138:141]
	v_mfma_f32_16x16x128_f8f6f4 v[130:133], v[2:9], v[192:199], v[130:133]
	v_mfma_f32_16x16x128_f8f6f4 v[122:125], v[10:17], v[192:199], v[122:125]
	v_mfma_f32_16x16x128_f8f6f4 v[114:117], v[2:9], v[200:207], v[114:117]
	v_mfma_f32_16x16x128_f8f6f4 v[106:109], v[10:17], v[200:207], v[106:109]
	s_setprio 0
	s_setprio 1
	v_mfma_f32_16x16x128_f8f6f4 v[150:153], v[18:25], v[176:183], v[150:153]
	v_mfma_f32_16x16x128_f8f6f4 v[142:145], v[26:33], v[176:183], v[142:145]
	v_mfma_f32_16x16x128_f8f6f4 v[134:137], v[18:25], v[184:191], v[134:137]
	v_mfma_f32_16x16x128_f8f6f4 v[126:129], v[26:33], v[184:191], v[126:129]
	v_mfma_f32_16x16x128_f8f6f4 v[118:121], v[18:25], v[192:199], v[118:121]
	v_mfma_f32_16x16x128_f8f6f4 v[110:113], v[26:33], v[192:199], v[110:113]
	v_mfma_f32_16x16x128_f8f6f4 v[102:105], v[18:25], v[200:207], v[102:105]
	v_mfma_f32_16x16x128_f8f6f4 v[98:101], v[26:33], v[200:207], v[98:101]
	s_setprio 0
	s_barrier
	ds_read_b128 v[176:179], v170 offset:49152
	ds_read_b128 v[180:183], v170 offset:50176
	ds_read_b128 v[184:187], v170 offset:51200
	ds_read_b128 v[188:191], v170 offset:52224
	ds_read_b128 v[192:195], v170 offset:53248
	ds_read_b128 v[196:199], v170 offset:54272
	ds_read_b128 v[200:203], v170 offset:55296
	ds_read_b128 v[204:207], v170 offset:56320
	s_add_u32 s80, s84, 0x80
	s_addc_u32 s81, s85, 0
	s_mov_b32 s29, m0
	s_mov_b32 m0, s90
	s_nop 2
	global_load_lds_dwordx4 v163, s[80:81]
	s_mov_b32 m0, s29
	s_nop 0
	s_mov_b32 s29, m0
	s_mov_b32 m0, s28
	s_nop 2
	global_load_lds_dwordx4 v165, s[80:81]
	s_mov_b32 m0, s29
	s_add_u32 s80, s84, 0x20080
	s_addc_u32 s81, s85, 0
	s_mov_b32 s29, m0
	s_mov_b32 m0, s94
	s_nop 2
	global_load_lds_dwordx4 v163, s[80:81]
	s_mov_b32 m0, s29
	s_nop 0
	s_mov_b32 s29, m0
	s_mov_b32 m0, s95
	s_nop 2
	global_load_lds_dwordx4 v165, s[80:81]
	s_mov_b32 m0, s29
	s_nop 0
	s_mov_b32 s29, m0
	s_mov_b32 m0, s93
	s_nop 2
	global_load_lds_dwordx4 v162, s[82:83]
	s_mov_b32 m0, s29
	s_nop 0
	s_mov_b32 s29, m0
	s_mov_b32 m0, s2
	s_nop 2
	global_load_lds_dwordx4 v164, s[82:83]
	s_mov_b32 m0, s29
	s_waitcnt vmcnt(8)
	s_waitcnt lgkmcnt(0)
	s_barrier
	s_setprio 1
	v_mfma_f32_16x16x128_f8f6f4 v[94:97], v[2:9], v[176:183], v[94:97]
	v_mfma_f32_16x16x128_f8f6f4 v[90:93], v[10:17], v[176:183], v[90:93]
	v_mfma_f32_16x16x128_f8f6f4 v[82:85], v[2:9], v[184:191], v[82:85]
	v_mfma_f32_16x16x128_f8f6f4 v[74:77], v[10:17], v[184:191], v[74:77]
	v_mfma_f32_16x16x128_f8f6f4 v[66:69], v[2:9], v[192:199], v[66:69]
	v_mfma_f32_16x16x128_f8f6f4 v[58:61], v[10:17], v[192:199], v[58:61]
	v_mfma_f32_16x16x128_f8f6f4 v[50:53], v[2:9], v[200:207], v[50:53]
	v_mfma_f32_16x16x128_f8f6f4 v[42:45], v[10:17], v[200:207], v[42:45]
	s_setprio 0
	s_setprio 1
	v_mfma_f32_16x16x128_f8f6f4 v[86:89], v[18:25], v[176:183], v[86:89]
	v_mfma_f32_16x16x128_f8f6f4 v[78:81], v[26:33], v[176:183], v[78:81]
	v_mfma_f32_16x16x128_f8f6f4 v[70:73], v[18:25], v[184:191], v[70:73]
	v_mfma_f32_16x16x128_f8f6f4 v[62:65], v[26:33], v[184:191], v[62:65]
	v_mfma_f32_16x16x128_f8f6f4 v[54:57], v[18:25], v[192:199], v[54:57]
	v_mfma_f32_16x16x128_f8f6f4 v[46:49], v[26:33], v[192:199], v[46:49]
	v_mfma_f32_16x16x128_f8f6f4 v[38:41], v[18:25], v[200:207], v[38:41]
	v_mfma_f32_16x16x128_f8f6f4 v[34:37], v[26:33], v[200:207], v[34:37]
	s_setprio 0
	s_cmp_lt_i32 s33, 4
	s_cbranch_scc1 .Lkb1_do
	s_cmp_lg_u64 s[10:11], 0
	s_cbranch_scc0 .Lkb1_skip

.Lpeel1:
	ds_read_b128 v[18:21], v168
	ds_read_b128 v[22:25], v168 offset:1024
	ds_read_b128 v[26:29], v168 offset:2048
	ds_read_b128 v[30:33], v168 offset:3072
	ds_read_b128 v[2:5], v169
	ds_read_b128 v[6:9], v169 offset:1024
	ds_read_b128 v[10:13], v169 offset:2048
	ds_read_b128 v[14:17], v169 offset:3072
	s_add_u32 s78, s80, 0x100
	s_addc_u32 s79, s81, 0
	s_cmp_eq_u32 s33, 4
	s_cselect_b32 s86, s57, s78
	s_cselect_b32 s87, s7, s79
	s_cselect_b32 s84, vcc_lo, vcc_hi
	s_cselect_b32 s85, s59, s89
	s_add_u32 s82, s86, 0x80
	s_addc_u32 s83, s87, 0
	ds_read_b128 v[176:179], v170
	ds_read_b128 v[180:183], v170 offset:1024
	ds_read_b128 v[184:187], v170 offset:2048
	ds_read_b128 v[188:191], v170 offset:3072
	ds_read_b128 v[192:195], v170 offset:4096
	ds_read_b128 v[196:199], v170 offset:5120
	ds_read_b128 v[200:203], v170 offset:6144
	ds_read_b128 v[204:207], v170 offset:7168
	s_add_u32 s80, s80, 0x20080
	s_addc_u32 s81, s81, 0
	s_mov_b32 s29, m0
	s_mov_b32 m0, s91
	s_nop 2
	global_load_lds_dwordx4 v162, s[80:81]
	s_mov_b32 m0, s29
	s_nop 0
	s_mov_b32 s29, m0
	s_mov_b32 m0, s92
	s_nop 2
	global_load_lds_dwordx4 v164, s[80:81]
	s_mov_b32 m0, s29
	s_waitcnt vmcnt(8)
	s_waitcnt lgkmcnt(0)
	s_barrier
	s_setprio 1
	v_mfma_f32_16x16x128_f8f6f4 v[158:161], v[18:25], v[176:183], 0
	v_mfma_f32_16x16x128_f8f6f4 v[154:157], v[26:33], v[176:183], 0
	v_mfma_f32_16x16x128_f8f6f4 v[146:149], v[18:25], v[184:191], 0
	v_mfma_f32_16x16x128_f8f6f4 v[138:141], v[26:33], v[184:191], 0
	v_mfma_f32_16x16x128_f8f6f4 v[130:133], v[18:25], v[192:199], 0
	v_mfma_f32_16x16x128_f8f6f4 v[122:125], v[26:33], v[192:199], 0
	v_mfma_f32_16x16x128_f8f6f4 v[114:117], v[18:25], v[200:207], 0
	v_mfma_f32_16x16x128_f8f6f4 v[106:109], v[26:33], v[200:207], 0
	s_setprio 0
	s_setprio 1
	v_mfma_f32_16x16x128_f8f6f4 v[150:153], v[2:9], v[176:183], 0
	v_mfma_f32_16x16x128_f8f6f4 v[142:145], v[10:17], v[176:183], 0
	v_mfma_f32_16x16x128_f8f6f4 v[134:137], v[2:9], v[184:191], 0
	v_mfma_f32_16x16x128_f8f6f4 v[126:129], v[10:17], v[184:191], 0
	v_mfma_f32_16x16x128_f8f6f4 v[118:121], v[2:9], v[192:199], 0
	v_mfma_f32_16x16x128_f8f6f4 v[110:113], v[10:17], v[192:199], 0
	v_mfma_f32_16x16x128_f8f6f4 v[102:105], v[2:9], v[200:207], 0
	v_mfma_f32_16x16x128_f8f6f4 v[98:101], v[10:17], v[200:207], 0
	s_setprio 0
	s_barrier
	ds_read_b128 v[176:179], v170 offset:16384
	ds_read_b128 v[180:183], v170 offset:17408
	ds_read_b128 v[184:187], v170 offset:18432
	ds_read_b128 v[188:191], v170 offset:19456
	ds_read_b128 v[192:195], v170 offset:20480
	ds_read_b128 v[196:199], v170 offset:21504
	ds_read_b128 v[200:203], v170 offset:22528
	ds_read_b128 v[204:207], v170 offset:23552
	s_mov_b32 s29, m0
	s_mov_b32 m0, s36
	s_nop 2
	global_load_lds_dwordx4 v163, s[84:85]
	s_mov_b32 m0, s29
	s_add_u32 s80, s84, 0x20000
	s_mov_b32 s29, m0
	s_mov_b32 m0, s37
	s_nop 2
	global_load_lds_dwordx4 v165, s[84:85]
	s_mov_b32 m0, s29
	s_addc_u32 s81, s85, 0
	s_mov_b32 s29, m0
	s_mov_b32 m0, s55
	s_nop 2
	global_load_lds_dwordx4 v163, s[80:81]
	s_mov_b32 m0, s29
	s_nop 0
	s_mov_b32 s29, m0
	s_mov_b32 m0, s77
	s_nop 2
	global_load_lds_dwordx4 v165, s[80:81]
	s_mov_b32 m0, s29
	s_nop 0
	s_mov_b32 s29, m0
	s_mov_b32 m0, s35
	s_nop 2
	global_load_lds_dwordx4 v162, s[86:87]
	s_mov_b32 m0, s29
	s_nop 0
	s_mov_b32 s29, m0
	s_mov_b32 m0, s88
	s_nop 2
	global_load_lds_dwordx4 v164, s[86:87]
	s_mov_b32 m0, s29
	s_waitcnt vmcnt(8)
	s_waitcnt lgkmcnt(0)
	s_barrier
	s_setprio 1
	v_mfma_f32_16x16x128_f8f6f4 v[94:97], v[18:25], v[176:183], 0
	v_mfma_f32_16x16x128_f8f6f4 v[90:93], v[26:33], v[176:183], 0
	v_mfma_f32_16x16x128_f8f6f4 v[82:85], v[18:25], v[184:191], 0
	v_mfma_f32_16x16x128_f8f6f4 v[74:77], v[26:33], v[184:191], 0
	v_mfma_f32_16x16x128_f8f6f4 v[66:69], v[18:25], v[192:199], 0
	v_mfma_f32_16x16x128_f8f6f4 v[58:61], v[26:33], v[192:199], 0
	v_mfma_f32_16x16x128_f8f6f4 v[50:53], v[18:25], v[200:207], 0
	v_mfma_f32_16x16x128_f8f6f4 v[42:45], v[26:33], v[200:207], 0
	s_setprio 0
	s_setprio 1
	v_mfma_f32_16x16x128_f8f6f4 v[86:89], v[2:9], v[176:183], 0
	v_mfma_f32_16x16x128_f8f6f4 v[78:81], v[10:17], v[176:183], 0
	v_mfma_f32_16x16x128_f8f6f4 v[70:73], v[2:9], v[184:191], 0
	v_mfma_f32_16x16x128_f8f6f4 v[62:65], v[10:17], v[184:191], 0
	v_mfma_f32_16x16x128_f8f6f4 v[54:57], v[2:9], v[192:199], 0
	v_mfma_f32_16x16x128_f8f6f4 v[46:49], v[10:17], v[192:199], 0
	v_mfma_f32_16x16x128_f8f6f4 v[38:41], v[2:9], v[200:207], 0
	v_mfma_f32_16x16x128_f8f6f4 v[34:37], v[10:17], v[200:207], 0
	s_setprio 0
	s_barrier
	s_branch .Lmid1

.Lpeel1046:
	ds_read_b128 v[136:139], v172
	ds_read_b128 v[140:143], v172 offset:1024
	ds_read_b128 v[144:147], v172 offset:2048
	ds_read_b128 v[148:151], v172 offset:3072
	ds_read_b128 v[152:155], v173
	ds_read_b128 v[156:159], v173 offset:1024
	ds_read_b128 v[160:163], v173 offset:2048
	ds_read_b128 v[178:181], v173 offset:3072
	s_add_u32 s25, s64, s56
	s_addc_u32 s33, s65, s57
	s_add_u32 s66, s25, 0x100
	s_addc_u32 s67, s33, 0
	s_add_u32 s23, s62, s56
	s_addc_u32 s24, s63, s57
	s_add_u32 s28, s23, 0x100
	s_addc_u32 s29, s24, 0
	s_add_u32 s58, s25, 0x180
	s_addc_u32 s59, s33, 0
	ds_read_b128 v[182:185], v174
	ds_read_b128 v[186:189], v174 offset:1024
	ds_read_b128 v[190:193], v174 offset:2048
	ds_read_b128 v[194:197], v174 offset:3072
	ds_read_b128 v[198:201], v174 offset:4096
	ds_read_b128 v[202:205], v174 offset:5120
	ds_read_b128 v[206:209], v174 offset:6144
	ds_read_b128 v[210:213], v174 offset:7168
	s_add_u32 s30, s25, 0x40080
	s_addc_u32 s31, s33, 0
	s_mov_b32 s36, m0
	s_mov_b32 m0, s26
	s_nop 2
	global_load_lds_dwordx4 v165, s[30:31]
	s_mov_b32 m0, s36
	s_nop 0
	s_mov_b32 s36, m0
	s_mov_b32 m0, s27
	s_nop 2
	global_load_lds_dwordx4 v167, s[30:31]
	s_mov_b32 m0, s36
	s_waitcnt vmcnt(8)
	s_waitcnt lgkmcnt(0)
	s_barrier
	s_setprio 1
	v_mfma_f32_16x16x32_bf16 v[26:29], v[136:139], v[182:185], 0
	v_mfma_f32_16x16x32_bf16 v[30:33], v[144:147], v[182:185], 0
	v_mfma_f32_16x16x32_bf16 v[50:53], v[136:139], v[190:193], 0
	v_mfma_f32_16x16x32_bf16 v[54:57], v[144:147], v[190:193], 0
	v_mfma_f32_16x16x32_bf16 v[74:77], v[136:139], v[198:201], 0
	v_mfma_f32_16x16x32_bf16 v[78:81], v[144:147], v[198:201], 0
	v_mfma_f32_16x16x32_bf16 v[94:97], v[136:139], v[206:209], 0
	v_mfma_f32_16x16x32_bf16 v[102:105], v[144:147], v[206:209], 0
	v_mfma_f32_16x16x32_bf16 v[26:29], v[140:143], v[186:189], v[26:29]
	v_mfma_f32_16x16x32_bf16 v[30:33], v[148:151], v[186:189], v[30:33]
	v_mfma_f32_16x16x32_bf16 v[50:53], v[140:143], v[194:197], v[50:53]
	v_mfma_f32_16x16x32_bf16 v[54:57], v[148:151], v[194:197], v[54:57]
	v_mfma_f32_16x16x32_bf16 v[74:77], v[140:143], v[202:205], v[74:77]
	v_mfma_f32_16x16x32_bf16 v[78:81], v[148:151], v[202:205], v[78:81]
	v_mfma_f32_16x16x32_bf16 v[94:97], v[140:143], v[210:213], v[94:97]
	v_mfma_f32_16x16x32_bf16 v[102:105], v[148:151], v[210:213], v[102:105]
	s_setprio 0
	s_setprio 1
	v_mfma_f32_16x16x32_bf16 v[38:41], v[152:155], v[182:185], 0
	v_mfma_f32_16x16x32_bf16 v[42:45], v[160:163], v[182:185], 0
	v_mfma_f32_16x16x32_bf16 v[62:65], v[152:155], v[190:193], 0
	v_mfma_f32_16x16x32_bf16 v[66:69], v[160:163], v[190:193], 0
	v_mfma_f32_16x16x32_bf16 v[82:85], v[152:155], v[198:201], 0
	v_mfma_f32_16x16x32_bf16 v[90:93], v[160:163], v[198:201], 0
	v_mfma_f32_16x16x32_bf16 v[106:109], v[152:155], v[206:209], 0
	v_mfma_f32_16x16x32_bf16 v[114:117], v[160:163], v[206:209], 0
	v_mfma_f32_16x16x32_bf16 v[38:41], v[156:159], v[186:189], v[38:41]
	v_mfma_f32_16x16x32_bf16 v[42:45], v[178:181], v[186:189], v[42:45]
	v_mfma_f32_16x16x32_bf16 v[62:65], v[156:159], v[194:197], v[62:65]
	v_mfma_f32_16x16x32_bf16 v[66:69], v[178:181], v[194:197], v[66:69]
	v_mfma_f32_16x16x32_bf16 v[82:85], v[156:159], v[202:205], v[82:85]
	v_mfma_f32_16x16x32_bf16 v[90:93], v[178:181], v[202:205], v[90:93]
	v_mfma_f32_16x16x32_bf16 v[106:109], v[156:159], v[210:213], v[106:109]
	v_mfma_f32_16x16x32_bf16 v[114:117], v[178:181], v[210:213], v[114:117]
	s_setprio 0
	s_barrier
	ds_read_b128 v[182:185], v174 offset:16384
	ds_read_b128 v[186:189], v174 offset:17408
	ds_read_b128 v[190:193], v174 offset:18432
	ds_read_b128 v[194:197], v174 offset:19456
	ds_read_b128 v[198:201], v174 offset:20480
	ds_read_b128 v[202:205], v174 offset:21504
	ds_read_b128 v[206:209], v174 offset:22528
	ds_read_b128 v[210:213], v174 offset:23552
	s_mov_b32 s30, m0
	s_mov_b32 m0, s80
	s_nop 2
	global_load_lds_dwordx4 v166, s[28:29]
	s_mov_b32 m0, s30
	s_nop 0
	s_mov_b32 s30, m0
	s_mov_b32 m0, s81
	s_nop 2
	global_load_lds_dwordx4 v168, s[28:29]
	s_mov_b32 m0, s30
	s_add_u32 s28, s23, 0x40100
	s_addc_u32 s29, s24, 0
	s_mov_b32 s30, m0
	s_mov_b32 m0, s82
	s_nop 2
	global_load_lds_dwordx4 v166, s[28:29]
	s_mov_b32 m0, s30
	s_nop 0
	s_mov_b32 s30, m0
	s_mov_b32 m0, s83
	s_nop 2
	global_load_lds_dwordx4 v168, s[28:29]
	s_mov_b32 m0, s30
	s_mov_b32 s28, m0
	s_mov_b32 m0, s79
	s_nop 2
	global_load_lds_dwordx4 v165, s[66:67]
	s_mov_b32 m0, s28
	s_nop 0
	s_mov_b32 s28, m0
	s_mov_b32 m0, s84
	s_nop 2
	global_load_lds_dwordx4 v167, s[66:67]
	s_mov_b32 m0, s28
	s_waitcnt vmcnt(8)
	s_waitcnt lgkmcnt(0)
	s_barrier
	s_setprio 1
	v_mfma_f32_16x16x32_bf16 v[118:121], v[136:139], v[182:185], 0
	v_mfma_f32_16x16x32_bf16 v[126:129], v[144:147], v[182:185], 0
	v_mfma_f32_16x16x32_bf16 v[98:101], v[136:139], v[190:193], 0
	v_mfma_f32_16x16x32_bf16 v[86:89], v[144:147], v[190:193], 0
	v_mfma_f32_16x16x32_bf16 v[46:49], v[136:139], v[198:201], 0
	v_mfma_f32_16x16x32_bf16 v[34:37], v[144:147], v[198:201], 0
	v_mfma_f32_16x16x32_bf16 v[14:17], v[136:139], v[206:209], 0
	v_mfma_f32_16x16x32_bf16 v[10:13], v[144:147], v[206:209], 0
	v_mfma_f32_16x16x32_bf16 v[118:121], v[140:143], v[186:189], v[118:121]
	v_mfma_f32_16x16x32_bf16 v[126:129], v[148:151], v[186:189], v[126:129]
	v_mfma_f32_16x16x32_bf16 v[98:101], v[140:143], v[194:197], v[98:101]
	v_mfma_f32_16x16x32_bf16 v[86:89], v[148:151], v[194:197], v[86:89]
	v_mfma_f32_16x16x32_bf16 v[46:49], v[140:143], v[202:205], v[46:49]
	v_mfma_f32_16x16x32_bf16 v[34:37], v[148:151], v[202:205], v[34:37]
	v_mfma_f32_16x16x32_bf16 v[14:17], v[140:143], v[210:213], v[14:17]
	v_mfma_f32_16x16x32_bf16 v[10:13], v[148:151], v[210:213], v[10:13]
	s_setprio 0
	s_setprio 1
	v_mfma_f32_16x16x32_bf16 v[122:125], v[152:155], v[182:185], 0
	v_mfma_f32_16x16x32_bf16 v[110:113], v[160:163], v[182:185], 0
	v_mfma_f32_16x16x32_bf16 v[70:73], v[152:155], v[190:193], 0
	v_mfma_f32_16x16x32_bf16 v[58:61], v[160:163], v[190:193], 0
	v_mfma_f32_16x16x32_bf16 v[22:25], v[152:155], v[198:201], 0
	v_mfma_f32_16x16x32_bf16 v[18:21], v[160:163], v[198:201], 0
	v_mfma_f32_16x16x32_bf16 v[6:9], v[152:155], v[206:209], 0
	v_mfma_f32_16x16x32_bf16 v[2:5], v[160:163], v[206:209], 0
	v_mfma_f32_16x16x32_bf16 v[122:125], v[156:159], v[186:189], v[122:125]
	v_mfma_f32_16x16x32_bf16 v[110:113], v[178:181], v[186:189], v[110:113]
	v_mfma_f32_16x16x32_bf16 v[70:73], v[156:159], v[194:197], v[70:73]
	v_mfma_f32_16x16x32_bf16 v[58:61], v[178:181], v[194:197], v[58:61]
	v_mfma_f32_16x16x32_bf16 v[22:25], v[156:159], v[202:205], v[22:25]
	v_mfma_f32_16x16x32_bf16 v[18:21], v[178:181], v[202:205], v[18:21]
	v_mfma_f32_16x16x32_bf16 v[6:9], v[156:159], v[210:213], v[6:9]
	v_mfma_f32_16x16x32_bf16 v[2:5], v[178:181], v[210:213], v[2:5]
	s_setprio 0
	s_barrier
	s_branch .Lmid1046
.LBB0_1046:
	ds_read_b128 v[136:139], v172
	ds_read_b128 v[140:143], v172 offset:1024
	ds_read_b128 v[144:147], v172 offset:2048
	ds_read_b128 v[148:151], v172 offset:3072
	ds_read_b128 v[152:155], v173
	ds_read_b128 v[156:159], v173 offset:1024
	ds_read_b128 v[160:163], v173 offset:2048
	ds_read_b128 v[178:181], v173 offset:3072
	s_add_u32 s25, s64, s56
	s_addc_u32 s33, s65, s57
	s_add_u32 s66, s25, 0x100
	s_addc_u32 s67, s33, 0
	s_add_u32 s23, s62, s56
	s_addc_u32 s24, s63, s57
	s_add_u32 s28, s23, 0x100
	s_addc_u32 s29, s24, 0
	s_add_u32 s58, s25, 0x180
	s_addc_u32 s59, s33, 0
	ds_read_b128 v[182:185], v174
	ds_read_b128 v[186:189], v174 offset:1024
	ds_read_b128 v[190:193], v174 offset:2048
	ds_read_b128 v[194:197], v174 offset:3072
	ds_read_b128 v[198:201], v174 offset:4096
	ds_read_b128 v[202:205], v174 offset:5120
	ds_read_b128 v[206:209], v174 offset:6144
	ds_read_b128 v[210:213], v174 offset:7168
	s_add_u32 s30, s25, 0x40080
	s_addc_u32 s31, s33, 0
	s_mov_b32 s36, m0
	s_mov_b32 m0, s26
	s_nop 2
	global_load_lds_dwordx4 v165, s[30:31]
	s_mov_b32 m0, s36
	s_nop 0
	s_mov_b32 s36, m0
	s_mov_b32 m0, s27
	s_nop 2
	global_load_lds_dwordx4 v167, s[30:31]
	s_mov_b32 m0, s36
	s_waitcnt vmcnt(8)
	s_waitcnt lgkmcnt(0)
	s_barrier
	s_setprio 1
	v_mfma_f32_16x16x32_bf16 v[26:29], v[136:139], v[182:185], v[26:29]
	v_mfma_f32_16x16x32_bf16 v[30:33], v[144:147], v[182:185], v[30:33]
	v_mfma_f32_16x16x32_bf16 v[50:53], v[136:139], v[190:193], v[50:53]
	v_mfma_f32_16x16x32_bf16 v[54:57], v[144:147], v[190:193], v[54:57]
	v_mfma_f32_16x16x32_bf16 v[74:77], v[136:139], v[198:201], v[74:77]
	v_mfma_f32_16x16x32_bf16 v[78:81], v[144:147], v[198:201], v[78:81]
	v_mfma_f32_16x16x32_bf16 v[94:97], v[136:139], v[206:209], v[94:97]
	v_mfma_f32_16x16x32_bf16 v[102:105], v[144:147], v[206:209], v[102:105]
	v_mfma_f32_16x16x32_bf16 v[26:29], v[140:143], v[186:189], v[26:29]
	v_mfma_f32_16x16x32_bf16 v[30:33], v[148:151], v[186:189], v[30:33]
	v_mfma_f32_16x16x32_bf16 v[50:53], v[140:143], v[194:197], v[50:53]
	v_mfma_f32_16x16x32_bf16 v[54:57], v[148:151], v[194:197], v[54:57]
	v_mfma_f32_16x16x32_bf16 v[74:77], v[140:143], v[202:205], v[74:77]
	v_mfma_f32_16x16x32_bf16 v[78:81], v[148:151], v[202:205], v[78:81]
	v_mfma_f32_16x16x32_bf16 v[94:97], v[140:143], v[210:213], v[94:97]
	v_mfma_f32_16x16x32_bf16 v[102:105], v[148:151], v[210:213], v[102:105]
	s_setprio 0
	s_setprio 1
	v_mfma_f32_16x16x32_bf16 v[38:41], v[152:155], v[182:185], v[38:41]
	v_mfma_f32_16x16x32_bf16 v[42:45], v[160:163], v[182:185], v[42:45]
	v_mfma_f32_16x16x32_bf16 v[62:65], v[152:155], v[190:193], v[62:65]
	v_mfma_f32_16x16x32_bf16 v[66:69], v[160:163], v[190:193], v[66:69]
	v_mfma_f32_16x16x32_bf16 v[82:85], v[152:155], v[198:201], v[82:85]
	v_mfma_f32_16x16x32_bf16 v[90:93], v[160:163], v[198:201], v[90:93]
	v_mfma_f32_16x16x32_bf16 v[106:109], v[152:155], v[206:209], v[106:109]
	v_mfma_f32_16x16x32_bf16 v[114:117], v[160:163], v[206:209], v[114:117]
	v_mfma_f32_16x16x32_bf16 v[38:41], v[156:159], v[186:189], v[38:41]
	v_mfma_f32_16x16x32_bf16 v[42:45], v[178:181], v[186:189], v[42:45]
	v_mfma_f32_16x16x32_bf16 v[62:65], v[156:159], v[194:197], v[62:65]
	v_mfma_f32_16x16x32_bf16 v[66:69], v[178:181], v[194:197], v[66:69]
	v_mfma_f32_16x16x32_bf16 v[82:85], v[156:159], v[202:205], v[82:85]
	v_mfma_f32_16x16x32_bf16 v[90:93], v[178:181], v[202:205], v[90:93]
	v_mfma_f32_16x16x32_bf16 v[106:109], v[156:159], v[210:213], v[106:109]
	v_mfma_f32_16x16x32_bf16 v[114:117], v[178:181], v[210:213], v[114:117]
	s_setprio 0
	s_barrier
	ds_read_b128 v[182:185], v174 offset:16384
	ds_read_b128 v[186:189], v174 offset:17408
	ds_read_b128 v[190:193], v174 offset:18432
	ds_read_b128 v[194:197], v174 offset:19456
	ds_read_b128 v[198:201], v174 offset:20480
	ds_read_b128 v[202:205], v174 offset:21504
	ds_read_b128 v[206:209], v174 offset:22528
	ds_read_b128 v[210:213], v174 offset:23552
	s_mov_b32 s30, m0
	s_mov_b32 m0, s80
	s_nop 2
	global_load_lds_dwordx4 v166, s[28:29]
	s_mov_b32 m0, s30
	s_nop 0
	s_mov_b32 s30, m0
	s_mov_b32 m0, s81
	s_nop 2
	global_load_lds_dwordx4 v168, s[28:29]
	s_mov_b32 m0, s30
	s_add_u32 s28, s23, 0x40100
	s_addc_u32 s29, s24, 0
	s_mov_b32 s30, m0
	s_mov_b32 m0, s82
	s_nop 2
	global_load_lds_dwordx4 v166, s[28:29]
	s_mov_b32 m0, s30
	s_nop 0
	s_mov_b32 s30, m0
	s_mov_b32 m0, s83
	s_nop 2
	global_load_lds_dwordx4 v168, s[28:29]
	s_mov_b32 m0, s30
	s_mov_b32 s28, m0
	s_mov_b32 m0, s79
	s_nop 2
	global_load_lds_dwordx4 v165, s[66:67]
	s_mov_b32 m0, s28
	s_nop 0
	s_mov_b32 s28, m0
	s_mov_b32 m0, s84
	s_nop 2
	global_load_lds_dwordx4 v167, s[66:67]
	s_mov_b32 m0, s28
	s_waitcnt vmcnt(8)
	s_waitcnt lgkmcnt(0)
	s_barrier
	s_setprio 1
	v_mfma_f32_16x16x32_bf16 v[118:121], v[136:139], v[182:185], v[118:121]
	v_mfma_f32_16x16x32_bf16 v[126:129], v[144:147], v[182:185], v[126:129]
	v_mfma_f32_16x16x32_bf16 v[98:101], v[136:139], v[190:193], v[98:101]
	v_mfma_f32_16x16x32_bf16 v[86:89], v[144:147], v[190:193], v[86:89]
	v_mfma_f32_16x16x32_bf16 v[46:49], v[136:139], v[198:201], v[46:49]
	v_mfma_f32_16x16x32_bf16 v[34:37], v[144:147], v[198:201], v[34:37]
	v_mfma_f32_16x16x32_bf16 v[14:17], v[136:139], v[206:209], v[14:17]
	v_mfma_f32_16x16x32_bf16 v[10:13], v[144:147], v[206:209], v[10:13]
	v_mfma_f32_16x16x32_bf16 v[118:121], v[140:143], v[186:189], v[118:121]
	v_mfma_f32_16x16x32_bf16 v[126:129], v[148:151], v[186:189], v[126:129]
	v_mfma_f32_16x16x32_bf16 v[98:101], v[140:143], v[194:197], v[98:101]
	v_mfma_f32_16x16x32_bf16 v[86:89], v[148:151], v[194:197], v[86:89]
	v_mfma_f32_16x16x32_bf16 v[46:49], v[140:143], v[202:205], v[46:49]
	v_mfma_f32_16x16x32_bf16 v[34:37], v[148:151], v[202:205], v[34:37]
	v_mfma_f32_16x16x32_bf16 v[14:17], v[140:143], v[210:213], v[14:17]
	v_mfma_f32_16x16x32_bf16 v[10:13], v[148:151], v[210:213], v[10:13]
	s_setprio 0
	s_setprio 1
	v_mfma_f32_16x16x32_bf16 v[122:125], v[152:155], v[182:185], v[122:125]
	v_mfma_f32_16x16x32_bf16 v[110:113], v[160:163], v[182:185], v[110:113]
	v_mfma_f32_16x16x32_bf16 v[70:73], v[152:155], v[190:193], v[70:73]
	v_mfma_f32_16x16x32_bf16 v[58:61], v[160:163], v[190:193], v[58:61]
	v_mfma_f32_16x16x32_bf16 v[22:25], v[152:155], v[198:201], v[22:25]
	v_mfma_f32_16x16x32_bf16 v[18:21], v[160:163], v[198:201], v[18:21]
	v_mfma_f32_16x16x32_bf16 v[6:9], v[152:155], v[206:209], v[6:9]
	v_mfma_f32_16x16x32_bf16 v[2:5], v[160:163], v[206:209], v[2:5]
	v_mfma_f32_16x16x32_bf16 v[122:125], v[156:159], v[186:189], v[122:125]
	v_mfma_f32_16x16x32_bf16 v[110:113], v[178:181], v[186:189], v[110:113]
	v_mfma_f32_16x16x32_bf16 v[70:73], v[156:159], v[194:197], v[70:73]
	v_mfma_f32_16x16x32_bf16 v[58:61], v[178:181], v[194:197], v[58:61]
	v_mfma_f32_16x16x32_bf16 v[22:25], v[156:159], v[202:205], v[22:25]
	v_mfma_f32_16x16x32_bf16 v[18:21], v[178:181], v[202:205], v[18:21]
	v_mfma_f32_16x16x32_bf16 v[6:9], v[156:159], v[210:213], v[6:9]
	v_mfma_f32_16x16x32_bf16 v[2:5], v[178:181], v[210:213], v[2:5]
	s_setprio 0
	s_barrier
.Lmid1046:
	ds_read_b128 v[136:139], v175
	ds_read_b128 v[140:143], v175 offset:1024
	ds_read_b128 v[144:147], v175 offset:2048
	ds_read_b128 v[148:151], v175 offset:3072
	ds_read_b128 v[152:155], v176
	ds_read_b128 v[156:159], v176 offset:1024
	ds_read_b128 v[160:163], v176 offset:2048
	ds_read_b128 v[178:181], v176 offset:3072
	ds_read_b128 v[182:185], v174 offset:32768
	ds_read_b128 v[186:189], v174 offset:33792
	ds_read_b128 v[190:193], v174 offset:34816
	ds_read_b128 v[194:197], v174 offset:35840
	ds_read_b128 v[198:201], v174 offset:36864
	ds_read_b128 v[202:205], v174 offset:37888
	ds_read_b128 v[206:209], v174 offset:38912
	ds_read_b128 v[210:213], v174 offset:39936
	s_add_u32 s28, s25, 0x40100
	s_addc_u32 s29, s33, 0
	s_mov_b32 s25, m0
	s_mov_b32 m0, s85
	s_nop 2
	global_load_lds_dwordx4 v165, s[28:29]
	s_mov_b32 m0, s25
	s_nop 0
	s_mov_b32 s25, m0
	s_mov_b32 m0, s86
	s_nop 2
	global_load_lds_dwordx4 v167, s[28:29]
	s_mov_b32 m0, s25
	s_waitcnt vmcnt(8)
	s_waitcnt lgkmcnt(0)
	s_barrier
	s_setprio 1
	v_mfma_f32_16x16x32_bf16 v[26:29], v[136:139], v[182:185], v[26:29]
	v_mfma_f32_16x16x32_bf16 v[30:33], v[144:147], v[182:185], v[30:33]
	v_mfma_f32_16x16x32_bf16 v[50:53], v[136:139], v[190:193], v[50:53]
	v_mfma_f32_16x16x32_bf16 v[54:57], v[144:147], v[190:193], v[54:57]
	v_mfma_f32_16x16x32_bf16 v[74:77], v[136:139], v[198:201], v[74:77]
	v_mfma_f32_16x16x32_bf16 v[78:81], v[144:147], v[198:201], v[78:81]
	v_mfma_f32_16x16x32_bf16 v[94:97], v[136:139], v[206:209], v[94:97]
	v_mfma_f32_16x16x32_bf16 v[102:105], v[144:147], v[206:209], v[102:105]
	v_mfma_f32_16x16x32_bf16 v[26:29], v[140:143], v[186:189], v[26:29]
	v_mfma_f32_16x16x32_bf16 v[30:33], v[148:151], v[186:189], v[30:33]
	v_mfma_f32_16x16x32_bf16 v[50:53], v[140:143], v[194:197], v[50:53]
	v_mfma_f32_16x16x32_bf16 v[54:57], v[148:151], v[194:197], v[54:57]
	v_mfma_f32_16x16x32_bf16 v[74:77], v[140:143], v[202:205], v[74:77]
	v_mfma_f32_16x16x32_bf16 v[78:81], v[148:151], v[202:205], v[78:81]
	v_mfma_f32_16x16x32_bf16 v[94:97], v[140:143], v[210:213], v[94:97]
	v_mfma_f32_16x16x32_bf16 v[102:105], v[148:151], v[210:213], v[102:105]
	s_setprio 0
	s_setprio 1
	v_mfma_f32_16x16x32_bf16 v[38:41], v[152:155], v[182:185], v[38:41]
	v_mfma_f32_16x16x32_bf16 v[42:45], v[160:163], v[182:185], v[42:45]
	v_mfma_f32_16x16x32_bf16 v[62:65], v[152:155], v[190:193], v[62:65]
	v_mfma_f32_16x16x32_bf16 v[66:69], v[160:163], v[190:193], v[66:69]
	v_mfma_f32_16x16x32_bf16 v[82:85], v[152:155], v[198:201], v[82:85]
	v_mfma_f32_16x16x32_bf16 v[90:93], v[160:163], v[198:201], v[90:93]
	v_mfma_f32_16x16x32_bf16 v[106:109], v[152:155], v[206:209], v[106:109]
	v_mfma_f32_16x16x32_bf16 v[114:117], v[160:163], v[206:209], v[114:117]
	v_mfma_f32_16x16x32_bf16 v[38:41], v[156:159], v[186:189], v[38:41]
	v_mfma_f32_16x16x32_bf16 v[42:45], v[178:181], v[186:189], v[42:45]
	v_mfma_f32_16x16x32_bf16 v[62:65], v[156:159], v[194:197], v[62:65]
	v_mfma_f32_16x16x32_bf16 v[66:69], v[178:181], v[194:197], v[66:69]
	v_mfma_f32_16x16x32_bf16 v[82:85], v[156:159], v[202:205], v[82:85]
	v_mfma_f32_16x16x32_bf16 v[90:93], v[178:181], v[202:205], v[90:93]
	v_mfma_f32_16x16x32_bf16 v[106:109], v[156:159], v[210:213], v[106:109]
	v_mfma_f32_16x16x32_bf16 v[114:117], v[178:181], v[210:213], v[114:117]
	s_setprio 0
	s_barrier
	ds_read_b128 v[182:185], v174 offset:49152
	ds_read_b128 v[186:189], v174 offset:50176
	ds_read_b128 v[190:193], v174 offset:51200
	ds_read_b128 v[194:197], v174 offset:52224
	ds_read_b128 v[198:201], v174 offset:53248
	ds_read_b128 v[202:205], v174 offset:54272
	ds_read_b128 v[206:209], v174 offset:55296
	ds_read_b128 v[210:213], v174 offset:56320
	s_add_u32 s28, s23, 0x180
	s_addc_u32 s29, s24, 0
	s_mov_b32 s25, m0
	s_mov_b32 m0, s92
	s_nop 2
	global_load_lds_dwordx4 v166, s[28:29]
	s_mov_b32 m0, s25
	s_nop 0
	s_mov_b32 s25, m0
	s_mov_b32 m0, s93
	s_nop 2
	global_load_lds_dwordx4 v168, s[28:29]
	s_mov_b32 m0, s25
	s_add_u32 s28, s23, 0x40180
	s_addc_u32 s29, s24, 0
	s_mov_b32 s23, m0
	s_mov_b32 m0, s96
	s_nop 2
	global_load_lds_dwordx4 v166, s[28:29]
	s_mov_b32 m0, s23
	s_nop 0
	s_mov_b32 s23, m0
	s_mov_b32 m0, s97
	s_nop 2
	global_load_lds_dwordx4 v168, s[28:29]
	s_mov_b32 m0, s23
	s_nop 0
	s_mov_b32 s23, m0
	s_mov_b32 m0, s94
	s_nop 2
	global_load_lds_dwordx4 v165, s[58:59]
	s_mov_b32 m0, s23
	s_nop 0
	s_mov_b32 s23, m0
	s_mov_b32 m0, s95
	s_nop 2
	global_load_lds_dwordx4 v167, s[58:59]
	s_mov_b32 m0, s23
	s_waitcnt vmcnt(8)
	s_waitcnt lgkmcnt(0)
	s_barrier
	s_setprio 1
	v_mfma_f32_16x16x32_bf16 v[118:121], v[136:139], v[182:185], v[118:121]
	v_mfma_f32_16x16x32_bf16 v[126:129], v[144:147], v[182:185], v[126:129]
	v_mfma_f32_16x16x32_bf16 v[98:101], v[136:139], v[190:193], v[98:101]
	v_mfma_f32_16x16x32_bf16 v[86:89], v[144:147], v[190:193], v[86:89]
	v_mfma_f32_16x16x32_bf16 v[46:49], v[136:139], v[198:201], v[46:49]
	v_mfma_f32_16x16x32_bf16 v[34:37], v[144:147], v[198:201], v[34:37]
	v_mfma_f32_16x16x32_bf16 v[14:17], v[136:139], v[206:209], v[14:17]
	v_mfma_f32_16x16x32_bf16 v[10:13], v[144:147], v[206:209], v[10:13]
	v_mfma_f32_16x16x32_bf16 v[118:121], v[140:143], v[186:189], v[118:121]
	v_mfma_f32_16x16x32_bf16 v[126:129], v[148:151], v[186:189], v[126:129]
	v_mfma_f32_16x16x32_bf16 v[98:101], v[140:143], v[194:197], v[98:101]
	v_mfma_f32_16x16x32_bf16 v[86:89], v[148:151], v[194:197], v[86:89]
	v_mfma_f32_16x16x32_bf16 v[46:49], v[140:143], v[202:205], v[46:49]
	v_mfma_f32_16x16x32_bf16 v[34:37], v[148:151], v[202:205], v[34:37]
	v_mfma_f32_16x16x32_bf16 v[14:17], v[140:143], v[210:213], v[14:17]
	v_mfma_f32_16x16x32_bf16 v[10:13], v[148:151], v[210:213], v[10:13]
	s_setprio 0
	s_setprio 1
	v_mfma_f32_16x16x32_bf16 v[122:125], v[152:155], v[182:185], v[122:125]
	v_mfma_f32_16x16x32_bf16 v[110:113], v[160:163], v[182:185], v[110:113]
	v_mfma_f32_16x16x32_bf16 v[70:73], v[152:155], v[190:193], v[70:73]
	v_mfma_f32_16x16x32_bf16 v[58:61], v[160:163], v[190:193], v[58:61]
	v_mfma_f32_16x16x32_bf16 v[22:25], v[152:155], v[198:201], v[22:25]
	v_mfma_f32_16x16x32_bf16 v[18:21], v[160:163], v[198:201], v[18:21]
	v_mfma_f32_16x16x32_bf16 v[6:9], v[152:155], v[206:209], v[6:9]
	v_mfma_f32_16x16x32_bf16 v[2:5], v[160:163], v[206:209], v[2:5]
	v_mfma_f32_16x16x32_bf16 v[122:125], v[156:159], v[186:189], v[122:125]
	v_mfma_f32_16x16x32_bf16 v[110:113], v[178:181], v[186:189], v[110:113]
	v_mfma_f32_16x16x32_bf16 v[70:73], v[156:159], v[194:197], v[70:73]
	v_mfma_f32_16x16x32_bf16 v[58:61], v[178:181], v[194:197], v[58:61]
	v_mfma_f32_16x16x32_bf16 v[22:25], v[156:159], v[202:205], v[22:25]
	v_mfma_f32_16x16x32_bf16 v[18:21], v[178:181], v[202:205], v[18:21]
	v_mfma_f32_16x16x32_bf16 v[6:9], v[156:159], v[210:213], v[6:9]
	v_mfma_f32_16x16x32_bf16 v[2:5], v[178:181], v[210:213], v[2:5]
	s_setprio 0
	s_barrier
	s_add_i32 s3, s3, 2
	s_add_u32 s56, s56, 0x100
	s_addc_u32 s57, s57, 0
	s_cmp_gt_u32 s3, 5
	s_cbranch_scc0 .LBB0_1046
	s_ashr_i32 s55, s54, 31
	s_lshl_b64 s[24:25], s[54:55], 19
	s_add_u32 s56, s69, s24
	s_addc_u32 s57, s76, s25
	s_ashr_i32 s23, s22, 31
	s_lshl_b64 s[24:25], s[22:23], 19
	s_add_u32 s58, s77, s24
	s_addc_u32 s59, s78, s25
	s_lshl_b32 s3, s60, 18
	s_lshl_b32 s23, s2, 8
	s_lshl_b32 s32, s2, 16
	s_add_i32 s2, s32, s3
	v_lshrrev_b32_e32 v214, 6, v0
	v_lshlrev_b32_e32 v214, 13, v214
	v_and_b32_e32 v215, 63, v0
	v_lshl_add_u32 v214, v215, 3, v214
	v_add_u32_e32 v134, s2, v214
	s_cmp_lg_u32 s37, 0
	s_cbranch_scc1 .Lmpf_have
	global_load_dwordx2 v[162:163], v134, s[14:15]
	global_load_dwordx2 v[178:179], v134, s[16:17]
	v_or_b32_e32 v136, 0x200, v134
	v_add_u32_e32 v137, 0x400, v134
	v_add_u32_e32 v138, 0x600, v134
	v_add_u32_e32 v139, 0x800, v134
	v_add_u32_e32 v140, 0xa00, v134
	v_add_u32_e32 v141, 0xc00, v134
	v_add_u32_e32 v161, 0xe00, v134
	global_load_dwordx2 v[180:181], v136, s[14:15]
	global_load_dwordx2 v[182:183], v136, s[16:17]
	global_load_dwordx2 v[158:159], v137, s[14:15]
	global_load_dwordx2 v[156:157], v137, s[16:17]
	global_load_dwordx2 v[154:155], v138, s[14:15]
	global_load_dwordx2 v[152:153], v138, s[16:17]
	global_load_dwordx2 v[150:151], v139, s[14:15]
	global_load_dwordx2 v[148:149], v139, s[16:17]
	global_load_dwordx2 v[146:147], v140, s[14:15]
	global_load_dwordx2 v[144:145], v140, s[16:17]
	global_load_dwordx2 v[142:143], v141, s[14:15]
	s_nop 0
	global_load_dwordx2 v[140:141], v141, s[16:17]
	s_nop 0
	global_load_dwordx2 v[138:139], v161, s[14:15]
	global_load_dwordx2 v[136:137], v161, s[16:17]
	s_branch .Lmpf_join

.LBB0_1048:
	ds_read_b128 v[136:139], v172
	ds_read_b128 v[140:143], v172 offset:1024
	ds_read_b128 v[144:147], v172 offset:2048
	ds_read_b128 v[148:151], v172 offset:3072
	ds_read_b128 v[152:155], v173
	ds_read_b128 v[156:159], v173 offset:1024
	ds_read_b128 v[160:163], v173 offset:2048
	ds_read_b128 v[178:181], v173 offset:3072
	s_cmp_eq_u32 s33, 12
	s_cselect_b32 s66, s3, s28
	s_cselect_b32 s67, s2, s29
	s_cselect_b32 s64, s25, s30
	s_cselect_b32 s65, s24, s31
	s_add_u32 s62, s66, 0x80
	s_addc_u32 s63, s67, 0
	ds_read_b128 v[182:185], v174
	ds_read_b128 v[186:189], v174 offset:1024
	ds_read_b128 v[190:193], v174 offset:2048
	ds_read_b128 v[194:197], v174 offset:3072
	ds_read_b128 v[198:201], v174 offset:4096
	ds_read_b128 v[202:205], v174 offset:5120
	ds_read_b128 v[206:209], v174 offset:6144
	ds_read_b128 v[210:213], v174 offset:7168
	s_add_u32 s36, s28, 0x3ff80
	s_addc_u32 s37, s29, 0
	s_mov_b32 s52, m0
	s_mov_b32 m0, s26
	s_nop 2
	global_load_lds_dwordx4 v165, s[36:37]
	s_mov_b32 m0, s52
	s_nop 0
	s_mov_b32 s52, m0
	s_mov_b32 m0, s27
	s_nop 2
	global_load_lds_dwordx4 v167, s[36:37]
	s_mov_b32 m0, s52
	s_waitcnt vmcnt(8)
	s_waitcnt lgkmcnt(0)
	s_barrier
	s_setprio 1
	v_mfma_f32_16x16x32_bf16 v[26:29], v[136:139], v[182:185], v[26:29]
	v_mfma_f32_16x16x32_bf16 v[30:33], v[144:147], v[182:185], v[30:33]
	v_mfma_f32_16x16x32_bf16 v[50:53], v[136:139], v[190:193], v[50:53]
	v_mfma_f32_16x16x32_bf16 v[54:57], v[144:147], v[190:193], v[54:57]
	v_mfma_f32_16x16x32_bf16 v[74:77], v[136:139], v[198:201], v[74:77]
	v_mfma_f32_16x16x32_bf16 v[78:81], v[144:147], v[198:201], v[78:81]
	v_mfma_f32_16x16x32_bf16 v[94:97], v[136:139], v[206:209], v[94:97]
	v_mfma_f32_16x16x32_bf16 v[102:105], v[144:147], v[206:209], v[102:105]
	v_mfma_f32_16x16x32_bf16 v[26:29], v[140:143], v[186:189], v[26:29]
	v_mfma_f32_16x16x32_bf16 v[30:33], v[148:151], v[186:189], v[30:33]
	v_mfma_f32_16x16x32_bf16 v[50:53], v[140:143], v[194:197], v[50:53]
	v_mfma_f32_16x16x32_bf16 v[54:57], v[148:151], v[194:197], v[54:57]
	v_mfma_f32_16x16x32_bf16 v[74:77], v[140:143], v[202:205], v[74:77]
	v_mfma_f32_16x16x32_bf16 v[78:81], v[148:151], v[202:205], v[78:81]
	v_mfma_f32_16x16x32_bf16 v[94:97], v[140:143], v[210:213], v[94:97]
	v_mfma_f32_16x16x32_bf16 v[102:105], v[148:151], v[210:213], v[102:105]
	s_setprio 0
	s_setprio 1
	v_mfma_f32_16x16x32_bf16 v[38:41], v[152:155], v[182:185], v[38:41]
	v_mfma_f32_16x16x32_bf16 v[42:45], v[160:163], v[182:185], v[42:45]
	v_mfma_f32_16x16x32_bf16 v[62:65], v[152:155], v[190:193], v[62:65]
	v_mfma_f32_16x16x32_bf16 v[66:69], v[160:163], v[190:193], v[66:69]
	v_mfma_f32_16x16x32_bf16 v[82:85], v[152:155], v[198:201], v[82:85]
	v_mfma_f32_16x16x32_bf16 v[90:93], v[160:163], v[198:201], v[90:93]
	v_mfma_f32_16x16x32_bf16 v[106:109], v[152:155], v[206:209], v[106:109]
	v_mfma_f32_16x16x32_bf16 v[114:117], v[160:163], v[206:209], v[114:117]
	v_mfma_f32_16x16x32_bf16 v[38:41], v[156:159], v[186:189], v[38:41]
	v_mfma_f32_16x16x32_bf16 v[42:45], v[178:181], v[186:189], v[42:45]
	v_mfma_f32_16x16x32_bf16 v[62:65], v[156:159], v[194:197], v[62:65]
	v_mfma_f32_16x16x32_bf16 v[66:69], v[178:181], v[194:197], v[66:69]
	v_mfma_f32_16x16x32_bf16 v[82:85], v[156:159], v[202:205], v[82:85]
	v_mfma_f32_16x16x32_bf16 v[90:93], v[178:181], v[202:205], v[90:93]
	v_mfma_f32_16x16x32_bf16 v[106:109], v[156:159], v[210:213], v[106:109]
	v_mfma_f32_16x16x32_bf16 v[114:117], v[178:181], v[210:213], v[114:117]
	s_setprio 0
	s_barrier
	ds_read_b128 v[182:185], v174 offset:16384
	ds_read_b128 v[186:189], v174 offset:17408
	ds_read_b128 v[190:193], v174 offset:18432
	ds_read_b128 v[194:197], v174 offset:19456
	ds_read_b128 v[198:201], v174 offset:20480
	ds_read_b128 v[202:205], v174 offset:21504
	ds_read_b128 v[206:209], v174 offset:22528
	ds_read_b128 v[210:213], v174 offset:23552
	s_mov_b32 s36, m0
	s_mov_b32 m0, s80
	s_nop 2
	global_load_lds_dwordx4 v166, s[64:65]
	s_mov_b32 m0, s36
	s_nop 0
	s_mov_b32 s36, m0
	s_mov_b32 m0, s81
	s_nop 2
	global_load_lds_dwordx4 v168, s[64:65]
	s_mov_b32 m0, s36
	s_add_u32 s36, s64, 0x40000
	s_addc_u32 s37, s65, 0
	s_mov_b32 s52, m0
	s_mov_b32 m0, s82
	s_nop 2
	global_load_lds_dwordx4 v166, s[36:37]
	s_mov_b32 m0, s52
	s_nop 0
	s_mov_b32 s52, m0
	s_mov_b32 m0, s83
	s_nop 2
	global_load_lds_dwordx4 v168, s[36:37]
	s_mov_b32 m0, s52
	s_mov_b32 s36, m0
	s_mov_b32 m0, s79
	s_nop 2
	global_load_lds_dwordx4 v165, s[66:67]
	s_mov_b32 m0, s36
	s_nop 0
	s_mov_b32 s36, m0
	s_mov_b32 m0, s84
	s_nop 2
	global_load_lds_dwordx4 v167, s[66:67]
	s_mov_b32 m0, s36
	s_waitcnt vmcnt(8)
	s_waitcnt lgkmcnt(0)
	s_barrier
	s_setprio 1
	v_mfma_f32_16x16x32_bf16 v[118:121], v[136:139], v[182:185], v[118:121]
	v_mfma_f32_16x16x32_bf16 v[126:129], v[144:147], v[182:185], v[126:129]
	v_mfma_f32_16x16x32_bf16 v[98:101], v[136:139], v[190:193], v[98:101]
	v_mfma_f32_16x16x32_bf16 v[86:89], v[144:147], v[190:193], v[86:89]
	v_mfma_f32_16x16x32_bf16 v[46:49], v[136:139], v[198:201], v[46:49]
	v_mfma_f32_16x16x32_bf16 v[34:37], v[144:147], v[198:201], v[34:37]
	v_mfma_f32_16x16x32_bf16 v[14:17], v[136:139], v[206:209], v[14:17]
	v_mfma_f32_16x16x32_bf16 v[10:13], v[144:147], v[206:209], v[10:13]
	v_mfma_f32_16x16x32_bf16 v[118:121], v[140:143], v[186:189], v[118:121]
	v_mfma_f32_16x16x32_bf16 v[126:129], v[148:151], v[186:189], v[126:129]
	v_mfma_f32_16x16x32_bf16 v[98:101], v[140:143], v[194:197], v[98:101]
	v_mfma_f32_16x16x32_bf16 v[86:89], v[148:151], v[194:197], v[86:89]
	v_mfma_f32_16x16x32_bf16 v[46:49], v[140:143], v[202:205], v[46:49]
	v_mfma_f32_16x16x32_bf16 v[34:37], v[148:151], v[202:205], v[34:37]
	v_mfma_f32_16x16x32_bf16 v[14:17], v[140:143], v[210:213], v[14:17]
	v_mfma_f32_16x16x32_bf16 v[10:13], v[148:151], v[210:213], v[10:13]
	s_setprio 0
	s_setprio 1
	v_mfma_f32_16x16x32_bf16 v[122:125], v[152:155], v[182:185], v[122:125]
	v_mfma_f32_16x16x32_bf16 v[110:113], v[160:163], v[182:185], v[110:113]
	v_mfma_f32_16x16x32_bf16 v[70:73], v[152:155], v[190:193], v[70:73]
	v_mfma_f32_16x16x32_bf16 v[58:61], v[160:163], v[190:193], v[58:61]
	v_mfma_f32_16x16x32_bf16 v[22:25], v[152:155], v[198:201], v[22:25]
	v_mfma_f32_16x16x32_bf16 v[18:21], v[160:163], v[198:201], v[18:21]
	v_mfma_f32_16x16x32_bf16 v[6:9], v[152:155], v[206:209], v[6:9]
	v_mfma_f32_16x16x32_bf16 v[2:5], v[160:163], v[206:209], v[2:5]
	v_mfma_f32_16x16x32_bf16 v[122:125], v[156:159], v[186:189], v[122:125]
	v_mfma_f32_16x16x32_bf16 v[110:113], v[178:181], v[186:189], v[110:113]
	v_mfma_f32_16x16x32_bf16 v[70:73], v[156:159], v[194:197], v[70:73]
	v_mfma_f32_16x16x32_bf16 v[58:61], v[178:181], v[194:197], v[58:61]
	v_mfma_f32_16x16x32_bf16 v[22:25], v[156:159], v[202:205], v[22:25]
	v_mfma_f32_16x16x32_bf16 v[18:21], v[178:181], v[202:205], v[18:21]
	v_mfma_f32_16x16x32_bf16 v[6:9], v[156:159], v[210:213], v[6:9]
	v_mfma_f32_16x16x32_bf16 v[2:5], v[178:181], v[210:213], v[2:5]
	s_setprio 0
	s_barrier
	ds_read_b128 v[136:139], v175
	ds_read_b128 v[140:143], v175 offset:1024
	ds_read_b128 v[144:147], v175 offset:2048
	ds_read_b128 v[148:151], v175 offset:3072
	ds_read_b128 v[152:155], v176
	ds_read_b128 v[156:159], v176 offset:1024
	ds_read_b128 v[160:163], v176 offset:2048
	ds_read_b128 v[178:181], v176 offset:3072
	ds_read_b128 v[182:185], v174 offset:32768
	ds_read_b128 v[186:189], v174 offset:33792
	ds_read_b128 v[190:193], v174 offset:34816
	ds_read_b128 v[194:197], v174 offset:35840
	ds_read_b128 v[198:201], v174 offset:36864
	ds_read_b128 v[202:205], v174 offset:37888
	ds_read_b128 v[206:209], v174 offset:38912
	ds_read_b128 v[210:213], v174 offset:39936
	s_add_u32 s36, s66, 0x40000
	s_addc_u32 s37, s67, 0
	s_mov_b32 s52, m0
	s_mov_b32 m0, s85
	s_nop 2
	global_load_lds_dwordx4 v165, s[36:37]
	s_mov_b32 m0, s52
	s_nop 0
	s_mov_b32 s52, m0
	s_mov_b32 m0, s86
	s_nop 2
	global_load_lds_dwordx4 v167, s[36:37]
	s_mov_b32 m0, s52
	s_waitcnt vmcnt(8)
	s_waitcnt lgkmcnt(0)
	s_barrier
	s_setprio 1
	v_mfma_f32_16x16x32_bf16 v[26:29], v[136:139], v[182:185], v[26:29]
	v_mfma_f32_16x16x32_bf16 v[30:33], v[144:147], v[182:185], v[30:33]
	v_mfma_f32_16x16x32_bf16 v[50:53], v[136:139], v[190:193], v[50:53]
	v_mfma_f32_16x16x32_bf16 v[54:57], v[144:147], v[190:193], v[54:57]
	v_mfma_f32_16x16x32_bf16 v[74:77], v[136:139], v[198:201], v[74:77]
	v_mfma_f32_16x16x32_bf16 v[78:81], v[144:147], v[198:201], v[78:81]
	v_mfma_f32_16x16x32_bf16 v[94:97], v[136:139], v[206:209], v[94:97]
	v_mfma_f32_16x16x32_bf16 v[102:105], v[144:147], v[206:209], v[102:105]
	v_mfma_f32_16x16x32_bf16 v[26:29], v[140:143], v[186:189], v[26:29]
	v_mfma_f32_16x16x32_bf16 v[30:33], v[148:151], v[186:189], v[30:33]
	v_mfma_f32_16x16x32_bf16 v[50:53], v[140:143], v[194:197], v[50:53]
	v_mfma_f32_16x16x32_bf16 v[54:57], v[148:151], v[194:197], v[54:57]
	v_mfma_f32_16x16x32_bf16 v[74:77], v[140:143], v[202:205], v[74:77]
	v_mfma_f32_16x16x32_bf16 v[78:81], v[148:151], v[202:205], v[78:81]
	v_mfma_f32_16x16x32_bf16 v[94:97], v[140:143], v[210:213], v[94:97]
	v_mfma_f32_16x16x32_bf16 v[102:105], v[148:151], v[210:213], v[102:105]
	s_setprio 0
	s_setprio 1
	v_mfma_f32_16x16x32_bf16 v[38:41], v[152:155], v[182:185], v[38:41]
	v_mfma_f32_16x16x32_bf16 v[42:45], v[160:163], v[182:185], v[42:45]
	v_mfma_f32_16x16x32_bf16 v[62:65], v[152:155], v[190:193], v[62:65]
	v_mfma_f32_16x16x32_bf16 v[66:69], v[160:163], v[190:193], v[66:69]
	v_mfma_f32_16x16x32_bf16 v[82:85], v[152:155], v[198:201], v[82:85]
	v_mfma_f32_16x16x32_bf16 v[90:93], v[160:163], v[198:201], v[90:93]
	v_mfma_f32_16x16x32_bf16 v[106:109], v[152:155], v[206:209], v[106:109]
	v_mfma_f32_16x16x32_bf16 v[114:117], v[160:163], v[206:209], v[114:117]
	v_mfma_f32_16x16x32_bf16 v[38:41], v[156:159], v[186:189], v[38:41]
	v_mfma_f32_16x16x32_bf16 v[42:45], v[178:181], v[186:189], v[42:45]
	v_mfma_f32_16x16x32_bf16 v[62:65], v[156:159], v[194:197], v[62:65]
	v_mfma_f32_16x16x32_bf16 v[66:69], v[178:181], v[194:197], v[66:69]
	v_mfma_f32_16x16x32_bf16 v[82:85], v[156:159], v[202:205], v[82:85]
	v_mfma_f32_16x16x32_bf16 v[90:93], v[178:181], v[202:205], v[90:93]
	v_mfma_f32_16x16x32_bf16 v[106:109], v[156:159], v[210:213], v[106:109]
	v_mfma_f32_16x16x32_bf16 v[114:117], v[178:181], v[210:213], v[114:117]
	s_setprio 0
	s_barrier
	ds_read_b128 v[182:185], v174 offset:49152
	ds_read_b128 v[186:189], v174 offset:50176
	ds_read_b128 v[190:193], v174 offset:51200
	ds_read_b128 v[194:197], v174 offset:52224
	ds_read_b128 v[198:201], v174 offset:53248
	ds_read_b128 v[202:205], v174 offset:54272
	ds_read_b128 v[206:209], v174 offset:55296
	ds_read_b128 v[210:213], v174 offset:56320
	s_add_u32 s36, s64, 0x80
	s_addc_u32 s37, s65, 0
	s_mov_b32 s52, m0
	s_mov_b32 m0, s92
	s_nop 2
	global_load_lds_dwordx4 v166, s[36:37]
	s_mov_b32 m0, s52
	s_nop 0
	s_mov_b32 s52, m0
	s_mov_b32 m0, s93
	s_nop 2
	global_load_lds_dwordx4 v168, s[36:37]
	s_mov_b32 m0, s52
	s_add_u32 s36, s64, 0x40080
	s_addc_u32 s37, s65, 0
	s_mov_b32 s52, m0
	s_mov_b32 m0, s96
	s_nop 2
	global_load_lds_dwordx4 v166, s[36:37]
	s_mov_b32 m0, s52
	s_nop 0
	s_mov_b32 s52, m0
	s_mov_b32 m0, s97
	s_nop 2
	global_load_lds_dwordx4 v168, s[36:37]
	s_mov_b32 m0, s52
	s_mov_b32 s36, m0
	s_mov_b32 m0, s94
	s_nop 2
	global_load_lds_dwordx4 v165, s[62:63]
	s_mov_b32 m0, s36
	s_nop 0
	s_mov_b32 s36, m0
	s_mov_b32 m0, s95
	s_nop 2
	global_load_lds_dwordx4 v167, s[62:63]
	s_mov_b32 m0, s36
	s_waitcnt vmcnt(8)
	s_waitcnt lgkmcnt(0)
	s_barrier
	s_setprio 1
	v_mfma_f32_16x16x32_bf16 v[118:121], v[136:139], v[182:185], v[118:121]
	v_mfma_f32_16x16x32_bf16 v[126:129], v[144:147], v[182:185], v[126:129]
	v_mfma_f32_16x16x32_bf16 v[98:101], v[136:139], v[190:193], v[98:101]
	v_mfma_f32_16x16x32_bf16 v[86:89], v[144:147], v[190:193], v[86:89]
	v_mfma_f32_16x16x32_bf16 v[46:49], v[136:139], v[198:201], v[46:49]
	v_mfma_f32_16x16x32_bf16 v[34:37], v[144:147], v[198:201], v[34:37]
	v_mfma_f32_16x16x32_bf16 v[14:17], v[136:139], v[206:209], v[14:17]
	v_mfma_f32_16x16x32_bf16 v[10:13], v[144:147], v[206:209], v[10:13]
	v_mfma_f32_16x16x32_bf16 v[118:121], v[140:143], v[186:189], v[118:121]
	v_mfma_f32_16x16x32_bf16 v[126:129], v[148:151], v[186:189], v[126:129]
	v_mfma_f32_16x16x32_bf16 v[98:101], v[140:143], v[194:197], v[98:101]
	v_mfma_f32_16x16x32_bf16 v[86:89], v[148:151], v[194:197], v[86:89]
	v_mfma_f32_16x16x32_bf16 v[46:49], v[140:143], v[202:205], v[46:49]
	v_mfma_f32_16x16x32_bf16 v[34:37], v[148:151], v[202:205], v[34:37]
	v_mfma_f32_16x16x32_bf16 v[14:17], v[140:143], v[210:213], v[14:17]
	v_mfma_f32_16x16x32_bf16 v[10:13], v[148:151], v[210:213], v[10:13]
	s_setprio 0
	s_setprio 1
	v_mfma_f32_16x16x32_bf16 v[122:125], v[152:155], v[182:185], v[122:125]
	v_mfma_f32_16x16x32_bf16 v[110:113], v[160:163], v[182:185], v[110:113]
	v_mfma_f32_16x16x32_bf16 v[70:73], v[152:155], v[190:193], v[70:73]
	v_mfma_f32_16x16x32_bf16 v[58:61], v[160:163], v[190:193], v[58:61]
	v_mfma_f32_16x16x32_bf16 v[22:25], v[152:155], v[198:201], v[22:25]
	v_mfma_f32_16x16x32_bf16 v[18:21], v[160:163], v[198:201], v[18:21]
	v_mfma_f32_16x16x32_bf16 v[6:9], v[152:155], v[206:209], v[6:9]
	v_mfma_f32_16x16x32_bf16 v[2:5], v[160:163], v[206:209], v[2:5]
	v_mfma_f32_16x16x32_bf16 v[122:125], v[156:159], v[186:189], v[122:125]
	v_mfma_f32_16x16x32_bf16 v[110:113], v[178:181], v[186:189], v[110:113]
	v_mfma_f32_16x16x32_bf16 v[70:73], v[156:159], v[194:197], v[70:73]
	v_mfma_f32_16x16x32_bf16 v[58:61], v[178:181], v[194:197], v[58:61]
	v_mfma_f32_16x16x32_bf16 v[22:25], v[156:159], v[202:205], v[22:25]
	v_mfma_f32_16x16x32_bf16 v[18:21], v[178:181], v[202:205], v[18:21]
	v_mfma_f32_16x16x32_bf16 v[6:9], v[156:159], v[210:213], v[6:9]
	v_mfma_f32_16x16x32_bf16 v[2:5], v[178:181], v[210:213], v[2:5]
	s_setprio 0
	s_barrier
	s_add_i32 s33, s33, 2
	s_add_u32 s28, s28, 0x100
	s_addc_u32 s29, s29, 0
	s_add_u32 s30, s30, 0x100
	s_addc_u32 s31, s31, 0
	s_cmp_lt_u32 s33, 14
	s_cbranch_scc1 .LBB0_1048
	s_and_b64 vcc, exec, s[20:21]
	s_cbranch_vccz .LBB0_1051
	s_barrier

.Lpeel1440:
	ds_read_b128 v[130:133], v234
	ds_read_b128 v[134:137], v234 offset:1024
	ds_read_b128 v[138:141], v234 offset:2048
	ds_read_b128 v[142:145], v234 offset:3072
	ds_read_b128 v[146:149], v235
	ds_read_b128 v[150:153], v235 offset:1024
	ds_read_b128 v[154:157], v235 offset:2048
	ds_read_b128 v[158:161], v235 offset:3072
	s_add_u32 s60, s58, 0x100
	s_addc_u32 s61, s59, 0
	s_cmp_eq_u32 s87, 12
	s_cselect_b32 s66, s33, s60
	s_cselect_b32 s67, s21, s61
	s_cselect_b32 s64, s84, s85
	s_cselect_b32 s65, s19, s86
	s_add_u32 s62, s66, 0x80
	s_addc_u32 s63, s67, 0
	ds_read_b128 v[162:165], v236
	ds_read_b128 v[166:169], v236 offset:1024
	ds_read_b128 v[170:173], v236 offset:2048
	ds_read_b128 v[174:177], v236 offset:3072
	ds_read_b128 v[178:181], v236 offset:4096
	ds_read_b128 v[182:185], v236 offset:5120
	ds_read_b128 v[186:189], v236 offset:6144
	ds_read_b128 v[190:193], v236 offset:7168
	s_add_u32 s58, s58, 0x40080
	s_addc_u32 s59, s59, 0
	s_mov_b32 s88, m0
	s_mov_b32 m0, s80
	s_nop 2
	global_load_lds_dwordx4 v228, s[58:59]
	s_mov_b32 m0, s88
	s_nop 0
	s_mov_b32 s88, m0
	s_mov_b32 m0, s81
	s_nop 2
	global_load_lds_dwordx4 v230, s[58:59]
	s_mov_b32 m0, s88
	s_waitcnt vmcnt(8)
	s_waitcnt lgkmcnt(0)
	s_barrier
	s_setprio 1
	v_mfma_f32_16x16x32_bf16 v[126:129], v[130:133], v[162:165], 0
	v_mfma_f32_16x16x32_bf16 v[122:125], v[138:141], v[162:165], 0
	v_mfma_f32_16x16x32_bf16 v[114:117], v[130:133], v[170:173], 0
	v_mfma_f32_16x16x32_bf16 v[106:109], v[138:141], v[170:173], 0
	v_mfma_f32_16x16x32_bf16 v[94:97], v[130:133], v[178:181], 0
	v_mfma_f32_16x16x32_bf16 v[90:93], v[138:141], v[178:181], 0
	v_mfma_f32_16x16x32_bf16 v[86:89], v[130:133], v[186:189], 0
	v_mfma_f32_16x16x32_bf16 v[78:81], v[138:141], v[186:189], 0
	v_mfma_f32_16x16x32_bf16 v[126:129], v[134:137], v[166:169], v[126:129]
	v_mfma_f32_16x16x32_bf16 v[122:125], v[142:145], v[166:169], v[122:125]
	v_mfma_f32_16x16x32_bf16 v[114:117], v[134:137], v[174:177], v[114:117]
	v_mfma_f32_16x16x32_bf16 v[106:109], v[142:145], v[174:177], v[106:109]
	v_mfma_f32_16x16x32_bf16 v[94:97], v[134:137], v[182:185], v[94:97]
	v_mfma_f32_16x16x32_bf16 v[90:93], v[142:145], v[182:185], v[90:93]
	v_mfma_f32_16x16x32_bf16 v[86:89], v[134:137], v[190:193], v[86:89]
	v_mfma_f32_16x16x32_bf16 v[78:81], v[142:145], v[190:193], v[78:81]
	s_setprio 0
	s_setprio 1
	v_mfma_f32_16x16x32_bf16 v[118:121], v[146:149], v[162:165], 0
	v_mfma_f32_16x16x32_bf16 v[110:113], v[154:157], v[162:165], 0
	v_mfma_f32_16x16x32_bf16 v[102:105], v[146:149], v[170:173], 0
	v_mfma_f32_16x16x32_bf16 v[98:101], v[154:157], v[170:173], 0
	v_mfma_f32_16x16x32_bf16 v[82:85], v[146:149], v[178:181], 0
	v_mfma_f32_16x16x32_bf16 v[74:77], v[154:157], v[178:181], 0
	v_mfma_f32_16x16x32_bf16 v[70:73], v[146:149], v[186:189], 0
	v_mfma_f32_16x16x32_bf16 v[66:69], v[154:157], v[186:189], 0
	v_mfma_f32_16x16x32_bf16 v[118:121], v[150:153], v[166:169], v[118:121]
	v_mfma_f32_16x16x32_bf16 v[110:113], v[158:161], v[166:169], v[110:113]
	v_mfma_f32_16x16x32_bf16 v[102:105], v[150:153], v[174:177], v[102:105]
	v_mfma_f32_16x16x32_bf16 v[98:101], v[158:161], v[174:177], v[98:101]
	v_mfma_f32_16x16x32_bf16 v[82:85], v[150:153], v[182:185], v[82:85]
	v_mfma_f32_16x16x32_bf16 v[74:77], v[158:161], v[182:185], v[74:77]
	v_mfma_f32_16x16x32_bf16 v[70:73], v[150:153], v[190:193], v[70:73]
	v_mfma_f32_16x16x32_bf16 v[66:69], v[158:161], v[190:193], v[66:69]
	s_setprio 0
	s_barrier
	ds_read_b128 v[162:165], v236 offset:16384
	ds_read_b128 v[166:169], v236 offset:17408
	ds_read_b128 v[170:173], v236 offset:18432
	ds_read_b128 v[174:177], v236 offset:19456
	ds_read_b128 v[178:181], v236 offset:20480
	ds_read_b128 v[182:185], v236 offset:21504
	ds_read_b128 v[186:189], v236 offset:22528
	ds_read_b128 v[190:193], v236 offset:23552
	s_mov_b32 s58, m0
	s_mov_b32 m0, s30
	s_nop 2
	global_load_lds_dwordx4 v229, s[64:65]
	s_mov_b32 m0, s58
	s_nop 0
	s_mov_b32 s58, m0
	s_mov_b32 m0, s31
	s_nop 2
	global_load_lds_dwordx4 v231, s[64:65]
	s_mov_b32 m0, s58
	s_add_u32 s58, s64, 0x40000
	s_addc_u32 s59, s65, 0
	s_mov_b32 s88, m0
	s_mov_b32 m0, s34
	s_nop 2
	global_load_lds_dwordx4 v229, s[58:59]
	s_mov_b32 m0, s88
	s_nop 0
	s_mov_b32 s88, m0
	s_mov_b32 m0, s35
	s_nop 2
	global_load_lds_dwordx4 v231, s[58:59]
	s_mov_b32 m0, s88
	s_mov_b32 s58, m0
	s_mov_b32 m0, s28
	s_nop 2
	global_load_lds_dwordx4 v228, s[66:67]
	s_mov_b32 m0, s58
	s_nop 0
	s_mov_b32 s58, m0
	s_mov_b32 m0, s36
	s_nop 2
	global_load_lds_dwordx4 v230, s[66:67]
	s_mov_b32 m0, s58
	s_waitcnt vmcnt(8)
	s_waitcnt lgkmcnt(0)
	s_barrier
	s_setprio 1
	v_mfma_f32_16x16x32_bf16 v[62:65], v[130:133], v[162:165], 0
	v_mfma_f32_16x16x32_bf16 v[58:61], v[138:141], v[162:165], 0
	v_mfma_f32_16x16x32_bf16 v[54:57], v[130:133], v[170:173], 0
	v_mfma_f32_16x16x32_bf16 v[46:49], v[138:141], v[170:173], 0
	v_mfma_f32_16x16x32_bf16 v[38:41], v[130:133], v[178:181], 0
	v_mfma_f32_16x16x32_bf16 v[30:33], v[138:141], v[178:181], 0
	v_mfma_f32_16x16x32_bf16 v[22:25], v[130:133], v[186:189], 0
	v_mfma_f32_16x16x32_bf16 v[14:17], v[138:141], v[186:189], 0
	v_mfma_f32_16x16x32_bf16 v[62:65], v[134:137], v[166:169], v[62:65]
	v_mfma_f32_16x16x32_bf16 v[58:61], v[142:145], v[166:169], v[58:61]
	v_mfma_f32_16x16x32_bf16 v[54:57], v[134:137], v[174:177], v[54:57]
	v_mfma_f32_16x16x32_bf16 v[46:49], v[142:145], v[174:177], v[46:49]
	v_mfma_f32_16x16x32_bf16 v[38:41], v[134:137], v[182:185], v[38:41]
	v_mfma_f32_16x16x32_bf16 v[30:33], v[142:145], v[182:185], v[30:33]
	v_mfma_f32_16x16x32_bf16 v[22:25], v[134:137], v[190:193], v[22:25]
	v_mfma_f32_16x16x32_bf16 v[14:17], v[142:145], v[190:193], v[14:17]
	s_setprio 0
	s_setprio 1
	v_mfma_f32_16x16x32_bf16 v[50:53], v[146:149], v[162:165], 0
	v_mfma_f32_16x16x32_bf16 v[42:45], v[154:157], v[162:165], 0
	v_mfma_f32_16x16x32_bf16 v[34:37], v[146:149], v[170:173], 0
	v_mfma_f32_16x16x32_bf16 v[26:29], v[154:157], v[170:173], 0
	v_mfma_f32_16x16x32_bf16 v[18:21], v[146:149], v[178:181], 0
	v_mfma_f32_16x16x32_bf16 v[10:13], v[154:157], v[178:181], 0
	v_mfma_f32_16x16x32_bf16 v[6:9], v[146:149], v[186:189], 0
	v_mfma_f32_16x16x32_bf16 v[2:5], v[154:157], v[186:189], 0
	v_mfma_f32_16x16x32_bf16 v[50:53], v[150:153], v[166:169], v[50:53]
	v_mfma_f32_16x16x32_bf16 v[42:45], v[158:161], v[166:169], v[42:45]
	v_mfma_f32_16x16x32_bf16 v[34:37], v[150:153], v[174:177], v[34:37]
	v_mfma_f32_16x16x32_bf16 v[26:29], v[158:161], v[174:177], v[26:29]
	v_mfma_f32_16x16x32_bf16 v[18:21], v[150:153], v[182:185], v[18:21]
	v_mfma_f32_16x16x32_bf16 v[10:13], v[158:161], v[182:185], v[10:13]
	v_mfma_f32_16x16x32_bf16 v[6:9], v[150:153], v[190:193], v[6:9]
	v_mfma_f32_16x16x32_bf16 v[2:5], v[158:161], v[190:193], v[2:5]
	s_setprio 0
	s_barrier
	s_branch .Lmid1440
.LBB0_1440:
	ds_read_b128 v[130:133], v234
	ds_read_b128 v[134:137], v234 offset:1024
	ds_read_b128 v[138:141], v234 offset:2048
	ds_read_b128 v[142:145], v234 offset:3072
	ds_read_b128 v[146:149], v235
	ds_read_b128 v[150:153], v235 offset:1024
	ds_read_b128 v[154:157], v235 offset:2048
	ds_read_b128 v[158:161], v235 offset:3072
	s_add_u32 s60, s58, 0x100
	s_addc_u32 s61, s59, 0
	s_cmp_eq_u32 s87, 12
	s_cselect_b32 s66, s33, s60
	s_cselect_b32 s67, s21, s61
	s_cselect_b32 s64, s84, s85
	s_cselect_b32 s65, s19, s86
	s_add_u32 s62, s66, 0x80
	s_addc_u32 s63, s67, 0
	ds_read_b128 v[162:165], v236
	ds_read_b128 v[166:169], v236 offset:1024
	ds_read_b128 v[170:173], v236 offset:2048
	ds_read_b128 v[174:177], v236 offset:3072
	ds_read_b128 v[178:181], v236 offset:4096
	ds_read_b128 v[182:185], v236 offset:5120
	ds_read_b128 v[186:189], v236 offset:6144
	ds_read_b128 v[190:193], v236 offset:7168
	s_add_u32 s58, s58, 0x40080
	s_addc_u32 s59, s59, 0
	s_mov_b32 s88, m0
	s_mov_b32 m0, s80
	s_nop 2
	global_load_lds_dwordx4 v228, s[58:59]
	s_mov_b32 m0, s88
	s_nop 0
	s_mov_b32 s88, m0
	s_mov_b32 m0, s81
	s_nop 2
	global_load_lds_dwordx4 v230, s[58:59]
	s_mov_b32 m0, s88
	s_waitcnt vmcnt(8)
	s_waitcnt lgkmcnt(0)
	s_barrier
	s_setprio 1
	v_mfma_f32_16x16x32_bf16 v[126:129], v[130:133], v[162:165], v[126:129]
	v_mfma_f32_16x16x32_bf16 v[122:125], v[138:141], v[162:165], v[122:125]
	v_mfma_f32_16x16x32_bf16 v[114:117], v[130:133], v[170:173], v[114:117]
	v_mfma_f32_16x16x32_bf16 v[106:109], v[138:141], v[170:173], v[106:109]
	v_mfma_f32_16x16x32_bf16 v[94:97], v[130:133], v[178:181], v[94:97]
	v_mfma_f32_16x16x32_bf16 v[90:93], v[138:141], v[178:181], v[90:93]
	v_mfma_f32_16x16x32_bf16 v[86:89], v[130:133], v[186:189], v[86:89]
	v_mfma_f32_16x16x32_bf16 v[78:81], v[138:141], v[186:189], v[78:81]
	v_mfma_f32_16x16x32_bf16 v[126:129], v[134:137], v[166:169], v[126:129]
	v_mfma_f32_16x16x32_bf16 v[122:125], v[142:145], v[166:169], v[122:125]
	v_mfma_f32_16x16x32_bf16 v[114:117], v[134:137], v[174:177], v[114:117]
	v_mfma_f32_16x16x32_bf16 v[106:109], v[142:145], v[174:177], v[106:109]
	v_mfma_f32_16x16x32_bf16 v[94:97], v[134:137], v[182:185], v[94:97]
	v_mfma_f32_16x16x32_bf16 v[90:93], v[142:145], v[182:185], v[90:93]
	v_mfma_f32_16x16x32_bf16 v[86:89], v[134:137], v[190:193], v[86:89]
	v_mfma_f32_16x16x32_bf16 v[78:81], v[142:145], v[190:193], v[78:81]
	s_setprio 0
	s_setprio 1
	v_mfma_f32_16x16x32_bf16 v[118:121], v[146:149], v[162:165], v[118:121]
	v_mfma_f32_16x16x32_bf16 v[110:113], v[154:157], v[162:165], v[110:113]
	v_mfma_f32_16x16x32_bf16 v[102:105], v[146:149], v[170:173], v[102:105]
	v_mfma_f32_16x16x32_bf16 v[98:101], v[154:157], v[170:173], v[98:101]
	v_mfma_f32_16x16x32_bf16 v[82:85], v[146:149], v[178:181], v[82:85]
	v_mfma_f32_16x16x32_bf16 v[74:77], v[154:157], v[178:181], v[74:77]
	v_mfma_f32_16x16x32_bf16 v[70:73], v[146:149], v[186:189], v[70:73]
	v_mfma_f32_16x16x32_bf16 v[66:69], v[154:157], v[186:189], v[66:69]
	v_mfma_f32_16x16x32_bf16 v[118:121], v[150:153], v[166:169], v[118:121]
	v_mfma_f32_16x16x32_bf16 v[110:113], v[158:161], v[166:169], v[110:113]
	v_mfma_f32_16x16x32_bf16 v[102:105], v[150:153], v[174:177], v[102:105]
	v_mfma_f32_16x16x32_bf16 v[98:101], v[158:161], v[174:177], v[98:101]
	v_mfma_f32_16x16x32_bf16 v[82:85], v[150:153], v[182:185], v[82:85]
	v_mfma_f32_16x16x32_bf16 v[74:77], v[158:161], v[182:185], v[74:77]
	v_mfma_f32_16x16x32_bf16 v[70:73], v[150:153], v[190:193], v[70:73]
	v_mfma_f32_16x16x32_bf16 v[66:69], v[158:161], v[190:193], v[66:69]
	s_setprio 0
	s_barrier
	ds_read_b128 v[162:165], v236 offset:16384
	ds_read_b128 v[166:169], v236 offset:17408
	ds_read_b128 v[170:173], v236 offset:18432
	ds_read_b128 v[174:177], v236 offset:19456
	ds_read_b128 v[178:181], v236 offset:20480
	ds_read_b128 v[182:185], v236 offset:21504
	ds_read_b128 v[186:189], v236 offset:22528
	ds_read_b128 v[190:193], v236 offset:23552
	s_mov_b32 s58, m0
	s_mov_b32 m0, s30
	s_nop 2
	global_load_lds_dwordx4 v229, s[64:65]
	s_mov_b32 m0, s58
	s_nop 0
	s_mov_b32 s58, m0
	s_mov_b32 m0, s31
	s_nop 2
	global_load_lds_dwordx4 v231, s[64:65]
	s_mov_b32 m0, s58
	s_add_u32 s58, s64, 0x40000
	s_addc_u32 s59, s65, 0
	s_mov_b32 s88, m0
	s_mov_b32 m0, s34
	s_nop 2
	global_load_lds_dwordx4 v229, s[58:59]
	s_mov_b32 m0, s88
	s_nop 0
	s_mov_b32 s88, m0
	s_mov_b32 m0, s35
	s_nop 2
	global_load_lds_dwordx4 v231, s[58:59]
	s_mov_b32 m0, s88
	s_mov_b32 s58, m0
	s_mov_b32 m0, s28
	s_nop 2
	global_load_lds_dwordx4 v228, s[66:67]
	s_mov_b32 m0, s58
	s_nop 0
	s_mov_b32 s58, m0
	s_mov_b32 m0, s36
	s_nop 2
	global_load_lds_dwordx4 v230, s[66:67]
	s_mov_b32 m0, s58
	s_waitcnt vmcnt(8)
	s_waitcnt lgkmcnt(0)
	s_barrier
	s_setprio 1
	v_mfma_f32_16x16x32_bf16 v[62:65], v[130:133], v[162:165], v[62:65]
	v_mfma_f32_16x16x32_bf16 v[58:61], v[138:141], v[162:165], v[58:61]
	v_mfma_f32_16x16x32_bf16 v[54:57], v[130:133], v[170:173], v[54:57]
	v_mfma_f32_16x16x32_bf16 v[46:49], v[138:141], v[170:173], v[46:49]
	v_mfma_f32_16x16x32_bf16 v[38:41], v[130:133], v[178:181], v[38:41]
	v_mfma_f32_16x16x32_bf16 v[30:33], v[138:141], v[178:181], v[30:33]
	v_mfma_f32_16x16x32_bf16 v[22:25], v[130:133], v[186:189], v[22:25]
	v_mfma_f32_16x16x32_bf16 v[14:17], v[138:141], v[186:189], v[14:17]
	v_mfma_f32_16x16x32_bf16 v[62:65], v[134:137], v[166:169], v[62:65]
	v_mfma_f32_16x16x32_bf16 v[58:61], v[142:145], v[166:169], v[58:61]
	v_mfma_f32_16x16x32_bf16 v[54:57], v[134:137], v[174:177], v[54:57]
	v_mfma_f32_16x16x32_bf16 v[46:49], v[142:145], v[174:177], v[46:49]
	v_mfma_f32_16x16x32_bf16 v[38:41], v[134:137], v[182:185], v[38:41]
	v_mfma_f32_16x16x32_bf16 v[30:33], v[142:145], v[182:185], v[30:33]
	v_mfma_f32_16x16x32_bf16 v[22:25], v[134:137], v[190:193], v[22:25]
	v_mfma_f32_16x16x32_bf16 v[14:17], v[142:145], v[190:193], v[14:17]
	s_setprio 0
	s_setprio 1
	v_mfma_f32_16x16x32_bf16 v[50:53], v[146:149], v[162:165], v[50:53]
	v_mfma_f32_16x16x32_bf16 v[42:45], v[154:157], v[162:165], v[42:45]
	v_mfma_f32_16x16x32_bf16 v[34:37], v[146:149], v[170:173], v[34:37]
	v_mfma_f32_16x16x32_bf16 v[26:29], v[154:157], v[170:173], v[26:29]
	v_mfma_f32_16x16x32_bf16 v[18:21], v[146:149], v[178:181], v[18:21]
	v_mfma_f32_16x16x32_bf16 v[10:13], v[154:157], v[178:181], v[10:13]
	v_mfma_f32_16x16x32_bf16 v[6:9], v[146:149], v[186:189], v[6:9]
	v_mfma_f32_16x16x32_bf16 v[2:5], v[154:157], v[186:189], v[2:5]
	v_mfma_f32_16x16x32_bf16 v[50:53], v[150:153], v[166:169], v[50:53]
	v_mfma_f32_16x16x32_bf16 v[42:45], v[158:161], v[166:169], v[42:45]
	v_mfma_f32_16x16x32_bf16 v[34:37], v[150:153], v[174:177], v[34:37]
	v_mfma_f32_16x16x32_bf16 v[26:29], v[158:161], v[174:177], v[26:29]
	v_mfma_f32_16x16x32_bf16 v[18:21], v[150:153], v[182:185], v[18:21]
	v_mfma_f32_16x16x32_bf16 v[10:13], v[158:161], v[182:185], v[10:13]
	v_mfma_f32_16x16x32_bf16 v[6:9], v[150:153], v[190:193], v[6:9]
	v_mfma_f32_16x16x32_bf16 v[2:5], v[158:161], v[190:193], v[2:5]
	s_setprio 0
	s_barrier
.Lmid1440:
	ds_read_b128 v[130:133], v237
	ds_read_b128 v[134:137], v237 offset:1024
	ds_read_b128 v[138:141], v237 offset:2048
	ds_read_b128 v[142:145], v237 offset:3072
	ds_read_b128 v[146:149], v238
	ds_read_b128 v[150:153], v238 offset:1024
	ds_read_b128 v[154:157], v238 offset:2048
	ds_read_b128 v[158:161], v238 offset:3072
	ds_read_b128 v[162:165], v236 offset:32768
	ds_read_b128 v[166:169], v236 offset:33792
	ds_read_b128 v[170:173], v236 offset:34816
	ds_read_b128 v[174:177], v236 offset:35840
	ds_read_b128 v[178:181], v236 offset:36864
	ds_read_b128 v[182:185], v236 offset:37888
	ds_read_b128 v[186:189], v236 offset:38912
	ds_read_b128 v[190:193], v236 offset:39936
	s_add_u32 s58, s66, 0x40000
	s_addc_u32 s59, s67, 0
	s_mov_b32 s66, m0
	s_mov_b32 m0, s37
	s_nop 2
	global_load_lds_dwordx4 v228, s[58:59]
	s_mov_b32 m0, s66
	s_nop 0
	s_mov_b32 s66, m0
	s_mov_b32 m0, s52
	s_nop 2
	global_load_lds_dwordx4 v230, s[58:59]
	s_mov_b32 m0, s66
	s_waitcnt vmcnt(8)
	s_waitcnt lgkmcnt(0)
	s_barrier
	s_setprio 1
	v_mfma_f32_16x16x32_bf16 v[126:129], v[130:133], v[162:165], v[126:129]
	v_mfma_f32_16x16x32_bf16 v[122:125], v[138:141], v[162:165], v[122:125]
	v_mfma_f32_16x16x32_bf16 v[114:117], v[130:133], v[170:173], v[114:117]
	v_mfma_f32_16x16x32_bf16 v[106:109], v[138:141], v[170:173], v[106:109]
	v_mfma_f32_16x16x32_bf16 v[94:97], v[130:133], v[178:181], v[94:97]
	v_mfma_f32_16x16x32_bf16 v[90:93], v[138:141], v[178:181], v[90:93]
	v_mfma_f32_16x16x32_bf16 v[86:89], v[130:133], v[186:189], v[86:89]
	v_mfma_f32_16x16x32_bf16 v[78:81], v[138:141], v[186:189], v[78:81]
	v_mfma_f32_16x16x32_bf16 v[126:129], v[134:137], v[166:169], v[126:129]
	v_mfma_f32_16x16x32_bf16 v[122:125], v[142:145], v[166:169], v[122:125]
	v_mfma_f32_16x16x32_bf16 v[114:117], v[134:137], v[174:177], v[114:117]
	v_mfma_f32_16x16x32_bf16 v[106:109], v[142:145], v[174:177], v[106:109]
	v_mfma_f32_16x16x32_bf16 v[94:97], v[134:137], v[182:185], v[94:97]
	v_mfma_f32_16x16x32_bf16 v[90:93], v[142:145], v[182:185], v[90:93]
	v_mfma_f32_16x16x32_bf16 v[86:89], v[134:137], v[190:193], v[86:89]
	v_mfma_f32_16x16x32_bf16 v[78:81], v[142:145], v[190:193], v[78:81]
	s_setprio 0
	s_setprio 1
	v_mfma_f32_16x16x32_bf16 v[118:121], v[146:149], v[162:165], v[118:121]
	v_mfma_f32_16x16x32_bf16 v[110:113], v[154:157], v[162:165], v[110:113]
	v_mfma_f32_16x16x32_bf16 v[102:105], v[146:149], v[170:173], v[102:105]
	v_mfma_f32_16x16x32_bf16 v[98:101], v[154:157], v[170:173], v[98:101]
	v_mfma_f32_16x16x32_bf16 v[82:85], v[146:149], v[178:181], v[82:85]
	v_mfma_f32_16x16x32_bf16 v[74:77], v[154:157], v[178:181], v[74:77]
	v_mfma_f32_16x16x32_bf16 v[70:73], v[146:149], v[186:189], v[70:73]
	v_mfma_f32_16x16x32_bf16 v[66:69], v[154:157], v[186:189], v[66:69]
	v_mfma_f32_16x16x32_bf16 v[118:121], v[150:153], v[166:169], v[118:121]
	v_mfma_f32_16x16x32_bf16 v[110:113], v[158:161], v[166:169], v[110:113]
	v_mfma_f32_16x16x32_bf16 v[102:105], v[150:153], v[174:177], v[102:105]
	v_mfma_f32_16x16x32_bf16 v[98:101], v[158:161], v[174:177], v[98:101]
	v_mfma_f32_16x16x32_bf16 v[82:85], v[150:153], v[182:185], v[82:85]
	v_mfma_f32_16x16x32_bf16 v[74:77], v[158:161], v[182:185], v[74:77]
	v_mfma_f32_16x16x32_bf16 v[70:73], v[150:153], v[190:193], v[70:73]
	v_mfma_f32_16x16x32_bf16 v[66:69], v[158:161], v[190:193], v[66:69]
	s_setprio 0
	s_barrier
	ds_read_b128 v[162:165], v236 offset:49152
	ds_read_b128 v[166:169], v236 offset:50176
	ds_read_b128 v[170:173], v236 offset:51200
	ds_read_b128 v[174:177], v236 offset:52224
	ds_read_b128 v[178:181], v236 offset:53248
	ds_read_b128 v[182:185], v236 offset:54272
	ds_read_b128 v[186:189], v236 offset:55296
	ds_read_b128 v[190:193], v236 offset:56320
	s_add_u32 s58, s64, 0x80
	s_addc_u32 s59, s65, 0
	s_mov_b32 s66, m0
	s_mov_b32 m0, s68
	s_nop 2
	global_load_lds_dwordx4 v229, s[58:59]
	s_mov_b32 m0, s66
	s_nop 0
	s_mov_b32 s66, m0
	s_mov_b32 m0, s69
	s_nop 2
	global_load_lds_dwordx4 v231, s[58:59]
	s_mov_b32 m0, s66
	s_add_u32 s58, s64, 0x40080
	s_addc_u32 s59, s65, 0
	s_mov_b32 s64, m0
	s_mov_b32 m0, s78
	s_nop 2
	global_load_lds_dwordx4 v229, s[58:59]
	s_mov_b32 m0, s64
	s_nop 0
	s_mov_b32 s64, m0
	s_mov_b32 m0, s79
	s_nop 2
	global_load_lds_dwordx4 v231, s[58:59]
	s_mov_b32 m0, s64
	s_mov_b32 s58, m0
	s_mov_b32 m0, s76
	s_nop 2
	global_load_lds_dwordx4 v228, s[62:63]
	s_mov_b32 m0, s58
	s_nop 0
	s_mov_b32 s58, m0
	s_mov_b32 m0, s77
	s_nop 2
	global_load_lds_dwordx4 v230, s[62:63]
	s_mov_b32 m0, s58
	s_waitcnt vmcnt(8)
	s_waitcnt lgkmcnt(0)
	s_barrier
	s_setprio 1
	v_mfma_f32_16x16x32_bf16 v[62:65], v[130:133], v[162:165], v[62:65]
	v_mfma_f32_16x16x32_bf16 v[58:61], v[138:141], v[162:165], v[58:61]
	v_mfma_f32_16x16x32_bf16 v[54:57], v[130:133], v[170:173], v[54:57]
	v_mfma_f32_16x16x32_bf16 v[46:49], v[138:141], v[170:173], v[46:49]
	v_mfma_f32_16x16x32_bf16 v[38:41], v[130:133], v[178:181], v[38:41]
	v_mfma_f32_16x16x32_bf16 v[30:33], v[138:141], v[178:181], v[30:33]
	v_mfma_f32_16x16x32_bf16 v[22:25], v[130:133], v[186:189], v[22:25]
	v_mfma_f32_16x16x32_bf16 v[14:17], v[138:141], v[186:189], v[14:17]
	v_mfma_f32_16x16x32_bf16 v[62:65], v[134:137], v[166:169], v[62:65]
	v_mfma_f32_16x16x32_bf16 v[58:61], v[142:145], v[166:169], v[58:61]
	v_mfma_f32_16x16x32_bf16 v[54:57], v[134:137], v[174:177], v[54:57]
	v_mfma_f32_16x16x32_bf16 v[46:49], v[142:145], v[174:177], v[46:49]
	v_mfma_f32_16x16x32_bf16 v[38:41], v[134:137], v[182:185], v[38:41]
	v_mfma_f32_16x16x32_bf16 v[30:33], v[142:145], v[182:185], v[30:33]
	v_mfma_f32_16x16x32_bf16 v[22:25], v[134:137], v[190:193], v[22:25]
	v_mfma_f32_16x16x32_bf16 v[14:17], v[142:145], v[190:193], v[14:17]
	s_setprio 0
	s_setprio 1
	v_mfma_f32_16x16x32_bf16 v[50:53], v[146:149], v[162:165], v[50:53]
	v_mfma_f32_16x16x32_bf16 v[42:45], v[154:157], v[162:165], v[42:45]
	v_mfma_f32_16x16x32_bf16 v[34:37], v[146:149], v[170:173], v[34:37]
	v_mfma_f32_16x16x32_bf16 v[26:29], v[154:157], v[170:173], v[26:29]
	v_mfma_f32_16x16x32_bf16 v[18:21], v[146:149], v[178:181], v[18:21]
	v_mfma_f32_16x16x32_bf16 v[10:13], v[154:157], v[178:181], v[10:13]
	v_mfma_f32_16x16x32_bf16 v[6:9], v[146:149], v[186:189], v[6:9]
	v_mfma_f32_16x16x32_bf16 v[2:5], v[154:157], v[186:189], v[2:5]
	v_mfma_f32_16x16x32_bf16 v[50:53], v[150:153], v[166:169], v[50:53]
	v_mfma_f32_16x16x32_bf16 v[42:45], v[158:161], v[166:169], v[42:45]
	v_mfma_f32_16x16x32_bf16 v[34:37], v[150:153], v[174:177], v[34:37]
	v_mfma_f32_16x16x32_bf16 v[26:29], v[158:161], v[174:177], v[26:29]
	v_mfma_f32_16x16x32_bf16 v[18:21], v[150:153], v[182:185], v[18:21]
	v_mfma_f32_16x16x32_bf16 v[10:13], v[158:161], v[182:185], v[10:13]
	v_mfma_f32_16x16x32_bf16 v[6:9], v[150:153], v[190:193], v[6:9]
	v_mfma_f32_16x16x32_bf16 v[2:5], v[158:161], v[190:193], v[2:5]
	s_setprio 0
	s_barrier
	s_add_i32 s87, s87, 2
	s_add_u32 s85, s85, 0x100
	s_addc_u32 s86, s86, 0
	s_cmp_gt_u32 s87, 13
	s_mov_b64 s[58:59], s[60:61]
	s_cbranch_scc0 .LBB0_1440
	s_and_b64 vcc, exec, s[16:17]
	s_cbranch_vccz .LBB0_1443
	s_barrier

.LBB0_1896:
	s_cmp_eq_u32 s40, 0
	s_cbranch_scc1 .Lpeel6
	s_add_u32 s33, s74, s40
	s_addc_u32 s44, s75, s41
	s_add_u32 s56, s33, 0x1d800080
	s_addc_u32 s57, s44, 0
	s_add_u32 s33, s33, 0x1d800100
	s_addc_u32 s52, s44, 0
	v_add_u32_e32 v2, 0x10000, v173
	v_add_u32_e32 v14, 0x14000, v173
	s_and_b64 s[44:45], s[42:43], exec
	ds_read_b128 v[18:21], v2
	ds_read_b128 v[22:25], v2 offset:1024
	ds_read_b128 v[26:29], v2 offset:2048
	ds_read_b128 v[30:33], v2 offset:3072
	ds_read_b128 v[2:5], v14
	ds_read_b128 v[6:9], v14 offset:1024
	ds_read_b128 v[10:13], v14 offset:2048
	ds_read_b128 v[14:17], v14 offset:3072
	s_cselect_b32 s55, s11, s52
	s_cselect_b32 s54, s10, s33
	s_add_u32 s33, s2, s40
	s_addc_u32 s44, s23, s41
	s_and_b64 s[42:43], s[42:43], exec
	s_cselect_b32 s43, s39, s44
	s_cselect_b32 s42, s38, s33
	s_add_u32 s44, s54, 0x80
	s_addc_u32 s45, s55, 0
	s_add_u32 s52, s42, 0x80
	s_addc_u32 s53, s43, 0
	ds_read_b128 v[180:183], v174
	ds_read_b128 v[184:187], v174 offset:1024
	ds_read_b128 v[188:191], v174 offset:2048
	ds_read_b128 v[192:195], v174 offset:3072
	ds_read_b128 v[196:199], v174 offset:4096
	ds_read_b128 v[200:203], v174 offset:5120
	ds_read_b128 v[204:207], v174 offset:6144
	ds_read_b128 v[208:211], v174 offset:7168
	s_mov_b32 s33, m0
	s_mov_b32 m0, s93
	s_nop 2
	global_load_lds_dwordx4 v178, s[56:57]
	s_mov_b32 m0, s33
	s_nop 0
	s_mov_b32 s33, m0
	s_mov_b32 m0, s94
	s_nop 2
	global_load_lds_dwordx4 v177, s[56:57]
	s_mov_b32 m0, s33
	s_waitcnt vmcnt(8)
	s_waitcnt lgkmcnt(0)
	s_barrier
	s_setprio 1
	v_mfma_f32_16x16x128_f8f6f4 v[158:161], v[18:25], v[180:187], v[158:161]
	v_mfma_f32_16x16x128_f8f6f4 v[154:157], v[26:33], v[180:187], v[154:157]
	v_mfma_f32_16x16x128_f8f6f4 v[150:153], v[18:25], v[188:195], v[150:153]
	v_mfma_f32_16x16x128_f8f6f4 v[146:149], v[26:33], v[188:195], v[146:149]
	v_mfma_f32_16x16x128_f8f6f4 v[142:145], v[18:25], v[196:203], v[142:145]
	v_mfma_f32_16x16x128_f8f6f4 v[138:141], v[26:33], v[196:203], v[138:141]
	v_mfma_f32_16x16x128_f8f6f4 v[134:137], v[18:25], v[204:211], v[134:137]
	v_mfma_f32_16x16x128_f8f6f4 v[130:133], v[26:33], v[204:211], v[130:133]
	s_setprio 0
	s_setprio 1
	v_mfma_f32_16x16x128_f8f6f4 v[126:129], v[2:9], v[180:187], v[126:129]
	v_mfma_f32_16x16x128_f8f6f4 v[122:125], v[10:17], v[180:187], v[122:125]
	v_mfma_f32_16x16x128_f8f6f4 v[118:121], v[2:9], v[188:195], v[118:121]
	v_mfma_f32_16x16x128_f8f6f4 v[114:117], v[10:17], v[188:195], v[114:117]
	v_mfma_f32_16x16x128_f8f6f4 v[110:113], v[2:9], v[196:203], v[110:113]
	v_mfma_f32_16x16x128_f8f6f4 v[106:109], v[10:17], v[196:203], v[106:109]
	v_mfma_f32_16x16x128_f8f6f4 v[102:105], v[2:9], v[204:211], v[102:105]
	v_mfma_f32_16x16x128_f8f6f4 v[98:101], v[10:17], v[204:211], v[98:101]
	s_setprio 0
	s_barrier
	ds_read_b128 v[180:183], v174 offset:16384
	ds_read_b128 v[184:187], v174 offset:17408
	ds_read_b128 v[188:191], v174 offset:18432
	ds_read_b128 v[192:195], v174 offset:19456
	ds_read_b128 v[196:199], v174 offset:20480
	ds_read_b128 v[200:203], v174 offset:21504
	ds_read_b128 v[204:207], v174 offset:22528
	ds_read_b128 v[208:211], v174 offset:23552
	s_mov_b32 s33, m0
	s_mov_b32 m0, s67
	s_nop 2
	global_load_lds_dwordx4 v1, s[42:43]
	s_mov_b32 m0, s33
	s_add_u32 s56, s42, 0x20000
	s_mov_b32 s33, m0
	s_mov_b32 m0, s68
	s_nop 2
	global_load_lds_dwordx4 v163, s[42:43]
	s_mov_b32 m0, s33
	s_addc_u32 s57, s43, 0
	s_mov_b32 s33, m0
	s_mov_b32 m0, s69
	s_nop 2
	global_load_lds_dwordx4 v1, s[56:57]
	s_mov_b32 m0, s33
	s_nop 0
	s_mov_b32 s33, m0
	s_mov_b32 m0, s76
	s_nop 2
	global_load_lds_dwordx4 v163, s[56:57]
	s_mov_b32 m0, s33
	s_nop 0
	s_mov_b32 s33, m0
	s_mov_b32 m0, s15
	s_nop 2
	global_load_lds_dwordx4 v168, s[54:55]
	s_mov_b32 m0, s33
	s_nop 0
	s_mov_b32 s33, m0
	s_mov_b32 m0, s79
	s_nop 2
	global_load_lds_dwordx4 v172, s[54:55]
	s_mov_b32 m0, s33
	s_waitcnt vmcnt(8)
	s_waitcnt lgkmcnt(0)
	s_barrier
	s_setprio 1
	v_mfma_f32_16x16x128_f8f6f4 v[94:97], v[18:25], v[180:187], v[94:97]
	v_mfma_f32_16x16x128_f8f6f4 v[90:93], v[26:33], v[180:187], v[90:93]
	v_mfma_f32_16x16x128_f8f6f4 v[86:89], v[18:25], v[188:195], v[86:89]
	v_mfma_f32_16x16x128_f8f6f4 v[82:85], v[26:33], v[188:195], v[82:85]
	v_mfma_f32_16x16x128_f8f6f4 v[78:81], v[18:25], v[196:203], v[78:81]
	v_mfma_f32_16x16x128_f8f6f4 v[74:77], v[26:33], v[196:203], v[74:77]
	v_mfma_f32_16x16x128_f8f6f4 v[70:73], v[18:25], v[204:211], v[70:73]
	v_mfma_f32_16x16x128_f8f6f4 v[66:69], v[26:33], v[204:211], v[66:69]
	s_setprio 0
	s_setprio 1
	v_mfma_f32_16x16x128_f8f6f4 v[62:65], v[2:9], v[180:187], v[62:65]
	v_mfma_f32_16x16x128_f8f6f4 v[58:61], v[10:17], v[180:187], v[58:61]
	v_mfma_f32_16x16x128_f8f6f4 v[54:57], v[2:9], v[188:195], v[54:57]
	v_mfma_f32_16x16x128_f8f6f4 v[50:53], v[10:17], v[188:195], v[50:53]
	v_mfma_f32_16x16x128_f8f6f4 v[46:49], v[2:9], v[196:203], v[46:49]
	v_mfma_f32_16x16x128_f8f6f4 v[42:45], v[10:17], v[196:203], v[42:45]
	v_mfma_f32_16x16x128_f8f6f4 v[38:41], v[2:9], v[204:211], v[38:41]
	v_mfma_f32_16x16x128_f8f6f4 v[34:37], v[10:17], v[204:211], v[34:37]
	s_setprio 0
	s_barrier
.Lmid6:
	v_add_u32_e32 v14, 0x18000, v173
	v_add_u32_e32 v30, 0x1c000, v173
	ds_read_b128 v[2:5], v14
	ds_read_b128 v[6:9], v14 offset:1024
	ds_read_b128 v[10:13], v14 offset:2048
	ds_read_b128 v[14:17], v14 offset:3072
	ds_read_b128 v[18:21], v30
	ds_read_b128 v[22:25], v30 offset:1024
	ds_read_b128 v[26:29], v30 offset:2048
	ds_read_b128 v[30:33], v30 offset:3072
	ds_read_b128 v[180:183], v174 offset:32768
	ds_read_b128 v[184:187], v174 offset:33792
	ds_read_b128 v[188:191], v174 offset:34816
	ds_read_b128 v[192:195], v174 offset:35840
	ds_read_b128 v[196:199], v174 offset:36864
	ds_read_b128 v[200:203], v174 offset:37888
	ds_read_b128 v[204:207], v174 offset:38912
	ds_read_b128 v[208:211], v174 offset:39936
	s_mov_b32 s33, m0
	s_mov_b32 m0, s80
	s_nop 2
	global_load_lds_dwordx4 v169, s[54:55]
	s_mov_b32 m0, s33
	s_nop 0
	s_mov_b32 s33, m0
	s_mov_b32 m0, s81
	s_nop 2
	global_load_lds_dwordx4 v175, s[54:55]
	s_mov_b32 m0, s33
	s_waitcnt vmcnt(8)
	s_waitcnt lgkmcnt(0)
	s_barrier
	s_setprio 1
	v_mfma_f32_16x16x128_f8f6f4 v[158:161], v[2:9], v[180:187], v[158:161]
	v_mfma_f32_16x16x128_f8f6f4 v[154:157], v[10:17], v[180:187], v[154:157]
	v_mfma_f32_16x16x128_f8f6f4 v[150:153], v[2:9], v[188:195], v[150:153]
	v_mfma_f32_16x16x128_f8f6f4 v[146:149], v[10:17], v[188:195], v[146:149]
	v_mfma_f32_16x16x128_f8f6f4 v[142:145], v[2:9], v[196:203], v[142:145]
	v_mfma_f32_16x16x128_f8f6f4 v[138:141], v[10:17], v[196:203], v[138:141]
	v_mfma_f32_16x16x128_f8f6f4 v[134:137], v[2:9], v[204:211], v[134:137]
	v_mfma_f32_16x16x128_f8f6f4 v[130:133], v[10:17], v[204:211], v[130:133]
	s_setprio 0
	s_setprio 1
	v_mfma_f32_16x16x128_f8f6f4 v[126:129], v[18:25], v[180:187], v[126:129]
	v_mfma_f32_16x16x128_f8f6f4 v[122:125], v[26:33], v[180:187], v[122:125]
	v_mfma_f32_16x16x128_f8f6f4 v[118:121], v[18:25], v[188:195], v[118:121]
	v_mfma_f32_16x16x128_f8f6f4 v[114:117], v[26:33], v[188:195], v[114:117]
	v_mfma_f32_16x16x128_f8f6f4 v[110:113], v[18:25], v[196:203], v[110:113]
	v_mfma_f32_16x16x128_f8f6f4 v[106:109], v[26:33], v[196:203], v[106:109]
	v_mfma_f32_16x16x128_f8f6f4 v[102:105], v[18:25], v[204:211], v[102:105]
	v_mfma_f32_16x16x128_f8f6f4 v[98:101], v[26:33], v[204:211], v[98:101]
	s_setprio 0
	s_barrier
	ds_read_b128 v[180:183], v174 offset:49152
	ds_read_b128 v[184:187], v174 offset:50176
	ds_read_b128 v[188:191], v174 offset:51200
	ds_read_b128 v[192:195], v174 offset:52224
	ds_read_b128 v[196:199], v174 offset:53248
	ds_read_b128 v[200:203], v174 offset:54272
	ds_read_b128 v[204:207], v174 offset:55296
	ds_read_b128 v[208:211], v174 offset:56320
	s_mov_b32 s33, m0
	s_mov_b32 m0, s84
	s_nop 2
	global_load_lds_dwordx4 v1, s[52:53]
	s_mov_b32 m0, s33
	s_add_u32 s42, s42, 0x20080
	s_mov_b32 s33, m0
	s_mov_b32 m0, s85
	s_nop 2
	global_load_lds_dwordx4 v163, s[52:53]
	s_mov_b32 m0, s33
	s_addc_u32 s43, s43, 0
	s_mov_b32 s33, m0
	s_mov_b32 m0, s91
	s_nop 2
	global_load_lds_dwordx4 v1, s[42:43]
	s_mov_b32 m0, s33
	s_nop 0
	s_mov_b32 s33, m0
	s_mov_b32 m0, s92
	s_nop 2
	global_load_lds_dwordx4 v163, s[42:43]
	s_mov_b32 m0, s33
	s_nop 0
	s_mov_b32 s33, m0
	s_mov_b32 m0, s86
	s_nop 2
	global_load_lds_dwordx4 v168, s[44:45]
	s_mov_b32 m0, s33
	s_nop 0
	s_mov_b32 s33, m0
	s_mov_b32 m0, s87
	s_nop 2
	global_load_lds_dwordx4 v172, s[44:45]
	s_mov_b32 m0, s33
	s_waitcnt vmcnt(8)
	s_waitcnt lgkmcnt(0)
	s_barrier
	s_setprio 1
	v_mfma_f32_16x16x128_f8f6f4 v[94:97], v[2:9], v[180:187], v[94:97]
	v_mfma_f32_16x16x128_f8f6f4 v[90:93], v[10:17], v[180:187], v[90:93]
	v_mfma_f32_16x16x128_f8f6f4 v[86:89], v[2:9], v[188:195], v[86:89]
	v_mfma_f32_16x16x128_f8f6f4 v[82:85], v[10:17], v[188:195], v[82:85]
	v_mfma_f32_16x16x128_f8f6f4 v[78:81], v[2:9], v[196:203], v[78:81]
	v_mfma_f32_16x16x128_f8f6f4 v[74:77], v[10:17], v[196:203], v[74:77]
	v_mfma_f32_16x16x128_f8f6f4 v[70:73], v[2:9], v[204:211], v[70:73]
	v_mfma_f32_16x16x128_f8f6f4 v[66:69], v[10:17], v[204:211], v[66:69]
	s_setprio 0
	s_setprio 1
	v_mfma_f32_16x16x128_f8f6f4 v[62:65], v[18:25], v[180:187], v[62:65]
	v_mfma_f32_16x16x128_f8f6f4 v[58:61], v[26:33], v[180:187], v[58:61]
	v_mfma_f32_16x16x128_f8f6f4 v[54:57], v[18:25], v[188:195], v[54:57]
	v_mfma_f32_16x16x128_f8f6f4 v[50:53], v[26:33], v[188:195], v[50:53]
	v_mfma_f32_16x16x128_f8f6f4 v[46:49], v[18:25], v[196:203], v[46:49]
	v_mfma_f32_16x16x128_f8f6f4 v[42:45], v[26:33], v[196:203], v[42:45]
	v_mfma_f32_16x16x128_f8f6f4 v[38:41], v[18:25], v[204:211], v[38:41]
	v_mfma_f32_16x16x128_f8f6f4 v[34:37], v[26:33], v[204:211], v[34:37]
	s_setprio 0
	s_cmp_lt_i32 s9, 4
	s_cbranch_scc1 .Lkb6_do
	s_cmp_lg_u64 s[16:17], 0
	s_cbranch_scc0 .Lkb6_skip

.Lpeel6:
	s_add_u32 s33, s74, s40
	s_addc_u32 s44, s75, s41
	s_add_u32 s56, s33, 0x1d800080
	s_addc_u32 s57, s44, 0
	s_add_u32 s33, s33, 0x1d800100
	s_addc_u32 s52, s44, 0
	v_add_u32_e32 v2, 0x10000, v173
	v_add_u32_e32 v14, 0x14000, v173
	s_and_b64 s[44:45], s[42:43], exec
	ds_read_b128 v[18:21], v2
	ds_read_b128 v[22:25], v2 offset:1024
	ds_read_b128 v[26:29], v2 offset:2048
	ds_read_b128 v[30:33], v2 offset:3072
	ds_read_b128 v[2:5], v14
	ds_read_b128 v[6:9], v14 offset:1024
	ds_read_b128 v[10:13], v14 offset:2048
	ds_read_b128 v[14:17], v14 offset:3072
	s_cselect_b32 s55, s11, s52
	s_cselect_b32 s54, s10, s33
	s_add_u32 s33, s2, s40
	s_addc_u32 s44, s23, s41
	s_and_b64 s[42:43], s[42:43], exec
	s_cselect_b32 s43, s39, s44
	s_cselect_b32 s42, s38, s33
	s_add_u32 s44, s54, 0x80
	s_addc_u32 s45, s55, 0
	s_add_u32 s52, s42, 0x80
	s_addc_u32 s53, s43, 0
	ds_read_b128 v[180:183], v174
	ds_read_b128 v[184:187], v174 offset:1024
	ds_read_b128 v[188:191], v174 offset:2048
	ds_read_b128 v[192:195], v174 offset:3072
	ds_read_b128 v[196:199], v174 offset:4096
	ds_read_b128 v[200:203], v174 offset:5120
	ds_read_b128 v[204:207], v174 offset:6144
	ds_read_b128 v[208:211], v174 offset:7168
	s_mov_b32 s33, m0
	s_mov_b32 m0, s93
	s_nop 2
	global_load_lds_dwordx4 v178, s[56:57]
	s_mov_b32 m0, s33
	s_nop 0
	s_mov_b32 s33, m0
	s_mov_b32 m0, s94
	s_nop 2
	global_load_lds_dwordx4 v177, s[56:57]
	s_mov_b32 m0, s33
	s_waitcnt vmcnt(8)
	s_waitcnt lgkmcnt(0)
	s_barrier
	s_setprio 1
	v_mfma_f32_16x16x128_f8f6f4 v[158:161], v[18:25], v[180:187], 0
	v_mfma_f32_16x16x128_f8f6f4 v[154:157], v[26:33], v[180:187], 0
	v_mfma_f32_16x16x128_f8f6f4 v[150:153], v[18:25], v[188:195], 0
	v_mfma_f32_16x16x128_f8f6f4 v[146:149], v[26:33], v[188:195], 0
	v_mfma_f32_16x16x128_f8f6f4 v[142:145], v[18:25], v[196:203], 0
	v_mfma_f32_16x16x128_f8f6f4 v[138:141], v[26:33], v[196:203], 0
	v_mfma_f32_16x16x128_f8f6f4 v[134:137], v[18:25], v[204:211], 0
	v_mfma_f32_16x16x128_f8f6f4 v[130:133], v[26:33], v[204:211], 0
	s_setprio 0
	s_setprio 1
	v_mfma_f32_16x16x128_f8f6f4 v[126:129], v[2:9], v[180:187], 0
	v_mfma_f32_16x16x128_f8f6f4 v[122:125], v[10:17], v[180:187], 0
	v_mfma_f32_16x16x128_f8f6f4 v[118:121], v[2:9], v[188:195], 0
	v_mfma_f32_16x16x128_f8f6f4 v[114:117], v[10:17], v[188:195], 0
	v_mfma_f32_16x16x128_f8f6f4 v[110:113], v[2:9], v[196:203], 0
	v_mfma_f32_16x16x128_f8f6f4 v[106:109], v[10:17], v[196:203], 0
	v_mfma_f32_16x16x128_f8f6f4 v[102:105], v[2:9], v[204:211], 0
	v_mfma_f32_16x16x128_f8f6f4 v[98:101], v[10:17], v[204:211], 0
	s_setprio 0
	s_barrier
	ds_read_b128 v[180:183], v174 offset:16384
	ds_read_b128 v[184:187], v174 offset:17408
	ds_read_b128 v[188:191], v174 offset:18432
	ds_read_b128 v[192:195], v174 offset:19456
	ds_read_b128 v[196:199], v174 offset:20480
	ds_read_b128 v[200:203], v174 offset:21504
	ds_read_b128 v[204:207], v174 offset:22528
	ds_read_b128 v[208:211], v174 offset:23552
	s_mov_b32 s33, m0
	s_mov_b32 m0, s67
	s_nop 2
	global_load_lds_dwordx4 v1, s[42:43]
	s_mov_b32 m0, s33
	s_add_u32 s56, s42, 0x20000
	s_mov_b32 s33, m0
	s_mov_b32 m0, s68
	s_nop 2
	global_load_lds_dwordx4 v163, s[42:43]
	s_mov_b32 m0, s33
	s_addc_u32 s57, s43, 0
	s_mov_b32 s33, m0
	s_mov_b32 m0, s69
	s_nop 2
	global_load_lds_dwordx4 v1, s[56:57]
	s_mov_b32 m0, s33
	s_nop 0
	s_mov_b32 s33, m0
	s_mov_b32 m0, s76
	s_nop 2
	global_load_lds_dwordx4 v163, s[56:57]
	s_mov_b32 m0, s33
	s_nop 0
	s_mov_b32 s33, m0
	s_mov_b32 m0, s15
	s_nop 2
	global_load_lds_dwordx4 v168, s[54:55]
	s_mov_b32 m0, s33
	s_nop 0
	s_mov_b32 s33, m0
	s_mov_b32 m0, s79
	s_nop 2
	global_load_lds_dwordx4 v172, s[54:55]
	s_mov_b32 m0, s33
	s_waitcnt vmcnt(8)
	s_waitcnt lgkmcnt(0)
	s_barrier
	s_setprio 1
	v_mfma_f32_16x16x128_f8f6f4 v[94:97], v[18:25], v[180:187], 0
	v_mfma_f32_16x16x128_f8f6f4 v[90:93], v[26:33], v[180:187], 0
	v_mfma_f32_16x16x128_f8f6f4 v[86:89], v[18:25], v[188:195], 0
	v_mfma_f32_16x16x128_f8f6f4 v[82:85], v[26:33], v[188:195], 0
	v_mfma_f32_16x16x128_f8f6f4 v[78:81], v[18:25], v[196:203], 0
	v_mfma_f32_16x16x128_f8f6f4 v[74:77], v[26:33], v[196:203], 0
	v_mfma_f32_16x16x128_f8f6f4 v[70:73], v[18:25], v[204:211], 0
	v_mfma_f32_16x16x128_f8f6f4 v[66:69], v[26:33], v[204:211], 0
	s_setprio 0
	s_setprio 1
	v_mfma_f32_16x16x128_f8f6f4 v[62:65], v[2:9], v[180:187], 0
	v_mfma_f32_16x16x128_f8f6f4 v[58:61], v[10:17], v[180:187], 0
	v_mfma_f32_16x16x128_f8f6f4 v[54:57], v[2:9], v[188:195], 0
	v_mfma_f32_16x16x128_f8f6f4 v[50:53], v[10:17], v[188:195], 0
	v_mfma_f32_16x16x128_f8f6f4 v[46:49], v[2:9], v[196:203], 0
	v_mfma_f32_16x16x128_f8f6f4 v[42:45], v[10:17], v[196:203], 0
	v_mfma_f32_16x16x128_f8f6f4 v[38:41], v[2:9], v[204:211], 0
	v_mfma_f32_16x16x128_f8f6f4 v[34:37], v[10:17], v[204:211], 0
	s_setprio 0
	s_barrier
	s_branch .Lmid6

.LBB0_1943:
	s_add_u32 s54, s38, 0x80
	s_addc_u32 s55, s39, 0
	v_add_u32_e32 v2, 0x10000, v174
	v_add_u32_e32 v14, 0x14000, v174
	s_add_u32 s38, s38, 0x100
	ds_read_b128 v[18:21], v2
	ds_read_b128 v[22:25], v2 offset:1024
	ds_read_b128 v[26:29], v2 offset:2048
	ds_read_b128 v[30:33], v2 offset:3072
	ds_read_b128 v[2:5], v14
	ds_read_b128 v[6:9], v14 offset:1024
	ds_read_b128 v[10:13], v14 offset:2048
	ds_read_b128 v[14:17], v14 offset:3072
	s_addc_u32 s39, s39, 0
	s_and_b64 s[40:41], s[40:41], exec
	s_cselect_b32 s52, s10, s38
	s_cselect_b32 s53, s11, s39
	s_cselect_b32 s41, s1, s87
	s_cselect_b32 s40, s0, s86
	s_add_u32 s42, s52, 0x80
	s_addc_u32 s43, s53, 0
	s_add_u32 s44, s40, 0x80
	s_addc_u32 s45, s41, 0
	ds_read_b128 v[180:183], v175
	ds_read_b128 v[184:187], v175 offset:1024
	ds_read_b128 v[188:191], v175 offset:2048
	ds_read_b128 v[192:195], v175 offset:3072
	ds_read_b128 v[196:199], v175 offset:4096
	ds_read_b128 v[200:203], v175 offset:5120
	ds_read_b128 v[204:207], v175 offset:6144
	ds_read_b128 v[208:211], v175 offset:7168
	s_mov_b32 s33, m0
	s_mov_b32 m0, s78
	s_nop 2
	global_load_lds_dwordx4 v164, s[54:55]
	s_mov_b32 m0, s33
	s_nop 0
	s_mov_b32 s33, m0
	s_mov_b32 m0, s79
	s_nop 2
	global_load_lds_dwordx4 v166, s[54:55]
	s_mov_b32 m0, s33
	s_waitcnt vmcnt(8)
	s_waitcnt lgkmcnt(0)
	s_barrier
	s_setprio 1
	v_mfma_f32_16x16x128_f8f6f4 v[158:161], v[18:25], v[180:187], v[158:161]
	v_mfma_f32_16x16x128_f8f6f4 v[150:153], v[26:33], v[180:187], v[150:153]
	v_mfma_f32_16x16x128_f8f6f4 v[142:145], v[18:25], v[188:195], v[142:145]
	v_mfma_f32_16x16x128_f8f6f4 v[134:137], v[26:33], v[188:195], v[134:137]
	v_mfma_f32_16x16x128_f8f6f4 v[126:129], v[18:25], v[196:203], v[126:129]
	v_mfma_f32_16x16x128_f8f6f4 v[118:121], v[26:33], v[196:203], v[118:121]
	v_mfma_f32_16x16x128_f8f6f4 v[110:113], v[18:25], v[204:211], v[110:113]
	v_mfma_f32_16x16x128_f8f6f4 v[102:105], v[26:33], v[204:211], v[102:105]
	s_setprio 0
	s_setprio 1
	v_mfma_f32_16x16x128_f8f6f4 v[154:157], v[2:9], v[180:187], v[154:157]
	v_mfma_f32_16x16x128_f8f6f4 v[146:149], v[10:17], v[180:187], v[146:149]
	v_mfma_f32_16x16x128_f8f6f4 v[138:141], v[2:9], v[188:195], v[138:141]
	v_mfma_f32_16x16x128_f8f6f4 v[130:133], v[10:17], v[188:195], v[130:133]
	v_mfma_f32_16x16x128_f8f6f4 v[122:125], v[2:9], v[196:203], v[122:125]
	v_mfma_f32_16x16x128_f8f6f4 v[114:117], v[10:17], v[196:203], v[114:117]
	v_mfma_f32_16x16x128_f8f6f4 v[106:109], v[2:9], v[204:211], v[106:109]
	v_mfma_f32_16x16x128_f8f6f4 v[98:101], v[10:17], v[204:211], v[98:101]
	s_setprio 0
	s_barrier
	ds_read_b128 v[180:183], v175 offset:16384
	ds_read_b128 v[184:187], v175 offset:17408
	ds_read_b128 v[188:191], v175 offset:18432
	ds_read_b128 v[192:195], v175 offset:19456
	ds_read_b128 v[196:199], v175 offset:20480
	ds_read_b128 v[200:203], v175 offset:21504
	ds_read_b128 v[204:207], v175 offset:22528
	ds_read_b128 v[208:211], v175 offset:23552
	s_mov_b32 s33, m0
	s_mov_b32 m0, s34
	s_nop 2
	global_load_lds_dwordx4 v165, s[40:41]
	s_mov_b32 m0, s33
	s_add_u32 s54, s40, 0x20000
	s_mov_b32 s33, m0
	s_mov_b32 m0, s35
	s_nop 2
	global_load_lds_dwordx4 v167, s[40:41]
	s_mov_b32 m0, s33
	s_addc_u32 s55, s41, 0
	s_mov_b32 s33, m0
	s_mov_b32 m0, s36
	s_nop 2
	global_load_lds_dwordx4 v165, s[54:55]
	s_mov_b32 m0, s33
	s_nop 0
	s_mov_b32 s33, m0
	s_mov_b32 m0, s37
	s_nop 2
	global_load_lds_dwordx4 v167, s[54:55]
	s_mov_b32 m0, s33
	s_nop 0
	s_mov_b32 s33, m0
	s_mov_b32 m0, s31
	s_nop 2
	global_load_lds_dwordx4 v171, s[52:53]
	s_mov_b32 m0, s33
	s_nop 0
	s_mov_b32 s33, m0
	s_mov_b32 m0, s56
	s_nop 2
	global_load_lds_dwordx4 v173, s[52:53]
	s_mov_b32 m0, s33
	s_waitcnt vmcnt(8)
	s_waitcnt lgkmcnt(0)
	s_barrier
	s_setprio 1
	v_mfma_f32_16x16x128_f8f6f4 v[94:97], v[18:25], v[180:187], v[94:97]
	v_mfma_f32_16x16x128_f8f6f4 v[86:89], v[26:33], v[180:187], v[86:89]
	v_mfma_f32_16x16x128_f8f6f4 v[78:81], v[18:25], v[188:195], v[78:81]
	v_mfma_f32_16x16x128_f8f6f4 v[70:73], v[26:33], v[188:195], v[70:73]
	v_mfma_f32_16x16x128_f8f6f4 v[62:65], v[18:25], v[196:203], v[62:65]
	v_mfma_f32_16x16x128_f8f6f4 v[54:57], v[26:33], v[196:203], v[54:57]
	v_mfma_f32_16x16x128_f8f6f4 v[46:49], v[18:25], v[204:211], v[46:49]
	v_mfma_f32_16x16x128_f8f6f4 v[38:41], v[26:33], v[204:211], v[38:41]
	s_setprio 0
	s_setprio 1
	v_mfma_f32_16x16x128_f8f6f4 v[90:93], v[2:9], v[180:187], v[90:93]
	v_mfma_f32_16x16x128_f8f6f4 v[82:85], v[10:17], v[180:187], v[82:85]
	v_mfma_f32_16x16x128_f8f6f4 v[74:77], v[2:9], v[188:195], v[74:77]
	v_mfma_f32_16x16x128_f8f6f4 v[66:69], v[10:17], v[188:195], v[66:69]
	v_mfma_f32_16x16x128_f8f6f4 v[58:61], v[2:9], v[196:203], v[58:61]
	v_mfma_f32_16x16x128_f8f6f4 v[50:53], v[10:17], v[196:203], v[50:53]
	v_mfma_f32_16x16x128_f8f6f4 v[42:45], v[2:9], v[204:211], v[42:45]
	v_mfma_f32_16x16x128_f8f6f4 v[34:37], v[10:17], v[204:211], v[34:37]
	s_setprio 0
	s_barrier
	v_add_u32_e32 v14, 0x18000, v174
	v_add_u32_e32 v30, 0x1c000, v174
	ds_read_b128 v[2:5], v14
	ds_read_b128 v[6:9], v14 offset:1024
	ds_read_b128 v[10:13], v14 offset:2048
	ds_read_b128 v[14:17], v14 offset:3072
	ds_read_b128 v[18:21], v30
	ds_read_b128 v[22:25], v30 offset:1024
	ds_read_b128 v[26:29], v30 offset:2048
	ds_read_b128 v[30:33], v30 offset:3072
	ds_read_b128 v[180:183], v175 offset:32768
	ds_read_b128 v[184:187], v175 offset:33792
	ds_read_b128 v[188:191], v175 offset:34816
	ds_read_b128 v[192:195], v175 offset:35840
	ds_read_b128 v[196:199], v175 offset:36864
	ds_read_b128 v[200:203], v175 offset:37888
	ds_read_b128 v[204:207], v175 offset:38912
	ds_read_b128 v[208:211], v175 offset:39936
	s_mov_b32 s33, m0
	s_mov_b32 m0, s57
	s_nop 2
	global_load_lds_dwordx4 v177, s[52:53]
	s_mov_b32 m0, s33
	s_nop 0
	s_mov_b32 s33, m0
	s_mov_b32 m0, s63
	s_nop 2
	global_load_lds_dwordx4 v178, s[52:53]
	s_mov_b32 m0, s33
	s_waitcnt vmcnt(8)
	s_waitcnt lgkmcnt(0)
	s_barrier
	s_setprio 1
	v_mfma_f32_16x16x128_f8f6f4 v[158:161], v[2:9], v[180:187], v[158:161]
	v_mfma_f32_16x16x128_f8f6f4 v[150:153], v[10:17], v[180:187], v[150:153]
	v_mfma_f32_16x16x128_f8f6f4 v[142:145], v[2:9], v[188:195], v[142:145]
	v_mfma_f32_16x16x128_f8f6f4 v[134:137], v[10:17], v[188:195], v[134:137]
	v_mfma_f32_16x16x128_f8f6f4 v[126:129], v[2:9], v[196:203], v[126:129]
	v_mfma_f32_16x16x128_f8f6f4 v[118:121], v[10:17], v[196:203], v[118:121]
	v_mfma_f32_16x16x128_f8f6f4 v[110:113], v[2:9], v[204:211], v[110:113]
	v_mfma_f32_16x16x128_f8f6f4 v[102:105], v[10:17], v[204:211], v[102:105]
	s_setprio 0
	s_setprio 1
	v_mfma_f32_16x16x128_f8f6f4 v[154:157], v[18:25], v[180:187], v[154:157]
	v_mfma_f32_16x16x128_f8f6f4 v[146:149], v[26:33], v[180:187], v[146:149]
	v_mfma_f32_16x16x128_f8f6f4 v[138:141], v[18:25], v[188:195], v[138:141]
	v_mfma_f32_16x16x128_f8f6f4 v[130:133], v[26:33], v[188:195], v[130:133]
	v_mfma_f32_16x16x128_f8f6f4 v[122:125], v[18:25], v[196:203], v[122:125]
	v_mfma_f32_16x16x128_f8f6f4 v[114:117], v[26:33], v[196:203], v[114:117]
	v_mfma_f32_16x16x128_f8f6f4 v[106:109], v[18:25], v[204:211], v[106:109]
	v_mfma_f32_16x16x128_f8f6f4 v[98:101], v[26:33], v[204:211], v[98:101]
	s_setprio 0
	s_barrier
	ds_read_b128 v[180:183], v175 offset:49152
	ds_read_b128 v[184:187], v175 offset:50176
	ds_read_b128 v[188:191], v175 offset:51200
	ds_read_b128 v[192:195], v175 offset:52224
	ds_read_b128 v[196:199], v175 offset:53248
	ds_read_b128 v[200:203], v175 offset:54272
	ds_read_b128 v[204:207], v175 offset:55296
	ds_read_b128 v[208:211], v175 offset:56320
	s_mov_b32 s33, m0
	s_mov_b32 m0, s66
	s_nop 2
	global_load_lds_dwordx4 v165, s[44:45]
	s_mov_b32 m0, s33
	s_add_u32 s40, s40, 0x20080
	s_mov_b32 s33, m0
	s_mov_b32 m0, s67
	s_nop 2
	global_load_lds_dwordx4 v167, s[44:45]
	s_mov_b32 m0, s33
	s_addc_u32 s41, s41, 0
	s_mov_b32 s33, m0
	s_mov_b32 m0, s76
	s_nop 2
	global_load_lds_dwordx4 v165, s[40:41]
	s_mov_b32 m0, s33
	s_nop 0
	s_mov_b32 s33, m0
	s_mov_b32 m0, s77
	s_nop 2
	global_load_lds_dwordx4 v167, s[40:41]
	s_mov_b32 m0, s33
	s_nop 0
	s_mov_b32 s33, m0
	s_mov_b32 m0, s68
	s_nop 2
	global_load_lds_dwordx4 v171, s[42:43]
	s_mov_b32 m0, s33
	s_nop 0
	s_mov_b32 s33, m0
	s_mov_b32 m0, s69
	s_nop 2
	global_load_lds_dwordx4 v173, s[42:43]
	s_mov_b32 m0, s33
	s_waitcnt vmcnt(8)
	s_waitcnt lgkmcnt(0)
	s_barrier
	s_setprio 1
	v_mfma_f32_16x16x128_f8f6f4 v[94:97], v[2:9], v[180:187], v[94:97]
	v_mfma_f32_16x16x128_f8f6f4 v[86:89], v[10:17], v[180:187], v[86:89]
	v_mfma_f32_16x16x128_f8f6f4 v[78:81], v[2:9], v[188:195], v[78:81]
	v_mfma_f32_16x16x128_f8f6f4 v[70:73], v[10:17], v[188:195], v[70:73]
	v_mfma_f32_16x16x128_f8f6f4 v[62:65], v[2:9], v[196:203], v[62:65]
	v_mfma_f32_16x16x128_f8f6f4 v[54:57], v[10:17], v[196:203], v[54:57]
	v_mfma_f32_16x16x128_f8f6f4 v[46:49], v[2:9], v[204:211], v[46:49]
	v_mfma_f32_16x16x128_f8f6f4 v[38:41], v[10:17], v[204:211], v[38:41]
	s_setprio 0
	s_setprio 1
	v_mfma_f32_16x16x128_f8f6f4 v[90:93], v[18:25], v[180:187], v[90:93]
	v_mfma_f32_16x16x128_f8f6f4 v[82:85], v[26:33], v[180:187], v[82:85]
	v_mfma_f32_16x16x128_f8f6f4 v[74:77], v[18:25], v[188:195], v[74:77]
	v_mfma_f32_16x16x128_f8f6f4 v[66:69], v[26:33], v[188:195], v[66:69]
	v_mfma_f32_16x16x128_f8f6f4 v[58:61], v[18:25], v[196:203], v[58:61]
	v_mfma_f32_16x16x128_f8f6f4 v[50:53], v[26:33], v[196:203], v[50:53]
	v_mfma_f32_16x16x128_f8f6f4 v[42:45], v[18:25], v[204:211], v[42:45]
	v_mfma_f32_16x16x128_f8f6f4 v[34:37], v[26:33], v[204:211], v[34:37]
	s_setprio 0
	s_barrier
	s_add_i32 s88, s88, 2
	s_add_u32 s86, s86, 0x100
	s_addc_u32 s87, s87, 0
	s_cmp_gt_u32 s88, 5
	s_cbranch_scc1 .LBB0_1957

.LBB0_2092:
	s_cmp_eq_u32 s91, 0
	s_cbranch_scc1 .Lpeel7
	s_lshl_b32 s33, s91, 7
	s_add_u32 s52, s36, s33
	s_addc_u32 s53, s37, 0
	s_add_u32 s46, s52, 0x100
	s_addc_u32 s47, s53, 0
	s_and_b64 s[44:45], s[42:43], exec
	s_cselect_b32 s49, s15, s47
	s_cselect_b32 s48, s17, s46
	s_add_u32 s33, s26, s33
	v_add_u32_e32 v2, 0x10000, v171
	v_add_u32_e32 v14, 0x14000, v171
	s_addc_u32 s44, s27, 0
	ds_read_b128 v[18:21], v2
	ds_read_b128 v[22:25], v2 offset:1024
	ds_read_b128 v[26:29], v2 offset:2048
	ds_read_b128 v[30:33], v2 offset:3072
	ds_read_b128 v[2:5], v14
	ds_read_b128 v[6:9], v14 offset:1024
	ds_read_b128 v[10:13], v14 offset:2048
	ds_read_b128 v[14:17], v14 offset:3072
	s_add_u32 s33, s33, 0x100
	s_addc_u32 s44, s44, 0
	s_and_b64 s[42:43], s[42:43], exec
	s_cselect_b32 s43, s19, s44
	s_cselect_b32 s42, s18, s33
	s_add_u32 s44, s48, 0x80
	s_addc_u32 s45, s49, 0
	s_add_u32 s46, s42, 0x80
	s_addc_u32 s47, s43, 0
	ds_read_b128 v[176:179], v172
	ds_read_b128 v[180:183], v172 offset:1024
	ds_read_b128 v[184:187], v172 offset:2048
	ds_read_b128 v[188:191], v172 offset:3072
	ds_read_b128 v[192:195], v172 offset:4096
	ds_read_b128 v[196:199], v172 offset:5120
	ds_read_b128 v[200:203], v172 offset:6144
	ds_read_b128 v[204:207], v172 offset:7168
	s_add_u32 s52, s52, 0x20080
	s_addc_u32 s53, s53, 0
	s_mov_b32 s33, m0
	s_mov_b32 m0, s79
	s_nop 2
	global_load_lds_dwordx4 v163, s[52:53]
	s_mov_b32 m0, s33
	s_nop 0
	s_mov_b32 s33, m0
	s_mov_b32 m0, s80
	s_nop 2
	global_load_lds_dwordx4 v164, s[52:53]
	s_mov_b32 m0, s33
	s_waitcnt vmcnt(8)
	s_waitcnt lgkmcnt(0)
	s_barrier
	s_setprio 1
	v_mfma_f32_16x16x128_f8f6f4 v[158:161], v[18:25], v[176:183], v[158:161]
	v_mfma_f32_16x16x128_f8f6f4 v[154:157], v[26:33], v[176:183], v[154:157]
	v_mfma_f32_16x16x128_f8f6f4 v[142:145], v[18:25], v[184:191], v[142:145]
	v_mfma_f32_16x16x128_f8f6f4 v[138:141], v[26:33], v[184:191], v[138:141]
	v_mfma_f32_16x16x128_f8f6f4 v[126:129], v[18:25], v[192:199], v[126:129]
	v_mfma_f32_16x16x128_f8f6f4 v[122:125], v[26:33], v[192:199], v[122:125]
	v_mfma_f32_16x16x128_f8f6f4 v[110:113], v[18:25], v[200:207], v[110:113]
	v_mfma_f32_16x16x128_f8f6f4 v[106:109], v[26:33], v[200:207], v[106:109]
	s_setprio 0
	s_setprio 1
	v_mfma_f32_16x16x128_f8f6f4 v[150:153], v[2:9], v[176:183], v[150:153]
	v_mfma_f32_16x16x128_f8f6f4 v[146:149], v[10:17], v[176:183], v[146:149]
	v_mfma_f32_16x16x128_f8f6f4 v[134:137], v[2:9], v[184:191], v[134:137]
	v_mfma_f32_16x16x128_f8f6f4 v[130:133], v[10:17], v[184:191], v[130:133]
	v_mfma_f32_16x16x128_f8f6f4 v[118:121], v[2:9], v[192:199], v[118:121]
	v_mfma_f32_16x16x128_f8f6f4 v[114:117], v[10:17], v[192:199], v[114:117]
	v_mfma_f32_16x16x128_f8f6f4 v[102:105], v[2:9], v[200:207], v[102:105]
	v_mfma_f32_16x16x128_f8f6f4 v[98:101], v[10:17], v[200:207], v[98:101]
	s_setprio 0
	s_barrier
	ds_read_b128 v[176:179], v172 offset:16384
	ds_read_b128 v[180:183], v172 offset:17408
	ds_read_b128 v[184:187], v172 offset:18432
	ds_read_b128 v[188:191], v172 offset:19456
	ds_read_b128 v[192:195], v172 offset:20480
	ds_read_b128 v[196:199], v172 offset:21504
	ds_read_b128 v[200:203], v172 offset:22528
	ds_read_b128 v[204:207], v172 offset:23552
	s_mov_b32 s33, m0
	s_mov_b32 m0, s64
	s_nop 2
	global_load_lds_dwordx4 v1, s[42:43]
	s_mov_b32 m0, s33
	s_add_u32 s52, s42, 0x20000
	s_mov_b32 s33, m0
	s_mov_b32 m0, s65
	s_nop 2
	global_load_lds_dwordx4 v162, s[42:43]
	s_mov_b32 m0, s33
	s_addc_u32 s53, s43, 0
	s_mov_b32 s33, m0
	s_mov_b32 m0, s24
	s_nop 2
	global_load_lds_dwordx4 v1, s[52:53]
	s_mov_b32 m0, s33
	s_nop 0
	s_mov_b32 s33, m0
	s_mov_b32 m0, s25
	s_nop 2
	global_load_lds_dwordx4 v162, s[52:53]
	s_mov_b32 m0, s33
	s_nop 0
	s_mov_b32 s33, m0
	s_mov_b32 m0, s63
	s_nop 2
	global_load_lds_dwordx4 v163, s[48:49]
	s_mov_b32 m0, s33
	s_nop 0
	s_mov_b32 s33, m0
	s_mov_b32 m0, s2
	s_nop 2
	global_load_lds_dwordx4 v164, s[48:49]
	s_mov_b32 m0, s33
	s_waitcnt vmcnt(8)
	s_waitcnt lgkmcnt(0)
	s_barrier
	s_setprio 1
	v_mfma_f32_16x16x128_f8f6f4 v[94:97], v[18:25], v[176:183], v[94:97]
	v_mfma_f32_16x16x128_f8f6f4 v[90:93], v[26:33], v[176:183], v[90:93]
	v_mfma_f32_16x16x128_f8f6f4 v[78:81], v[18:25], v[184:191], v[78:81]
	v_mfma_f32_16x16x128_f8f6f4 v[74:77], v[26:33], v[184:191], v[74:77]
	v_mfma_f32_16x16x128_f8f6f4 v[62:65], v[18:25], v[192:199], v[62:65]
	v_mfma_f32_16x16x128_f8f6f4 v[58:61], v[26:33], v[192:199], v[58:61]
	v_mfma_f32_16x16x128_f8f6f4 v[46:49], v[18:25], v[200:207], v[46:49]
	v_mfma_f32_16x16x128_f8f6f4 v[42:45], v[26:33], v[200:207], v[42:45]
	s_setprio 0
	s_setprio 1
	v_mfma_f32_16x16x128_f8f6f4 v[86:89], v[2:9], v[176:183], v[86:89]
	v_mfma_f32_16x16x128_f8f6f4 v[82:85], v[10:17], v[176:183], v[82:85]
	v_mfma_f32_16x16x128_f8f6f4 v[70:73], v[2:9], v[184:191], v[70:73]
	v_mfma_f32_16x16x128_f8f6f4 v[66:69], v[10:17], v[184:191], v[66:69]
	v_mfma_f32_16x16x128_f8f6f4 v[54:57], v[2:9], v[192:199], v[54:57]
	v_mfma_f32_16x16x128_f8f6f4 v[50:53], v[10:17], v[192:199], v[50:53]
	v_mfma_f32_16x16x128_f8f6f4 v[38:41], v[2:9], v[200:207], v[38:41]
	v_mfma_f32_16x16x128_f8f6f4 v[34:37], v[10:17], v[200:207], v[34:37]
	s_setprio 0
	s_barrier
.Lmid7:
	v_add_u32_e32 v14, 0x18000, v171
	v_add_u32_e32 v30, 0x1c000, v171
	ds_read_b128 v[2:5], v14
	ds_read_b128 v[6:9], v14 offset:1024
	ds_read_b128 v[10:13], v14 offset:2048
	ds_read_b128 v[14:17], v14 offset:3072
	ds_read_b128 v[18:21], v30
	ds_read_b128 v[22:25], v30 offset:1024
	ds_read_b128 v[26:29], v30 offset:2048
	ds_read_b128 v[30:33], v30 offset:3072
	ds_read_b128 v[176:179], v172 offset:32768
	ds_read_b128 v[180:183], v172 offset:33792
	ds_read_b128 v[184:187], v172 offset:34816
	ds_read_b128 v[188:191], v172 offset:35840
	ds_read_b128 v[192:195], v172 offset:36864
	ds_read_b128 v[196:199], v172 offset:37888
	ds_read_b128 v[200:203], v172 offset:38912
	ds_read_b128 v[204:207], v172 offset:39936
	s_add_u32 s48, s48, 0x20000
	s_addc_u32 s49, s49, 0
	s_mov_b32 s33, m0
	s_mov_b32 m0, s23
	s_nop 2
	global_load_lds_dwordx4 v163, s[48:49]
	s_mov_b32 m0, s33
	s_nop 0
	s_mov_b32 s33, m0
	s_mov_b32 m0, s28
	s_nop 2
	global_load_lds_dwordx4 v164, s[48:49]
	s_mov_b32 m0, s33
	s_waitcnt vmcnt(8)
	s_waitcnt lgkmcnt(0)
	s_barrier
	s_setprio 1
	v_mfma_f32_16x16x128_f8f6f4 v[158:161], v[2:9], v[176:183], v[158:161]
	v_mfma_f32_16x16x128_f8f6f4 v[154:157], v[10:17], v[176:183], v[154:157]
	v_mfma_f32_16x16x128_f8f6f4 v[142:145], v[2:9], v[184:191], v[142:145]
	v_mfma_f32_16x16x128_f8f6f4 v[138:141], v[10:17], v[184:191], v[138:141]
	v_mfma_f32_16x16x128_f8f6f4 v[126:129], v[2:9], v[192:199], v[126:129]
	v_mfma_f32_16x16x128_f8f6f4 v[122:125], v[10:17], v[192:199], v[122:125]
	v_mfma_f32_16x16x128_f8f6f4 v[110:113], v[2:9], v[200:207], v[110:113]
	v_mfma_f32_16x16x128_f8f6f4 v[106:109], v[10:17], v[200:207], v[106:109]
	s_setprio 0
	s_setprio 1
	v_mfma_f32_16x16x128_f8f6f4 v[150:153], v[18:25], v[176:183], v[150:153]
	v_mfma_f32_16x16x128_f8f6f4 v[146:149], v[26:33], v[176:183], v[146:149]
	v_mfma_f32_16x16x128_f8f6f4 v[134:137], v[18:25], v[184:191], v[134:137]
	v_mfma_f32_16x16x128_f8f6f4 v[130:133], v[26:33], v[184:191], v[130:133]
	v_mfma_f32_16x16x128_f8f6f4 v[118:121], v[18:25], v[192:199], v[118:121]
	v_mfma_f32_16x16x128_f8f6f4 v[114:117], v[26:33], v[192:199], v[114:117]
	v_mfma_f32_16x16x128_f8f6f4 v[102:105], v[18:25], v[200:207], v[102:105]
	v_mfma_f32_16x16x128_f8f6f4 v[98:101], v[26:33], v[200:207], v[98:101]
	s_setprio 0
	s_barrier
	ds_read_b128 v[176:179], v172 offset:49152
	ds_read_b128 v[180:183], v172 offset:50176
	ds_read_b128 v[184:187], v172 offset:51200
	ds_read_b128 v[188:191], v172 offset:52224
	ds_read_b128 v[192:195], v172 offset:53248
	ds_read_b128 v[196:199], v172 offset:54272
	ds_read_b128 v[200:203], v172 offset:55296
	ds_read_b128 v[204:207], v172 offset:56320
	s_mov_b32 s33, m0
	s_mov_b32 m0, s67
	s_nop 2
	global_load_lds_dwordx4 v1, s[46:47]
	s_mov_b32 m0, s33
	s_add_u32 s42, s42, 0x20080
	s_mov_b32 s33, m0
	s_mov_b32 m0, s68
	s_nop 2
	global_load_lds_dwordx4 v162, s[46:47]
	s_mov_b32 m0, s33
	s_addc_u32 s43, s43, 0
	s_mov_b32 s33, m0
	s_mov_b32 m0, s77
	s_nop 2
	global_load_lds_dwordx4 v1, s[42:43]
	s_mov_b32 m0, s33
	s_nop 0
	s_mov_b32 s33, m0
	s_mov_b32 m0, s78
	s_nop 2
	global_load_lds_dwordx4 v162, s[42:43]
	s_mov_b32 m0, s33
	s_nop 0
	s_mov_b32 s33, m0
	s_mov_b32 m0, s69
	s_nop 2
	global_load_lds_dwordx4 v163, s[44:45]
	s_mov_b32 m0, s33
	s_nop 0
	s_mov_b32 s33, m0
	s_mov_b32 m0, s76
	s_nop 2
	global_load_lds_dwordx4 v164, s[44:45]
	s_mov_b32 m0, s33
	s_waitcnt vmcnt(8)
	s_waitcnt lgkmcnt(0)
	s_barrier
	s_setprio 1
	v_mfma_f32_16x16x128_f8f6f4 v[94:97], v[2:9], v[176:183], v[94:97]
	v_mfma_f32_16x16x128_f8f6f4 v[90:93], v[10:17], v[176:183], v[90:93]
	v_mfma_f32_16x16x128_f8f6f4 v[78:81], v[2:9], v[184:191], v[78:81]
	v_mfma_f32_16x16x128_f8f6f4 v[74:77], v[10:17], v[184:191], v[74:77]
	v_mfma_f32_16x16x128_f8f6f4 v[62:65], v[2:9], v[192:199], v[62:65]
	v_mfma_f32_16x16x128_f8f6f4 v[58:61], v[10:17], v[192:199], v[58:61]
	v_mfma_f32_16x16x128_f8f6f4 v[46:49], v[2:9], v[200:207], v[46:49]
	v_mfma_f32_16x16x128_f8f6f4 v[42:45], v[10:17], v[200:207], v[42:45]
	s_setprio 0
	s_setprio 1
	v_mfma_f32_16x16x128_f8f6f4 v[86:89], v[18:25], v[176:183], v[86:89]
	v_mfma_f32_16x16x128_f8f6f4 v[82:85], v[26:33], v[176:183], v[82:85]
	v_mfma_f32_16x16x128_f8f6f4 v[70:73], v[18:25], v[184:191], v[70:73]
	v_mfma_f32_16x16x128_f8f6f4 v[66:69], v[26:33], v[184:191], v[66:69]
	v_mfma_f32_16x16x128_f8f6f4 v[54:57], v[18:25], v[192:199], v[54:57]
	v_mfma_f32_16x16x128_f8f6f4 v[50:53], v[26:33], v[192:199], v[50:53]
	v_mfma_f32_16x16x128_f8f6f4 v[38:41], v[18:25], v[200:207], v[38:41]
	v_mfma_f32_16x16x128_f8f6f4 v[34:37], v[26:33], v[200:207], v[34:37]
	s_setprio 0
	s_cmp_lt_u32 s91, 6
	s_cbranch_scc1 .Lkb7_do
	s_cmp_lg_u64 s[12:13], 0
	s_cbranch_scc0 .Lkb7_skip

.Lpeel7:
	s_lshl_b32 s33, s91, 7
	s_add_u32 s52, s36, s33
	s_addc_u32 s53, s37, 0
	s_add_u32 s46, s52, 0x100
	s_addc_u32 s47, s53, 0
	s_and_b64 s[44:45], s[42:43], exec
	s_cselect_b32 s49, s15, s47
	s_cselect_b32 s48, s17, s46
	s_add_u32 s33, s26, s33
	v_add_u32_e32 v2, 0x10000, v171
	v_add_u32_e32 v14, 0x14000, v171
	s_addc_u32 s44, s27, 0
	ds_read_b128 v[18:21], v2
	ds_read_b128 v[22:25], v2 offset:1024
	ds_read_b128 v[26:29], v2 offset:2048
	ds_read_b128 v[30:33], v2 offset:3072
	ds_read_b128 v[2:5], v14
	ds_read_b128 v[6:9], v14 offset:1024
	ds_read_b128 v[10:13], v14 offset:2048
	ds_read_b128 v[14:17], v14 offset:3072
	s_add_u32 s33, s33, 0x100
	s_addc_u32 s44, s44, 0
	s_and_b64 s[42:43], s[42:43], exec
	s_cselect_b32 s43, s19, s44
	s_cselect_b32 s42, s18, s33
	s_add_u32 s44, s48, 0x80
	s_addc_u32 s45, s49, 0
	s_add_u32 s46, s42, 0x80
	s_addc_u32 s47, s43, 0
	ds_read_b128 v[176:179], v172
	ds_read_b128 v[180:183], v172 offset:1024
	ds_read_b128 v[184:187], v172 offset:2048
	ds_read_b128 v[188:191], v172 offset:3072
	ds_read_b128 v[192:195], v172 offset:4096
	ds_read_b128 v[196:199], v172 offset:5120
	ds_read_b128 v[200:203], v172 offset:6144
	ds_read_b128 v[204:207], v172 offset:7168
	s_add_u32 s52, s52, 0x20080
	s_addc_u32 s53, s53, 0
	s_mov_b32 s33, m0
	s_mov_b32 m0, s79
	s_nop 2
	global_load_lds_dwordx4 v163, s[52:53]
	s_mov_b32 m0, s33
	s_nop 0
	s_mov_b32 s33, m0
	s_mov_b32 m0, s80
	s_nop 2
	global_load_lds_dwordx4 v164, s[52:53]
	s_mov_b32 m0, s33
	s_waitcnt vmcnt(8)
	s_waitcnt lgkmcnt(0)
	s_barrier
	s_setprio 1
	v_mfma_f32_16x16x128_f8f6f4 v[158:161], v[18:25], v[176:183], 0
	v_mfma_f32_16x16x128_f8f6f4 v[154:157], v[26:33], v[176:183], 0
	v_mfma_f32_16x16x128_f8f6f4 v[142:145], v[18:25], v[184:191], 0
	v_mfma_f32_16x16x128_f8f6f4 v[138:141], v[26:33], v[184:191], 0
	v_mfma_f32_16x16x128_f8f6f4 v[126:129], v[18:25], v[192:199], 0
	v_mfma_f32_16x16x128_f8f6f4 v[122:125], v[26:33], v[192:199], 0
	v_mfma_f32_16x16x128_f8f6f4 v[110:113], v[18:25], v[200:207], 0
	v_mfma_f32_16x16x128_f8f6f4 v[106:109], v[26:33], v[200:207], 0
	s_setprio 0
	s_setprio 1
	v_mfma_f32_16x16x128_f8f6f4 v[150:153], v[2:9], v[176:183], 0
	v_mfma_f32_16x16x128_f8f6f4 v[146:149], v[10:17], v[176:183], 0
	v_mfma_f32_16x16x128_f8f6f4 v[134:137], v[2:9], v[184:191], 0
	v_mfma_f32_16x16x128_f8f6f4 v[130:133], v[10:17], v[184:191], 0
	v_mfma_f32_16x16x128_f8f6f4 v[118:121], v[2:9], v[192:199], 0
	v_mfma_f32_16x16x128_f8f6f4 v[114:117], v[10:17], v[192:199], 0
	v_mfma_f32_16x16x128_f8f6f4 v[102:105], v[2:9], v[200:207], 0
	v_mfma_f32_16x16x128_f8f6f4 v[98:101], v[10:17], v[200:207], 0
	s_setprio 0
	s_barrier
	ds_read_b128 v[176:179], v172 offset:16384
	ds_read_b128 v[180:183], v172 offset:17408
	ds_read_b128 v[184:187], v172 offset:18432
	ds_read_b128 v[188:191], v172 offset:19456
	ds_read_b128 v[192:195], v172 offset:20480
	ds_read_b128 v[196:199], v172 offset:21504
	ds_read_b128 v[200:203], v172 offset:22528
	ds_read_b128 v[204:207], v172 offset:23552
	s_mov_b32 s33, m0
	s_mov_b32 m0, s64
	s_nop 2
	global_load_lds_dwordx4 v1, s[42:43]
	s_mov_b32 m0, s33
	s_add_u32 s52, s42, 0x20000
	s_mov_b32 s33, m0
	s_mov_b32 m0, s65
	s_nop 2
	global_load_lds_dwordx4 v162, s[42:43]
	s_mov_b32 m0, s33
	s_addc_u32 s53, s43, 0
	s_mov_b32 s33, m0
	s_mov_b32 m0, s24
	s_nop 2
	global_load_lds_dwordx4 v1, s[52:53]
	s_mov_b32 m0, s33
	s_nop 0
	s_mov_b32 s33, m0
	s_mov_b32 m0, s25
	s_nop 2
	global_load_lds_dwordx4 v162, s[52:53]
	s_mov_b32 m0, s33
	s_nop 0
	s_mov_b32 s33, m0
	s_mov_b32 m0, s63
	s_nop 2
	global_load_lds_dwordx4 v163, s[48:49]
	s_mov_b32 m0, s33
	s_nop 0
	s_mov_b32 s33, m0
	s_mov_b32 m0, s2
	s_nop 2
	global_load_lds_dwordx4 v164, s[48:49]
	s_mov_b32 m0, s33
	s_waitcnt vmcnt(8)
	s_waitcnt lgkmcnt(0)
	s_barrier
	s_setprio 1
	v_mfma_f32_16x16x128_f8f6f4 v[94:97], v[18:25], v[176:183], 0
	v_mfma_f32_16x16x128_f8f6f4 v[90:93], v[26:33], v[176:183], 0
	v_mfma_f32_16x16x128_f8f6f4 v[78:81], v[18:25], v[184:191], 0
	v_mfma_f32_16x16x128_f8f6f4 v[74:77], v[26:33], v[184:191], 0
	v_mfma_f32_16x16x128_f8f6f4 v[62:65], v[18:25], v[192:199], 0
	v_mfma_f32_16x16x128_f8f6f4 v[58:61], v[26:33], v[192:199], 0
	v_mfma_f32_16x16x128_f8f6f4 v[46:49], v[18:25], v[200:207], 0
	v_mfma_f32_16x16x128_f8f6f4 v[42:45], v[26:33], v[200:207], 0
	s_setprio 0
	s_setprio 1
	v_mfma_f32_16x16x128_f8f6f4 v[86:89], v[2:9], v[176:183], 0
	v_mfma_f32_16x16x128_f8f6f4 v[82:85], v[10:17], v[176:183], 0
	v_mfma_f32_16x16x128_f8f6f4 v[70:73], v[2:9], v[184:191], 0
	v_mfma_f32_16x16x128_f8f6f4 v[66:69], v[10:17], v[184:191], 0
	v_mfma_f32_16x16x128_f8f6f4 v[54:57], v[2:9], v[192:199], 0
	v_mfma_f32_16x16x128_f8f6f4 v[50:53], v[10:17], v[192:199], 0
	v_mfma_f32_16x16x128_f8f6f4 v[38:41], v[2:9], v[200:207], 0
	v_mfma_f32_16x16x128_f8f6f4 v[34:37], v[10:17], v[200:207], 0
	s_setprio 0
	s_barrier
	s_branch .Lmid7

.LBB0_2128:
	v_add_u32_e32 v0, 0x10000, v169
	v_add_u32_e32 v12, 0x14000, v169
	s_add_u32 s26, s22, 0x100
	ds_read_b128 v[16:19], v0
	ds_read_b128 v[20:23], v0 offset:1024
	ds_read_b128 v[24:27], v0 offset:2048
	ds_read_b128 v[28:31], v0 offset:3072
	ds_read_b128 v[0:3], v12
	ds_read_b128 v[4:7], v12 offset:1024
	ds_read_b128 v[8:11], v12 offset:2048
	ds_read_b128 v[12:15], v12 offset:3072
	s_addc_u32 s27, s23, 0
	s_cmp_eq_u32 s83, 4
	s_cselect_b32 s42, s15, s26
	s_cselect_b32 s43, s13, s27
	s_cselect_b32 s37, s17, s82
	s_cselect_b32 s36, s16, s81
	s_add_u32 s38, s42, 0x80
	s_addc_u32 s39, s43, 0
	s_add_u32 s40, s36, 0x80
	s_addc_u32 s41, s37, 0
	ds_read_b128 v[172:175], v170
	ds_read_b128 v[176:179], v170 offset:1024
	ds_read_b128 v[180:183], v170 offset:2048
	ds_read_b128 v[184:187], v170 offset:3072
	ds_read_b128 v[188:191], v170 offset:4096
	ds_read_b128 v[192:195], v170 offset:5120
	ds_read_b128 v[196:199], v170 offset:6144
	ds_read_b128 v[200:203], v170 offset:7168
	s_add_u32 s22, s22, 0x20080
	s_addc_u32 s23, s23, 0
	s_mov_b32 s33, m0
	s_mov_b32 m0, s64
	s_nop 2
	global_load_lds_dwordx4 v162, s[22:23]
	s_mov_b32 m0, s33
	s_nop 0
	s_mov_b32 s33, m0
	s_mov_b32 m0, s65
	s_nop 2
	global_load_lds_dwordx4 v164, s[22:23]
	s_mov_b32 m0, s33
	s_waitcnt vmcnt(8)
	s_waitcnt lgkmcnt(0)
	s_barrier
	s_setprio 1
	v_mfma_f32_16x16x128_f8f6f4 v[156:159], v[16:23], v[172:179], v[156:159]
	v_mfma_f32_16x16x128_f8f6f4 v[152:155], v[24:31], v[172:179], v[152:155]
	v_mfma_f32_16x16x128_f8f6f4 v[140:143], v[16:23], v[180:187], v[140:143]
	v_mfma_f32_16x16x128_f8f6f4 v[136:139], v[24:31], v[180:187], v[136:139]
	v_mfma_f32_16x16x128_f8f6f4 v[124:127], v[16:23], v[188:195], v[124:127]
	v_mfma_f32_16x16x128_f8f6f4 v[120:123], v[24:31], v[188:195], v[120:123]
	v_mfma_f32_16x16x128_f8f6f4 v[108:111], v[16:23], v[196:203], v[108:111]
	v_mfma_f32_16x16x128_f8f6f4 v[104:107], v[24:31], v[196:203], v[104:107]
	s_setprio 0
	s_setprio 1
	v_mfma_f32_16x16x128_f8f6f4 v[148:151], v[0:7], v[172:179], v[148:151]
	v_mfma_f32_16x16x128_f8f6f4 v[144:147], v[8:15], v[172:179], v[144:147]
	v_mfma_f32_16x16x128_f8f6f4 v[132:135], v[0:7], v[180:187], v[132:135]
	v_mfma_f32_16x16x128_f8f6f4 v[128:131], v[8:15], v[180:187], v[128:131]
	v_mfma_f32_16x16x128_f8f6f4 v[116:119], v[0:7], v[188:195], v[116:119]
	v_mfma_f32_16x16x128_f8f6f4 v[112:115], v[8:15], v[188:195], v[112:115]
	v_mfma_f32_16x16x128_f8f6f4 v[100:103], v[0:7], v[196:203], v[100:103]
	v_mfma_f32_16x16x128_f8f6f4 v[96:99], v[8:15], v[196:203], v[96:99]
	s_setprio 0
	s_barrier
	ds_read_b128 v[172:175], v170 offset:16384
	ds_read_b128 v[176:179], v170 offset:17408
	ds_read_b128 v[180:183], v170 offset:18432
	ds_read_b128 v[184:187], v170 offset:19456
	ds_read_b128 v[188:191], v170 offset:20480
	ds_read_b128 v[192:195], v170 offset:21504
	ds_read_b128 v[196:199], v170 offset:22528
	ds_read_b128 v[200:203], v170 offset:23552
	s_mov_b32 s22, m0
	s_mov_b32 m0, s31
	s_nop 2
	global_load_lds_dwordx4 v163, s[36:37]
	s_mov_b32 m0, s22
	s_nop 0
	s_mov_b32 s22, m0
	s_mov_b32 m0, s44
	s_nop 2
	global_load_lds_dwordx4 v165, s[36:37]
	s_mov_b32 m0, s22
	s_add_u32 s22, s36, 0x20000
	s_addc_u32 s23, s37, 0
	s_mov_b32 s33, m0
	s_mov_b32 m0, s45
	s_nop 2
	global_load_lds_dwordx4 v163, s[22:23]
	s_mov_b32 m0, s33
	s_nop 0
	s_mov_b32 s33, m0
	s_mov_b32 m0, s46
	s_nop 2
	global_load_lds_dwordx4 v165, s[22:23]
	s_mov_b32 m0, s33
	s_mov_b32 s22, m0
	s_mov_b32 m0, s21
	s_nop 2
	global_load_lds_dwordx4 v162, s[42:43]
	s_mov_b32 m0, s22
	s_nop 0
	s_mov_b32 s22, m0
	s_mov_b32 m0, s47
	s_nop 2
	global_load_lds_dwordx4 v164, s[42:43]
	s_mov_b32 m0, s22
	s_waitcnt vmcnt(8)
	s_waitcnt lgkmcnt(0)
	s_barrier
	s_setprio 1
	v_mfma_f32_16x16x128_f8f6f4 v[92:95], v[16:23], v[172:179], v[92:95]
	v_mfma_f32_16x16x128_f8f6f4 v[88:91], v[24:31], v[172:179], v[88:91]
	v_mfma_f32_16x16x128_f8f6f4 v[76:79], v[16:23], v[180:187], v[76:79]
	v_mfma_f32_16x16x128_f8f6f4 v[72:75], v[24:31], v[180:187], v[72:75]
	v_mfma_f32_16x16x128_f8f6f4 v[60:63], v[16:23], v[188:195], v[60:63]
	v_mfma_f32_16x16x128_f8f6f4 v[56:59], v[24:31], v[188:195], v[56:59]
	v_mfma_f32_16x16x128_f8f6f4 v[44:47], v[16:23], v[196:203], v[44:47]
	v_mfma_f32_16x16x128_f8f6f4 v[40:43], v[24:31], v[196:203], v[40:43]
	s_setprio 0
	s_setprio 1
	v_mfma_f32_16x16x128_f8f6f4 v[84:87], v[0:7], v[172:179], v[84:87]
	v_mfma_f32_16x16x128_f8f6f4 v[80:83], v[8:15], v[172:179], v[80:83]
	v_mfma_f32_16x16x128_f8f6f4 v[68:71], v[0:7], v[180:187], v[68:71]
	v_mfma_f32_16x16x128_f8f6f4 v[64:67], v[8:15], v[180:187], v[64:67]
	v_mfma_f32_16x16x128_f8f6f4 v[52:55], v[0:7], v[188:195], v[52:55]
	v_mfma_f32_16x16x128_f8f6f4 v[48:51], v[8:15], v[188:195], v[48:51]
	v_mfma_f32_16x16x128_f8f6f4 v[36:39], v[0:7], v[196:203], v[36:39]
	v_mfma_f32_16x16x128_f8f6f4 v[32:35], v[8:15], v[196:203], v[32:35]
	s_setprio 0
	s_barrier
	v_add_u32_e32 v12, 0x18000, v169
	v_add_u32_e32 v28, 0x1c000, v169
	ds_read_b128 v[0:3], v12
	ds_read_b128 v[4:7], v12 offset:1024
	ds_read_b128 v[8:11], v12 offset:2048
	ds_read_b128 v[12:15], v12 offset:3072
	ds_read_b128 v[16:19], v28
	ds_read_b128 v[20:23], v28 offset:1024
	ds_read_b128 v[24:27], v28 offset:2048
	ds_read_b128 v[28:31], v28 offset:3072
	ds_read_b128 v[172:175], v170 offset:32768
	ds_read_b128 v[176:179], v170 offset:33792
	ds_read_b128 v[180:183], v170 offset:34816
	ds_read_b128 v[184:187], v170 offset:35840
	ds_read_b128 v[188:191], v170 offset:36864
	ds_read_b128 v[192:195], v170 offset:37888
	ds_read_b128 v[196:199], v170 offset:38912
	ds_read_b128 v[200:203], v170 offset:39936
	s_add_u32 s22, s42, 0x20000
	s_addc_u32 s23, s43, 0
	s_mov_b32 s33, m0
	s_mov_b32 m0, s48
	s_nop 2
	global_load_lds_dwordx4 v162, s[22:23]
	s_mov_b32 m0, s33
	s_nop 0
	s_mov_b32 s33, m0
	s_mov_b32 m0, s49
	s_nop 2
	global_load_lds_dwordx4 v164, s[22:23]
	s_mov_b32 m0, s33
	s_waitcnt vmcnt(8)
	s_waitcnt lgkmcnt(0)
	s_barrier
	s_setprio 1
	v_mfma_f32_16x16x128_f8f6f4 v[156:159], v[0:7], v[172:179], v[156:159]
	v_mfma_f32_16x16x128_f8f6f4 v[152:155], v[8:15], v[172:179], v[152:155]
	v_mfma_f32_16x16x128_f8f6f4 v[140:143], v[0:7], v[180:187], v[140:143]
	v_mfma_f32_16x16x128_f8f6f4 v[136:139], v[8:15], v[180:187], v[136:139]
	v_mfma_f32_16x16x128_f8f6f4 v[124:127], v[0:7], v[188:195], v[124:127]
	v_mfma_f32_16x16x128_f8f6f4 v[120:123], v[8:15], v[188:195], v[120:123]
	v_mfma_f32_16x16x128_f8f6f4 v[108:111], v[0:7], v[196:203], v[108:111]
	v_mfma_f32_16x16x128_f8f6f4 v[104:107], v[8:15], v[196:203], v[104:107]
	s_setprio 0
	s_setprio 1
	v_mfma_f32_16x16x128_f8f6f4 v[148:151], v[16:23], v[172:179], v[148:151]
	v_mfma_f32_16x16x128_f8f6f4 v[144:147], v[24:31], v[172:179], v[144:147]
	v_mfma_f32_16x16x128_f8f6f4 v[132:135], v[16:23], v[180:187], v[132:135]
	v_mfma_f32_16x16x128_f8f6f4 v[128:131], v[24:31], v[180:187], v[128:131]
	v_mfma_f32_16x16x128_f8f6f4 v[116:119], v[16:23], v[188:195], v[116:119]
	v_mfma_f32_16x16x128_f8f6f4 v[112:115], v[24:31], v[188:195], v[112:115]
	v_mfma_f32_16x16x128_f8f6f4 v[100:103], v[16:23], v[196:203], v[100:103]
	v_mfma_f32_16x16x128_f8f6f4 v[96:99], v[24:31], v[196:203], v[96:99]
	s_setprio 0
	s_barrier
	ds_read_b128 v[172:175], v170 offset:49152
	ds_read_b128 v[176:179], v170 offset:50176
	ds_read_b128 v[180:183], v170 offset:51200
	ds_read_b128 v[184:187], v170 offset:52224
	ds_read_b128 v[188:191], v170 offset:53248
	ds_read_b128 v[192:195], v170 offset:54272
	ds_read_b128 v[196:199], v170 offset:55296
	ds_read_b128 v[200:203], v170 offset:56320
	s_mov_b32 s22, m0
	s_mov_b32 m0, s58
	s_nop 2
	global_load_lds_dwordx4 v163, s[40:41]
	s_mov_b32 m0, s22
	s_nop 0
	s_mov_b32 s22, m0
	s_mov_b32 m0, s59
	s_nop 2
	global_load_lds_dwordx4 v165, s[40:41]
	s_mov_b32 m0, s22
	s_add_u32 s22, s36, 0x20080
	s_addc_u32 s23, s37, 0
	s_mov_b32 s33, m0
	s_mov_b32 m0, s62
	s_nop 2
	global_load_lds_dwordx4 v163, s[22:23]
	s_mov_b32 m0, s33
	s_nop 0
	s_mov_b32 s33, m0
	s_mov_b32 m0, s63
	s_nop 2
	global_load_lds_dwordx4 v165, s[22:23]
	s_mov_b32 m0, s33
	s_mov_b32 s22, m0
	s_mov_b32 m0, s60
	s_nop 2
	global_load_lds_dwordx4 v162, s[38:39]
	s_mov_b32 m0, s22
	s_nop 0
	s_mov_b32 s22, m0
	s_mov_b32 m0, s61
	s_nop 2
	global_load_lds_dwordx4 v164, s[38:39]
	s_mov_b32 m0, s22
	s_waitcnt vmcnt(8)
	s_waitcnt lgkmcnt(0)
	s_barrier
	s_setprio 1
	v_mfma_f32_16x16x128_f8f6f4 v[92:95], v[0:7], v[172:179], v[92:95]
	v_mfma_f32_16x16x128_f8f6f4 v[88:91], v[8:15], v[172:179], v[88:91]
	v_mfma_f32_16x16x128_f8f6f4 v[76:79], v[0:7], v[180:187], v[76:79]
	v_mfma_f32_16x16x128_f8f6f4 v[72:75], v[8:15], v[180:187], v[72:75]
	v_mfma_f32_16x16x128_f8f6f4 v[60:63], v[0:7], v[188:195], v[60:63]
	v_mfma_f32_16x16x128_f8f6f4 v[56:59], v[8:15], v[188:195], v[56:59]
	v_mfma_f32_16x16x128_f8f6f4 v[44:47], v[0:7], v[196:203], v[44:47]
	v_mfma_f32_16x16x128_f8f6f4 v[40:43], v[8:15], v[196:203], v[40:43]
	s_setprio 0
	s_setprio 1
	v_mfma_f32_16x16x128_f8f6f4 v[84:87], v[16:23], v[172:179], v[84:87]
	v_mfma_f32_16x16x128_f8f6f4 v[80:83], v[24:31], v[172:179], v[80:83]
	v_mfma_f32_16x16x128_f8f6f4 v[68:71], v[16:23], v[180:187], v[68:71]
	v_mfma_f32_16x16x128_f8f6f4 v[64:67], v[24:31], v[180:187], v[64:67]
	v_mfma_f32_16x16x128_f8f6f4 v[52:55], v[16:23], v[188:195], v[52:55]
	v_mfma_f32_16x16x128_f8f6f4 v[48:51], v[24:31], v[188:195], v[48:51]
	v_mfma_f32_16x16x128_f8f6f4 v[36:39], v[16:23], v[196:203], v[36:39]
	v_mfma_f32_16x16x128_f8f6f4 v[32:35], v[24:31], v[196:203], v[32:35]
	s_setprio 0
	s_barrier
	s_add_i32 s83, s83, 2
	s_add_u32 s81, s81, 0x100
	s_addc_u32 s82, s82, 0
	s_cmp_gt_u32 s83, 5
	s_cbranch_scc1 .LBB0_2130
	s_mov_b64 s[22:23], s[26:27]
	s_cmp_lg_u32 s83, -2
	s_cbranch_scc0 .LBB0_2121
	s_branch .LBB0_2128
